# speedup vs baseline: 1.1141x; 1.1001x over previous
.Lscan_loop_a_st:
	ds_read_b64 v[128:129], v106 offset:96
	ds_read_b64 v[130:131], v106 offset:104
	ds_read_b64 v[132:133], v106 offset:112
	s_waitcnt vmcnt(8)
	global_load_dwordx4 v[146:149], v[196:197], off
	global_load_dwordx4 v[150:153], v[196:197], off offset:512
	global_load_dwordx4 v[154:157], v[196:197], off offset:1024
	v_lshl_add_u64 v[196:197], v[196:197], 0, s[42:43]
	s_waitcnt lgkmcnt(3)
	v_mfma_f32_16x16x128_f8f6f4 v[134:137], v[122:127], v[2:7], 0 cbsz:2 blgp:2
	v_mfma_f32_16x16x128_f8f6f4 v[138:141], v[122:127], v[14:19], 0 cbsz:2 blgp:2
	v_mfma_f32_16x16x128_f8f6f4 v[142:145], v[122:127], v[26:31], v[188:191] cbsz:2 blgp:2
	v_mfma_f32_16x16x128_f8f6f4 v[204:207], v[122:127], v[38:43], 0 cbsz:2 blgp:2
	v_mfma_f32_16x16x128_f8f6f4 v[208:211], v[122:127], v[50:55], 0 cbsz:2 blgp:2
	v_mfma_f32_16x16x128_f8f6f4 v[212:215], v[122:127], v[62:67], v[188:191] cbsz:2 blgp:2
	s_waitcnt lgkmcnt(0)
	v_mfma_f32_16x16x128_f8f6f4 v[134:137], v[128:133], v[8:13], v[134:137] cbsz:2 blgp:2
	v_mfma_f32_16x16x128_f8f6f4 v[204:207], v[128:133], v[44:49], v[204:207] cbsz:2 blgp:2
	v_mfma_f32_16x16x128_f8f6f4 v[138:141], v[128:133], v[20:25], v[138:141] cbsz:2 blgp:2
	v_mfma_f32_16x16x128_f8f6f4 v[208:211], v[128:133], v[56:61], v[208:211] cbsz:2 blgp:2
	v_mfma_f32_16x16x128_f8f6f4 v[142:145], v[128:133], v[32:37], v[142:145] cbsz:2 blgp:2
	v_mfma_f32_16x16x128_f8f6f4 v[212:215], v[128:133], v[68:73], v[212:215] cbsz:2 blgp:2
	v_cndmask_b32_e64 v158, v134, v204, s[4:5]
	v_fma_mix_f32 v158, v158, v1, v82 op_sel_hi:[0,0,1]
	v_exp_f32_e32 v158, v158
	v_cndmask_b32_e64 v159, v138, v208, s[4:5]
	v_fma_mix_f32 v159, v159, v99, v74 op_sel_hi:[0,0,1]
	v_exp_f32_e32 v159, v159
	v_fma_f32 v158, v158, v186, v186
	v_rcp_f32_e32 v158, v158
	v_add_f32_e32 v159, 1.0, v159
	v_rcp_f32_e32 v159, v159
	v_cndmask_b32_e64 v160, v142, v212, s[4:5]
	v_fma_mix_f32 v161, v158, v160, v78 op_sel_hi:[0,0,1]
	v_exp_f32_e32 v161, v161
	s_add_u32 s48, s48, s40
	v_add_f32_e32 v161, 1.0, v161
	v_rcp_f32_e32 v161, v161
	s_addc_u32 s49, s49, s41
	v_fma_f32 v162, v161, -2.0, 1.0
	v_sub_f32_e32 v163, v176, v162
	v_fma_f32 v176, v159, v163, v162
	v_fma_f32 v164, |v176|, s16, v117
	v_fma_f32 v165, |v176|, s17, v118
	v_fma_f32 v166, |v176|, s18, v119
	v_lshrrev_b32_e32 v167, 26, v176
	v_min3_u32 v164, v164, v165, v166
	v_bfi_b32 v168, 31, v164, v167
	v_lshrrev_b32_e32 v169, v181, v168
	global_store_short_d16_hi v185, v176, s[48:49]
	v_mul_u32_u24_dpp v170, v168, v180 quad_perm:[1,2,3,3] row_mask:0xf bank_mask:0xf bound_ctrl:1
	v_or_b32_e32 v171, v169, v170
	ds_write_b8 v184, v171 offset:416
	s_waitcnt lgkmcnt(0)
	s_barrier
	ds_read_b64 v[122:123], v106 offset:416
	ds_read_b64 v[124:125], v106 offset:424
	ds_read_b64 v[126:127], v106 offset:432
	s_barrier
	ds_read_b64 v[128:129], v106 offset:512
	ds_read_b64 v[130:131], v106 offset:520
	ds_read_b64 v[132:133], v106 offset:528
	s_waitcnt lgkmcnt(3)
	v_mfma_f32_16x16x128_f8f6f4 v[134:137], v[122:127], v[2:7], 0 cbsz:2 blgp:2
	v_mfma_f32_16x16x128_f8f6f4 v[138:141], v[122:127], v[14:19], 0 cbsz:2 blgp:2
	v_mfma_f32_16x16x128_f8f6f4 v[142:145], v[122:127], v[26:31], v[188:191] cbsz:2 blgp:2
	v_mfma_f32_16x16x128_f8f6f4 v[204:207], v[122:127], v[38:43], 0 cbsz:2 blgp:2
	v_mfma_f32_16x16x128_f8f6f4 v[208:211], v[122:127], v[50:55], 0 cbsz:2 blgp:2
	v_mfma_f32_16x16x128_f8f6f4 v[212:215], v[122:127], v[62:67], v[188:191] cbsz:2 blgp:2
	s_waitcnt lgkmcnt(0)
	v_mfma_f32_16x16x128_f8f6f4 v[134:137], v[128:133], v[8:13], v[134:137] cbsz:2 blgp:2
	v_mfma_f32_16x16x128_f8f6f4 v[204:207], v[128:133], v[44:49], v[204:207] cbsz:2 blgp:2
	v_mfma_f32_16x16x128_f8f6f4 v[138:141], v[128:133], v[20:25], v[138:141] cbsz:2 blgp:2
	v_mfma_f32_16x16x128_f8f6f4 v[208:211], v[128:133], v[56:61], v[208:211] cbsz:2 blgp:2
	v_mfma_f32_16x16x128_f8f6f4 v[142:145], v[128:133], v[32:37], v[142:145] cbsz:2 blgp:2
	v_mfma_f32_16x16x128_f8f6f4 v[212:215], v[128:133], v[68:73], v[212:215] cbsz:2 blgp:2
	v_cndmask_b32_e64 v158, v134, v204, s[4:5]
	v_fma_mix_f32 v158, v158, v1, v82 op_sel:[0,0,1] op_sel_hi:[0,0,1]
	v_exp_f32_e32 v158, v158
	v_cndmask_b32_e64 v159, v138, v208, s[4:5]
	v_fma_mix_f32 v159, v159, v99, v74 op_sel:[0,0,1] op_sel_hi:[0,0,1]
	v_exp_f32_e32 v159, v159
	v_fma_f32 v158, v158, v186, v186
	v_rcp_f32_e32 v158, v158
	v_add_f32_e32 v159, 1.0, v159
	v_rcp_f32_e32 v159, v159
	v_cndmask_b32_e64 v160, v142, v212, s[4:5]
	v_fma_mix_f32 v161, v158, v160, v78 op_sel:[0,0,1] op_sel_hi:[0,0,1]
	v_exp_f32_e32 v161, v161
	s_add_u32 s48, s48, s40
	v_add_f32_e32 v161, 1.0, v161
	v_rcp_f32_e32 v161, v161
	s_addc_u32 s49, s49, s41
	v_fma_f32 v162, v161, -2.0, 1.0
	v_sub_f32_e32 v163, v176, v162
	v_fma_f32 v176, v159, v163, v162
	v_fma_f32 v164, |v176|, s16, v117
	v_fma_f32 v165, |v176|, s17, v118
	v_fma_f32 v166, |v176|, s18, v119
	v_lshrrev_b32_e32 v167, 26, v176
	v_min3_u32 v164, v164, v165, v166
	v_bfi_b32 v168, 31, v164, v167
	v_lshrrev_b32_e32 v169, v181, v168
	global_store_short_d16_hi v185, v176, s[48:49]
	v_mul_u32_u24_dpp v170, v168, v180 quad_perm:[1,2,3,3] row_mask:0xf bank_mask:0xf bound_ctrl:1
	v_or_b32_e32 v171, v169, v170
	ds_write_b8 v184, v171
	s_waitcnt lgkmcnt(0)
	s_barrier
	ds_read_b64 v[122:123], v106 offset:0
	ds_read_b64 v[124:125], v106 offset:8
	ds_read_b64 v[126:127], v106 offset:16
	s_barrier
	ds_read_b64 v[128:129], v106 offset:96
	ds_read_b64 v[130:131], v106 offset:104
	ds_read_b64 v[132:133], v106 offset:112
	s_waitcnt lgkmcnt(3)
	v_mfma_f32_16x16x128_f8f6f4 v[134:137], v[122:127], v[2:7], 0 cbsz:2 blgp:2
	v_mfma_f32_16x16x128_f8f6f4 v[138:141], v[122:127], v[14:19], 0 cbsz:2 blgp:2
	v_mfma_f32_16x16x128_f8f6f4 v[142:145], v[122:127], v[26:31], v[188:191] cbsz:2 blgp:2
	v_mfma_f32_16x16x128_f8f6f4 v[204:207], v[122:127], v[38:43], 0 cbsz:2 blgp:2
	v_mfma_f32_16x16x128_f8f6f4 v[208:211], v[122:127], v[50:55], 0 cbsz:2 blgp:2
	v_mfma_f32_16x16x128_f8f6f4 v[212:215], v[122:127], v[62:67], v[188:191] cbsz:2 blgp:2
	s_waitcnt lgkmcnt(0)
	v_mfma_f32_16x16x128_f8f6f4 v[134:137], v[128:133], v[8:13], v[134:137] cbsz:2 blgp:2
	v_mfma_f32_16x16x128_f8f6f4 v[204:207], v[128:133], v[44:49], v[204:207] cbsz:2 blgp:2
	v_mfma_f32_16x16x128_f8f6f4 v[138:141], v[128:133], v[20:25], v[138:141] cbsz:2 blgp:2
	v_mfma_f32_16x16x128_f8f6f4 v[208:211], v[128:133], v[56:61], v[208:211] cbsz:2 blgp:2
	v_mfma_f32_16x16x128_f8f6f4 v[142:145], v[128:133], v[32:37], v[142:145] cbsz:2 blgp:2
	v_mfma_f32_16x16x128_f8f6f4 v[212:215], v[128:133], v[68:73], v[212:215] cbsz:2 blgp:2
	v_cndmask_b32_e64 v158, v134, v204, s[4:5]
	v_fma_mix_f32 v158, v158, v1, v83 op_sel_hi:[0,0,1]
	v_exp_f32_e32 v158, v158
	v_cndmask_b32_e64 v159, v138, v208, s[4:5]
	v_fma_mix_f32 v159, v159, v99, v75 op_sel_hi:[0,0,1]
	v_exp_f32_e32 v159, v159
	v_fma_f32 v158, v158, v186, v186
	v_rcp_f32_e32 v158, v158
	v_add_f32_e32 v159, 1.0, v159
	v_rcp_f32_e32 v159, v159
	v_cndmask_b32_e64 v160, v142, v212, s[4:5]
	v_fma_mix_f32 v161, v158, v160, v79 op_sel_hi:[0,0,1]
	v_exp_f32_e32 v161, v161
	s_add_u32 s48, s48, s40
	v_add_f32_e32 v161, 1.0, v161
	v_rcp_f32_e32 v161, v161
	s_addc_u32 s49, s49, s41
	v_fma_f32 v162, v161, -2.0, 1.0
	v_sub_f32_e32 v163, v176, v162
	v_fma_f32 v176, v159, v163, v162
	v_fma_f32 v164, |v176|, s16, v117
	v_fma_f32 v165, |v176|, s17, v118
	v_fma_f32 v166, |v176|, s18, v119
	v_lshrrev_b32_e32 v167, 26, v176
	v_min3_u32 v164, v164, v165, v166
	v_bfi_b32 v168, 31, v164, v167
	v_lshrrev_b32_e32 v169, v181, v168
	global_store_short_d16_hi v185, v176, s[48:49]
	v_mul_u32_u24_dpp v170, v168, v180 quad_perm:[1,2,3,3] row_mask:0xf bank_mask:0xf bound_ctrl:1
	v_or_b32_e32 v171, v169, v170
	ds_write_b8 v184, v171 offset:416
	s_waitcnt lgkmcnt(0)
	s_barrier
	ds_read_b64 v[122:123], v106 offset:416
	ds_read_b64 v[124:125], v106 offset:424
	ds_read_b64 v[126:127], v106 offset:432
	s_barrier
	ds_read_b64 v[128:129], v106 offset:512
	ds_read_b64 v[130:131], v106 offset:520
	ds_read_b64 v[132:133], v106 offset:528
	s_waitcnt lgkmcnt(3)
	v_mfma_f32_16x16x128_f8f6f4 v[134:137], v[122:127], v[2:7], 0 cbsz:2 blgp:2
	v_mfma_f32_16x16x128_f8f6f4 v[138:141], v[122:127], v[14:19], 0 cbsz:2 blgp:2
	v_mfma_f32_16x16x128_f8f6f4 v[142:145], v[122:127], v[26:31], v[188:191] cbsz:2 blgp:2
	v_mfma_f32_16x16x128_f8f6f4 v[204:207], v[122:127], v[38:43], 0 cbsz:2 blgp:2
	v_mfma_f32_16x16x128_f8f6f4 v[208:211], v[122:127], v[50:55], 0 cbsz:2 blgp:2
	v_mfma_f32_16x16x128_f8f6f4 v[212:215], v[122:127], v[62:67], v[188:191] cbsz:2 blgp:2
	s_waitcnt lgkmcnt(0)
	v_mfma_f32_16x16x128_f8f6f4 v[134:137], v[128:133], v[8:13], v[134:137] cbsz:2 blgp:2
	v_mfma_f32_16x16x128_f8f6f4 v[204:207], v[128:133], v[44:49], v[204:207] cbsz:2 blgp:2
	v_mfma_f32_16x16x128_f8f6f4 v[138:141], v[128:133], v[20:25], v[138:141] cbsz:2 blgp:2
	v_mfma_f32_16x16x128_f8f6f4 v[208:211], v[128:133], v[56:61], v[208:211] cbsz:2 blgp:2
	v_mfma_f32_16x16x128_f8f6f4 v[142:145], v[128:133], v[32:37], v[142:145] cbsz:2 blgp:2
	v_mfma_f32_16x16x128_f8f6f4 v[212:215], v[128:133], v[68:73], v[212:215] cbsz:2 blgp:2
	v_cndmask_b32_e64 v158, v134, v204, s[4:5]
	v_fma_mix_f32 v158, v158, v1, v83 op_sel:[0,0,1] op_sel_hi:[0,0,1]
	v_exp_f32_e32 v158, v158
	v_cndmask_b32_e64 v159, v138, v208, s[4:5]
	v_fma_mix_f32 v159, v159, v99, v75 op_sel:[0,0,1] op_sel_hi:[0,0,1]
	v_exp_f32_e32 v159, v159
	v_fma_f32 v158, v158, v186, v186
	v_rcp_f32_e32 v158, v158
	v_add_f32_e32 v159, 1.0, v159
	v_rcp_f32_e32 v159, v159
	v_cndmask_b32_e64 v160, v142, v212, s[4:5]
	v_fma_mix_f32 v161, v158, v160, v79 op_sel:[0,0,1] op_sel_hi:[0,0,1]
	v_exp_f32_e32 v161, v161
	s_add_u32 s48, s48, s40
	v_add_f32_e32 v161, 1.0, v161
	v_rcp_f32_e32 v161, v161
	s_addc_u32 s49, s49, s41
	v_fma_f32 v162, v161, -2.0, 1.0
	v_sub_f32_e32 v163, v176, v162
	v_fma_f32 v176, v159, v163, v162
	v_fma_f32 v164, |v176|, s16, v117
	v_fma_f32 v165, |v176|, s17, v118
	v_fma_f32 v166, |v176|, s18, v119
	v_lshrrev_b32_e32 v167, 26, v176
	v_min3_u32 v164, v164, v165, v166
	v_bfi_b32 v168, 31, v164, v167
	v_lshrrev_b32_e32 v169, v181, v168
	global_store_short_d16_hi v185, v176, s[48:49]
	v_mul_u32_u24_dpp v170, v168, v180 quad_perm:[1,2,3,3] row_mask:0xf bank_mask:0xf bound_ctrl:1
	v_or_b32_e32 v171, v169, v170
	ds_write_b8 v184, v171
	s_waitcnt lgkmcnt(0)
	s_barrier
	ds_read_b64 v[122:123], v106 offset:0
	ds_read_b64 v[124:125], v106 offset:8
	ds_read_b64 v[126:127], v106 offset:16
	s_barrier
	ds_read_b64 v[128:129], v106 offset:96
	ds_read_b64 v[130:131], v106 offset:104
	ds_read_b64 v[132:133], v106 offset:112
	s_waitcnt lgkmcnt(3)
	v_mfma_f32_16x16x128_f8f6f4 v[134:137], v[122:127], v[2:7], 0 cbsz:2 blgp:2
	v_mfma_f32_16x16x128_f8f6f4 v[138:141], v[122:127], v[14:19], 0 cbsz:2 blgp:2
	v_mfma_f32_16x16x128_f8f6f4 v[142:145], v[122:127], v[26:31], v[188:191] cbsz:2 blgp:2
	v_mfma_f32_16x16x128_f8f6f4 v[204:207], v[122:127], v[38:43], 0 cbsz:2 blgp:2
	v_mfma_f32_16x16x128_f8f6f4 v[208:211], v[122:127], v[50:55], 0 cbsz:2 blgp:2
	v_mfma_f32_16x16x128_f8f6f4 v[212:215], v[122:127], v[62:67], v[188:191] cbsz:2 blgp:2
	s_waitcnt lgkmcnt(0)
	v_mfma_f32_16x16x128_f8f6f4 v[134:137], v[128:133], v[8:13], v[134:137] cbsz:2 blgp:2
	v_mfma_f32_16x16x128_f8f6f4 v[204:207], v[128:133], v[44:49], v[204:207] cbsz:2 blgp:2
	v_mfma_f32_16x16x128_f8f6f4 v[138:141], v[128:133], v[20:25], v[138:141] cbsz:2 blgp:2
	v_mfma_f32_16x16x128_f8f6f4 v[208:211], v[128:133], v[56:61], v[208:211] cbsz:2 blgp:2
	v_mfma_f32_16x16x128_f8f6f4 v[142:145], v[128:133], v[32:37], v[142:145] cbsz:2 blgp:2
	v_mfma_f32_16x16x128_f8f6f4 v[212:215], v[128:133], v[68:73], v[212:215] cbsz:2 blgp:2
	v_cndmask_b32_e64 v158, v134, v204, s[4:5]
	v_fma_mix_f32 v158, v158, v1, v84 op_sel_hi:[0,0,1]
	v_exp_f32_e32 v158, v158
	v_cndmask_b32_e64 v159, v138, v208, s[4:5]
	v_fma_mix_f32 v159, v159, v99, v76 op_sel_hi:[0,0,1]
	v_exp_f32_e32 v159, v159
	v_fma_f32 v158, v158, v186, v186
	v_rcp_f32_e32 v158, v158
	v_add_f32_e32 v159, 1.0, v159
	v_rcp_f32_e32 v159, v159
	v_cndmask_b32_e64 v160, v142, v212, s[4:5]
	v_fma_mix_f32 v161, v158, v160, v80 op_sel_hi:[0,0,1]
	v_exp_f32_e32 v161, v161
	s_add_u32 s48, s48, s40
	v_add_f32_e32 v161, 1.0, v161
	v_rcp_f32_e32 v161, v161
	s_addc_u32 s49, s49, s41
	v_fma_f32 v162, v161, -2.0, 1.0
	v_sub_f32_e32 v163, v176, v162
	v_fma_f32 v176, v159, v163, v162
	v_fma_f32 v164, |v176|, s16, v117
	v_fma_f32 v165, |v176|, s17, v118
	v_fma_f32 v166, |v176|, s18, v119
	v_lshrrev_b32_e32 v167, 26, v176
	v_min3_u32 v164, v164, v165, v166
	v_bfi_b32 v168, 31, v164, v167
	v_lshrrev_b32_e32 v169, v181, v168
	global_store_short_d16_hi v185, v176, s[48:49]
	v_mul_u32_u24_dpp v170, v168, v180 quad_perm:[1,2,3,3] row_mask:0xf bank_mask:0xf bound_ctrl:1
	v_or_b32_e32 v171, v169, v170
	ds_write_b8 v184, v171 offset:416
	s_waitcnt lgkmcnt(0)
	s_barrier
	ds_read_b64 v[122:123], v106 offset:416
	ds_read_b64 v[124:125], v106 offset:424
	ds_read_b64 v[126:127], v106 offset:432
	s_barrier
	ds_read_b64 v[128:129], v106 offset:512
	ds_read_b64 v[130:131], v106 offset:520
	ds_read_b64 v[132:133], v106 offset:528
	s_waitcnt lgkmcnt(3)
	v_mfma_f32_16x16x128_f8f6f4 v[134:137], v[122:127], v[2:7], 0 cbsz:2 blgp:2
	v_mfma_f32_16x16x128_f8f6f4 v[138:141], v[122:127], v[14:19], 0 cbsz:2 blgp:2
	v_mfma_f32_16x16x128_f8f6f4 v[142:145], v[122:127], v[26:31], v[188:191] cbsz:2 blgp:2
	v_mfma_f32_16x16x128_f8f6f4 v[204:207], v[122:127], v[38:43], 0 cbsz:2 blgp:2
	v_mfma_f32_16x16x128_f8f6f4 v[208:211], v[122:127], v[50:55], 0 cbsz:2 blgp:2
	v_mfma_f32_16x16x128_f8f6f4 v[212:215], v[122:127], v[62:67], v[188:191] cbsz:2 blgp:2
	s_waitcnt lgkmcnt(0)
	v_mfma_f32_16x16x128_f8f6f4 v[134:137], v[128:133], v[8:13], v[134:137] cbsz:2 blgp:2
	v_mfma_f32_16x16x128_f8f6f4 v[204:207], v[128:133], v[44:49], v[204:207] cbsz:2 blgp:2
	v_mfma_f32_16x16x128_f8f6f4 v[138:141], v[128:133], v[20:25], v[138:141] cbsz:2 blgp:2
	v_mfma_f32_16x16x128_f8f6f4 v[208:211], v[128:133], v[56:61], v[208:211] cbsz:2 blgp:2
	v_mfma_f32_16x16x128_f8f6f4 v[142:145], v[128:133], v[32:37], v[142:145] cbsz:2 blgp:2
	v_mfma_f32_16x16x128_f8f6f4 v[212:215], v[128:133], v[68:73], v[212:215] cbsz:2 blgp:2
	v_cndmask_b32_e64 v158, v134, v204, s[4:5]
	v_fma_mix_f32 v158, v158, v1, v84 op_sel:[0,0,1] op_sel_hi:[0,0,1]
	v_exp_f32_e32 v158, v158
	v_cndmask_b32_e64 v159, v138, v208, s[4:5]
	v_fma_mix_f32 v159, v159, v99, v76 op_sel:[0,0,1] op_sel_hi:[0,0,1]
	v_exp_f32_e32 v159, v159
	v_fma_f32 v158, v158, v186, v186
	v_rcp_f32_e32 v158, v158
	v_add_f32_e32 v159, 1.0, v159
	v_rcp_f32_e32 v159, v159
	v_cndmask_b32_e64 v160, v142, v212, s[4:5]
	v_fma_mix_f32 v161, v158, v160, v80 op_sel:[0,0,1] op_sel_hi:[0,0,1]
	v_exp_f32_e32 v161, v161
	s_add_u32 s48, s48, s40
	v_add_f32_e32 v161, 1.0, v161
	v_rcp_f32_e32 v161, v161
	s_addc_u32 s49, s49, s41
	v_fma_f32 v162, v161, -2.0, 1.0
	v_sub_f32_e32 v163, v176, v162
	v_fma_f32 v176, v159, v163, v162
	v_fma_f32 v164, |v176|, s16, v117
	v_fma_f32 v165, |v176|, s17, v118
	v_fma_f32 v166, |v176|, s18, v119
	v_lshrrev_b32_e32 v167, 26, v176
	v_min3_u32 v164, v164, v165, v166
	v_bfi_b32 v168, 31, v164, v167
	v_lshrrev_b32_e32 v169, v181, v168
	global_store_short_d16_hi v185, v176, s[48:49]
	v_mul_u32_u24_dpp v170, v168, v180 quad_perm:[1,2,3,3] row_mask:0xf bank_mask:0xf bound_ctrl:1
	v_or_b32_e32 v171, v169, v170
	ds_write_b8 v184, v171
	s_waitcnt lgkmcnt(0)
	s_barrier
	ds_read_b64 v[122:123], v106 offset:0
	ds_read_b64 v[124:125], v106 offset:8
	ds_read_b64 v[126:127], v106 offset:16
	s_barrier
	ds_read_b64 v[128:129], v106 offset:96
	ds_read_b64 v[130:131], v106 offset:104
	ds_read_b64 v[132:133], v106 offset:112
	s_waitcnt lgkmcnt(3)
	v_mfma_f32_16x16x128_f8f6f4 v[134:137], v[122:127], v[2:7], 0 cbsz:2 blgp:2
	v_mfma_f32_16x16x128_f8f6f4 v[138:141], v[122:127], v[14:19], 0 cbsz:2 blgp:2
	v_mfma_f32_16x16x128_f8f6f4 v[142:145], v[122:127], v[26:31], v[188:191] cbsz:2 blgp:2
	v_mfma_f32_16x16x128_f8f6f4 v[204:207], v[122:127], v[38:43], 0 cbsz:2 blgp:2
	v_mfma_f32_16x16x128_f8f6f4 v[208:211], v[122:127], v[50:55], 0 cbsz:2 blgp:2
	v_mfma_f32_16x16x128_f8f6f4 v[212:215], v[122:127], v[62:67], v[188:191] cbsz:2 blgp:2
	s_waitcnt lgkmcnt(0)
	v_mfma_f32_16x16x128_f8f6f4 v[134:137], v[128:133], v[8:13], v[134:137] cbsz:2 blgp:2
	v_mfma_f32_16x16x128_f8f6f4 v[204:207], v[128:133], v[44:49], v[204:207] cbsz:2 blgp:2
	v_mfma_f32_16x16x128_f8f6f4 v[138:141], v[128:133], v[20:25], v[138:141] cbsz:2 blgp:2
	v_mfma_f32_16x16x128_f8f6f4 v[208:211], v[128:133], v[56:61], v[208:211] cbsz:2 blgp:2
	v_mfma_f32_16x16x128_f8f6f4 v[142:145], v[128:133], v[32:37], v[142:145] cbsz:2 blgp:2
	v_mfma_f32_16x16x128_f8f6f4 v[212:215], v[128:133], v[68:73], v[212:215] cbsz:2 blgp:2
	v_cndmask_b32_e64 v158, v134, v204, s[4:5]
	v_fma_mix_f32 v158, v158, v1, v85 op_sel_hi:[0,0,1]
	v_exp_f32_e32 v158, v158
	v_cndmask_b32_e64 v159, v138, v208, s[4:5]
	v_fma_mix_f32 v159, v159, v99, v77 op_sel_hi:[0,0,1]
	v_exp_f32_e32 v159, v159
	v_fma_f32 v158, v158, v186, v186
	v_rcp_f32_e32 v158, v158
	v_add_f32_e32 v159, 1.0, v159
	v_rcp_f32_e32 v159, v159
	v_cndmask_b32_e64 v160, v142, v212, s[4:5]
	v_fma_mix_f32 v161, v158, v160, v81 op_sel_hi:[0,0,1]
	v_exp_f32_e32 v161, v161
	s_add_u32 s48, s48, s40
	v_add_f32_e32 v161, 1.0, v161
	v_rcp_f32_e32 v161, v161
	s_addc_u32 s49, s49, s41
	v_fma_f32 v162, v161, -2.0, 1.0
	v_sub_f32_e32 v163, v176, v162
	v_fma_f32 v176, v159, v163, v162
	v_fma_f32 v164, |v176|, s16, v117
	v_fma_f32 v165, |v176|, s17, v118
	v_fma_f32 v166, |v176|, s18, v119
	v_lshrrev_b32_e32 v167, 26, v176
	v_min3_u32 v164, v164, v165, v166
	v_bfi_b32 v168, 31, v164, v167
	v_lshrrev_b32_e32 v169, v181, v168
	global_store_short_d16_hi v185, v176, s[48:49]
	v_mul_u32_u24_dpp v170, v168, v180 quad_perm:[1,2,3,3] row_mask:0xf bank_mask:0xf bound_ctrl:1
	v_or_b32_e32 v171, v169, v170
	ds_write_b8 v184, v171 offset:416
	s_waitcnt lgkmcnt(0)
	s_barrier
	ds_read_b64 v[122:123], v106 offset:416
	ds_read_b64 v[124:125], v106 offset:424
	ds_read_b64 v[126:127], v106 offset:432
	s_barrier
	ds_read_b64 v[128:129], v106 offset:512
	ds_read_b64 v[130:131], v106 offset:520
	ds_read_b64 v[132:133], v106 offset:528
	s_waitcnt lgkmcnt(3)
	v_mfma_f32_16x16x128_f8f6f4 v[134:137], v[122:127], v[2:7], 0 cbsz:2 blgp:2
	v_mfma_f32_16x16x128_f8f6f4 v[138:141], v[122:127], v[14:19], 0 cbsz:2 blgp:2
	v_mfma_f32_16x16x128_f8f6f4 v[142:145], v[122:127], v[26:31], v[188:191] cbsz:2 blgp:2
	v_mfma_f32_16x16x128_f8f6f4 v[204:207], v[122:127], v[38:43], 0 cbsz:2 blgp:2
	v_mfma_f32_16x16x128_f8f6f4 v[208:211], v[122:127], v[50:55], 0 cbsz:2 blgp:2
	v_mfma_f32_16x16x128_f8f6f4 v[212:215], v[122:127], v[62:67], v[188:191] cbsz:2 blgp:2
	s_waitcnt lgkmcnt(0)
	v_mfma_f32_16x16x128_f8f6f4 v[134:137], v[128:133], v[8:13], v[134:137] cbsz:2 blgp:2
	v_mfma_f32_16x16x128_f8f6f4 v[204:207], v[128:133], v[44:49], v[204:207] cbsz:2 blgp:2
	v_mfma_f32_16x16x128_f8f6f4 v[138:141], v[128:133], v[20:25], v[138:141] cbsz:2 blgp:2
	v_mfma_f32_16x16x128_f8f6f4 v[208:211], v[128:133], v[56:61], v[208:211] cbsz:2 blgp:2
	v_mfma_f32_16x16x128_f8f6f4 v[142:145], v[128:133], v[32:37], v[142:145] cbsz:2 blgp:2
	v_mfma_f32_16x16x128_f8f6f4 v[212:215], v[128:133], v[68:73], v[212:215] cbsz:2 blgp:2
	v_cndmask_b32_e64 v158, v134, v204, s[4:5]
	v_fma_mix_f32 v158, v158, v1, v85 op_sel:[0,0,1] op_sel_hi:[0,0,1]
	v_exp_f32_e32 v158, v158
	v_cndmask_b32_e64 v159, v138, v208, s[4:5]
	v_fma_mix_f32 v159, v159, v99, v77 op_sel:[0,0,1] op_sel_hi:[0,0,1]
	v_exp_f32_e32 v159, v159
	v_fma_f32 v158, v158, v186, v186
	v_rcp_f32_e32 v158, v158
	v_add_f32_e32 v159, 1.0, v159
	v_rcp_f32_e32 v159, v159
	v_cndmask_b32_e64 v160, v142, v212, s[4:5]
	v_fma_mix_f32 v161, v158, v160, v81 op_sel:[0,0,1] op_sel_hi:[0,0,1]
	v_exp_f32_e32 v161, v161
	s_add_u32 s48, s48, s40
	v_add_f32_e32 v161, 1.0, v161
	v_rcp_f32_e32 v161, v161
	s_addc_u32 s49, s49, s41
	v_fma_f32 v162, v161, -2.0, 1.0
	v_sub_f32_e32 v163, v176, v162
	v_fma_f32 v176, v159, v163, v162
	v_fma_f32 v164, |v176|, s16, v117
	v_fma_f32 v165, |v176|, s17, v118
	v_fma_f32 v166, |v176|, s18, v119
	v_lshrrev_b32_e32 v167, 26, v176
	v_min3_u32 v164, v164, v165, v166
	v_bfi_b32 v168, 31, v164, v167
	v_lshrrev_b32_e32 v169, v181, v168
	global_store_short_d16_hi v185, v176, s[48:49]
	v_mul_u32_u24_dpp v170, v168, v180 quad_perm:[1,2,3,3] row_mask:0xf bank_mask:0xf bound_ctrl:1
	v_or_b32_e32 v171, v169, v170
	ds_write_b8 v184, v171
	s_waitcnt lgkmcnt(0)
	s_barrier
	ds_read_b64 v[122:123], v106 offset:0
	ds_read_b64 v[124:125], v106 offset:8
	ds_read_b64 v[126:127], v106 offset:16
	s_barrier
	ds_read_b64 v[128:129], v106 offset:96
	ds_read_b64 v[130:131], v106 offset:104
	ds_read_b64 v[132:133], v106 offset:112
	s_waitcnt vmcnt(8)
	global_load_dwordx4 v[82:85], v[196:197], off
	global_load_dwordx4 v[74:77], v[196:197], off offset:512
	global_load_dwordx4 v[78:81], v[196:197], off offset:1024
	v_lshl_add_u64 v[196:197], v[196:197], 0, s[42:43]
	s_waitcnt lgkmcnt(3)
	v_mfma_f32_16x16x128_f8f6f4 v[134:137], v[122:127], v[2:7], 0 cbsz:2 blgp:2
	v_mfma_f32_16x16x128_f8f6f4 v[138:141], v[122:127], v[14:19], 0 cbsz:2 blgp:2
	v_mfma_f32_16x16x128_f8f6f4 v[142:145], v[122:127], v[26:31], v[188:191] cbsz:2 blgp:2
	v_mfma_f32_16x16x128_f8f6f4 v[204:207], v[122:127], v[38:43], 0 cbsz:2 blgp:2
	v_mfma_f32_16x16x128_f8f6f4 v[208:211], v[122:127], v[50:55], 0 cbsz:2 blgp:2
	v_mfma_f32_16x16x128_f8f6f4 v[212:215], v[122:127], v[62:67], v[188:191] cbsz:2 blgp:2
	s_waitcnt lgkmcnt(0)
	v_mfma_f32_16x16x128_f8f6f4 v[134:137], v[128:133], v[8:13], v[134:137] cbsz:2 blgp:2
	v_mfma_f32_16x16x128_f8f6f4 v[204:207], v[128:133], v[44:49], v[204:207] cbsz:2 blgp:2
	v_mfma_f32_16x16x128_f8f6f4 v[138:141], v[128:133], v[20:25], v[138:141] cbsz:2 blgp:2
	v_mfma_f32_16x16x128_f8f6f4 v[208:211], v[128:133], v[56:61], v[208:211] cbsz:2 blgp:2
	v_mfma_f32_16x16x128_f8f6f4 v[142:145], v[128:133], v[32:37], v[142:145] cbsz:2 blgp:2
	v_mfma_f32_16x16x128_f8f6f4 v[212:215], v[128:133], v[68:73], v[212:215] cbsz:2 blgp:2
	v_cndmask_b32_e64 v158, v134, v204, s[4:5]
	v_fma_mix_f32 v158, v158, v1, v146 op_sel_hi:[0,0,1]
	v_exp_f32_e32 v158, v158
	v_cndmask_b32_e64 v159, v138, v208, s[4:5]
	v_fma_mix_f32 v159, v159, v99, v150 op_sel_hi:[0,0,1]
	v_exp_f32_e32 v159, v159
	v_fma_f32 v158, v158, v186, v186
	v_rcp_f32_e32 v158, v158
	v_add_f32_e32 v159, 1.0, v159
	v_rcp_f32_e32 v159, v159
	v_cndmask_b32_e64 v160, v142, v212, s[4:5]
	v_fma_mix_f32 v161, v158, v160, v154 op_sel_hi:[0,0,1]
	v_exp_f32_e32 v161, v161
	s_add_u32 s48, s48, s40
	v_add_f32_e32 v161, 1.0, v161
	v_rcp_f32_e32 v161, v161
	s_addc_u32 s49, s49, s41
	v_fma_f32 v162, v161, -2.0, 1.0
	v_sub_f32_e32 v163, v176, v162
	v_fma_f32 v176, v159, v163, v162
	v_fma_f32 v164, |v176|, s16, v117
	v_fma_f32 v165, |v176|, s17, v118
	v_fma_f32 v166, |v176|, s18, v119
	v_lshrrev_b32_e32 v167, 26, v176
	v_min3_u32 v164, v164, v165, v166
	v_bfi_b32 v168, 31, v164, v167
	v_lshrrev_b32_e32 v169, v181, v168
	global_store_short_d16_hi v185, v176, s[48:49]
	v_mul_u32_u24_dpp v170, v168, v180 quad_perm:[1,2,3,3] row_mask:0xf bank_mask:0xf bound_ctrl:1
	v_or_b32_e32 v171, v169, v170
	ds_write_b8 v184, v171 offset:416
	s_waitcnt lgkmcnt(0)
	s_barrier
	ds_read_b64 v[122:123], v106 offset:416
	ds_read_b64 v[124:125], v106 offset:424
	ds_read_b64 v[126:127], v106 offset:432
	s_barrier
	ds_read_b64 v[128:129], v106 offset:512
	ds_read_b64 v[130:131], v106 offset:520
	ds_read_b64 v[132:133], v106 offset:528
	s_waitcnt lgkmcnt(3)
	v_mfma_f32_16x16x128_f8f6f4 v[134:137], v[122:127], v[2:7], 0 cbsz:2 blgp:2
	v_mfma_f32_16x16x128_f8f6f4 v[138:141], v[122:127], v[14:19], 0 cbsz:2 blgp:2
	v_mfma_f32_16x16x128_f8f6f4 v[142:145], v[122:127], v[26:31], v[188:191] cbsz:2 blgp:2
	v_mfma_f32_16x16x128_f8f6f4 v[204:207], v[122:127], v[38:43], 0 cbsz:2 blgp:2
	v_mfma_f32_16x16x128_f8f6f4 v[208:211], v[122:127], v[50:55], 0 cbsz:2 blgp:2
	v_mfma_f32_16x16x128_f8f6f4 v[212:215], v[122:127], v[62:67], v[188:191] cbsz:2 blgp:2
	s_waitcnt lgkmcnt(0)
	v_mfma_f32_16x16x128_f8f6f4 v[134:137], v[128:133], v[8:13], v[134:137] cbsz:2 blgp:2
	v_mfma_f32_16x16x128_f8f6f4 v[204:207], v[128:133], v[44:49], v[204:207] cbsz:2 blgp:2
	v_mfma_f32_16x16x128_f8f6f4 v[138:141], v[128:133], v[20:25], v[138:141] cbsz:2 blgp:2
	v_mfma_f32_16x16x128_f8f6f4 v[208:211], v[128:133], v[56:61], v[208:211] cbsz:2 blgp:2
	v_mfma_f32_16x16x128_f8f6f4 v[142:145], v[128:133], v[32:37], v[142:145] cbsz:2 blgp:2
	v_mfma_f32_16x16x128_f8f6f4 v[212:215], v[128:133], v[68:73], v[212:215] cbsz:2 blgp:2
	v_cndmask_b32_e64 v158, v134, v204, s[4:5]
	v_fma_mix_f32 v158, v158, v1, v146 op_sel:[0,0,1] op_sel_hi:[0,0,1]
	v_exp_f32_e32 v158, v158
	v_cndmask_b32_e64 v159, v138, v208, s[4:5]
	v_fma_mix_f32 v159, v159, v99, v150 op_sel:[0,0,1] op_sel_hi:[0,0,1]
	v_exp_f32_e32 v159, v159
	v_fma_f32 v158, v158, v186, v186
	v_rcp_f32_e32 v158, v158
	v_add_f32_e32 v159, 1.0, v159
	v_rcp_f32_e32 v159, v159
	v_cndmask_b32_e64 v160, v142, v212, s[4:5]
	v_fma_mix_f32 v161, v158, v160, v154 op_sel:[0,0,1] op_sel_hi:[0,0,1]
	v_exp_f32_e32 v161, v161
	s_add_u32 s48, s48, s40
	v_add_f32_e32 v161, 1.0, v161
	v_rcp_f32_e32 v161, v161
	s_addc_u32 s49, s49, s41
	v_fma_f32 v162, v161, -2.0, 1.0
	v_sub_f32_e32 v163, v176, v162
	v_fma_f32 v176, v159, v163, v162
	v_fma_f32 v164, |v176|, s16, v117
	v_fma_f32 v165, |v176|, s17, v118
	v_fma_f32 v166, |v176|, s18, v119
	v_lshrrev_b32_e32 v167, 26, v176
	v_min3_u32 v164, v164, v165, v166
	v_bfi_b32 v168, 31, v164, v167
	v_lshrrev_b32_e32 v169, v181, v168
	global_store_short_d16_hi v185, v176, s[48:49]
	v_mul_u32_u24_dpp v170, v168, v180 quad_perm:[1,2,3,3] row_mask:0xf bank_mask:0xf bound_ctrl:1
	v_or_b32_e32 v171, v169, v170
	ds_write_b8 v184, v171
	s_waitcnt lgkmcnt(0)
	s_barrier
	ds_read_b64 v[122:123], v106 offset:0
	ds_read_b64 v[124:125], v106 offset:8
	ds_read_b64 v[126:127], v106 offset:16
	s_barrier
	ds_read_b64 v[128:129], v106 offset:96
	ds_read_b64 v[130:131], v106 offset:104
	ds_read_b64 v[132:133], v106 offset:112
	s_waitcnt lgkmcnt(3)
	v_mfma_f32_16x16x128_f8f6f4 v[134:137], v[122:127], v[2:7], 0 cbsz:2 blgp:2
	v_mfma_f32_16x16x128_f8f6f4 v[138:141], v[122:127], v[14:19], 0 cbsz:2 blgp:2
	v_mfma_f32_16x16x128_f8f6f4 v[142:145], v[122:127], v[26:31], v[188:191] cbsz:2 blgp:2
	v_mfma_f32_16x16x128_f8f6f4 v[204:207], v[122:127], v[38:43], 0 cbsz:2 blgp:2
	v_mfma_f32_16x16x128_f8f6f4 v[208:211], v[122:127], v[50:55], 0 cbsz:2 blgp:2
	v_mfma_f32_16x16x128_f8f6f4 v[212:215], v[122:127], v[62:67], v[188:191] cbsz:2 blgp:2
	s_waitcnt lgkmcnt(0)
	v_mfma_f32_16x16x128_f8f6f4 v[134:137], v[128:133], v[8:13], v[134:137] cbsz:2 blgp:2
	v_mfma_f32_16x16x128_f8f6f4 v[204:207], v[128:133], v[44:49], v[204:207] cbsz:2 blgp:2
	v_mfma_f32_16x16x128_f8f6f4 v[138:141], v[128:133], v[20:25], v[138:141] cbsz:2 blgp:2
	v_mfma_f32_16x16x128_f8f6f4 v[208:211], v[128:133], v[56:61], v[208:211] cbsz:2 blgp:2
	v_mfma_f32_16x16x128_f8f6f4 v[142:145], v[128:133], v[32:37], v[142:145] cbsz:2 blgp:2
	v_mfma_f32_16x16x128_f8f6f4 v[212:215], v[128:133], v[68:73], v[212:215] cbsz:2 blgp:2
	v_cndmask_b32_e64 v158, v134, v204, s[4:5]
	v_fma_mix_f32 v158, v158, v1, v147 op_sel_hi:[0,0,1]
	v_exp_f32_e32 v158, v158
	v_cndmask_b32_e64 v159, v138, v208, s[4:5]
	v_fma_mix_f32 v159, v159, v99, v151 op_sel_hi:[0,0,1]
	v_exp_f32_e32 v159, v159
	v_fma_f32 v158, v158, v186, v186
	v_rcp_f32_e32 v158, v158
	v_add_f32_e32 v159, 1.0, v159
	v_rcp_f32_e32 v159, v159
	v_cndmask_b32_e64 v160, v142, v212, s[4:5]
	v_fma_mix_f32 v161, v158, v160, v155 op_sel_hi:[0,0,1]
	v_exp_f32_e32 v161, v161
	s_add_u32 s48, s48, s40
	v_add_f32_e32 v161, 1.0, v161
	v_rcp_f32_e32 v161, v161
	s_addc_u32 s49, s49, s41
	v_fma_f32 v162, v161, -2.0, 1.0
	v_sub_f32_e32 v163, v176, v162
	v_fma_f32 v176, v159, v163, v162
	v_fma_f32 v164, |v176|, s16, v117
	v_fma_f32 v165, |v176|, s17, v118
	v_fma_f32 v166, |v176|, s18, v119
	v_lshrrev_b32_e32 v167, 26, v176
	v_min3_u32 v164, v164, v165, v166
	v_bfi_b32 v168, 31, v164, v167
	v_lshrrev_b32_e32 v169, v181, v168
	global_store_short_d16_hi v185, v176, s[48:49]
	v_mul_u32_u24_dpp v170, v168, v180 quad_perm:[1,2,3,3] row_mask:0xf bank_mask:0xf bound_ctrl:1
	v_or_b32_e32 v171, v169, v170
	ds_write_b8 v184, v171 offset:416
	s_waitcnt lgkmcnt(0)
	s_barrier
	ds_read_b64 v[122:123], v106 offset:416
	ds_read_b64 v[124:125], v106 offset:424
	ds_read_b64 v[126:127], v106 offset:432
	s_barrier
	ds_read_b64 v[128:129], v106 offset:512
	ds_read_b64 v[130:131], v106 offset:520
	ds_read_b64 v[132:133], v106 offset:528
	s_waitcnt lgkmcnt(3)
	v_mfma_f32_16x16x128_f8f6f4 v[134:137], v[122:127], v[2:7], 0 cbsz:2 blgp:2
	v_mfma_f32_16x16x128_f8f6f4 v[138:141], v[122:127], v[14:19], 0 cbsz:2 blgp:2
	v_mfma_f32_16x16x128_f8f6f4 v[142:145], v[122:127], v[26:31], v[188:191] cbsz:2 blgp:2
	v_mfma_f32_16x16x128_f8f6f4 v[204:207], v[122:127], v[38:43], 0 cbsz:2 blgp:2
	v_mfma_f32_16x16x128_f8f6f4 v[208:211], v[122:127], v[50:55], 0 cbsz:2 blgp:2
	v_mfma_f32_16x16x128_f8f6f4 v[212:215], v[122:127], v[62:67], v[188:191] cbsz:2 blgp:2
	s_waitcnt lgkmcnt(0)
	v_mfma_f32_16x16x128_f8f6f4 v[134:137], v[128:133], v[8:13], v[134:137] cbsz:2 blgp:2
	v_mfma_f32_16x16x128_f8f6f4 v[204:207], v[128:133], v[44:49], v[204:207] cbsz:2 blgp:2
	v_mfma_f32_16x16x128_f8f6f4 v[138:141], v[128:133], v[20:25], v[138:141] cbsz:2 blgp:2
	v_mfma_f32_16x16x128_f8f6f4 v[208:211], v[128:133], v[56:61], v[208:211] cbsz:2 blgp:2
	v_mfma_f32_16x16x128_f8f6f4 v[142:145], v[128:133], v[32:37], v[142:145] cbsz:2 blgp:2
	v_mfma_f32_16x16x128_f8f6f4 v[212:215], v[128:133], v[68:73], v[212:215] cbsz:2 blgp:2
	v_cndmask_b32_e64 v158, v134, v204, s[4:5]
	v_fma_mix_f32 v158, v158, v1, v147 op_sel:[0,0,1] op_sel_hi:[0,0,1]
	v_exp_f32_e32 v158, v158
	v_cndmask_b32_e64 v159, v138, v208, s[4:5]
	v_fma_mix_f32 v159, v159, v99, v151 op_sel:[0,0,1] op_sel_hi:[0,0,1]
	v_exp_f32_e32 v159, v159
	v_fma_f32 v158, v158, v186, v186
	v_rcp_f32_e32 v158, v158
	v_add_f32_e32 v159, 1.0, v159
	v_rcp_f32_e32 v159, v159
	v_cndmask_b32_e64 v160, v142, v212, s[4:5]
	v_fma_mix_f32 v161, v158, v160, v155 op_sel:[0,0,1] op_sel_hi:[0,0,1]
	v_exp_f32_e32 v161, v161
	s_add_u32 s48, s48, s40
	v_add_f32_e32 v161, 1.0, v161
	v_rcp_f32_e32 v161, v161
	s_addc_u32 s49, s49, s41
	v_fma_f32 v162, v161, -2.0, 1.0
	v_sub_f32_e32 v163, v176, v162
	v_fma_f32 v176, v159, v163, v162
	v_fma_f32 v164, |v176|, s16, v117
	v_fma_f32 v165, |v176|, s17, v118
	v_fma_f32 v166, |v176|, s18, v119
	v_lshrrev_b32_e32 v167, 26, v176
	v_min3_u32 v164, v164, v165, v166
	v_bfi_b32 v168, 31, v164, v167
	v_lshrrev_b32_e32 v169, v181, v168
	global_store_short_d16_hi v185, v176, s[48:49]
	v_mul_u32_u24_dpp v170, v168, v180 quad_perm:[1,2,3,3] row_mask:0xf bank_mask:0xf bound_ctrl:1
	v_or_b32_e32 v171, v169, v170
	ds_write_b8 v184, v171
	s_waitcnt lgkmcnt(0)
	s_barrier
	ds_read_b64 v[122:123], v106 offset:0
	ds_read_b64 v[124:125], v106 offset:8
	ds_read_b64 v[126:127], v106 offset:16
	s_barrier
	ds_read_b64 v[128:129], v106 offset:96
	ds_read_b64 v[130:131], v106 offset:104
	ds_read_b64 v[132:133], v106 offset:112
	s_waitcnt lgkmcnt(3)
	v_mfma_f32_16x16x128_f8f6f4 v[134:137], v[122:127], v[2:7], 0 cbsz:2 blgp:2
	v_mfma_f32_16x16x128_f8f6f4 v[138:141], v[122:127], v[14:19], 0 cbsz:2 blgp:2
	v_mfma_f32_16x16x128_f8f6f4 v[142:145], v[122:127], v[26:31], v[188:191] cbsz:2 blgp:2
	v_mfma_f32_16x16x128_f8f6f4 v[204:207], v[122:127], v[38:43], 0 cbsz:2 blgp:2
	v_mfma_f32_16x16x128_f8f6f4 v[208:211], v[122:127], v[50:55], 0 cbsz:2 blgp:2
	v_mfma_f32_16x16x128_f8f6f4 v[212:215], v[122:127], v[62:67], v[188:191] cbsz:2 blgp:2
	s_waitcnt lgkmcnt(0)
	v_mfma_f32_16x16x128_f8f6f4 v[134:137], v[128:133], v[8:13], v[134:137] cbsz:2 blgp:2
	v_mfma_f32_16x16x128_f8f6f4 v[204:207], v[128:133], v[44:49], v[204:207] cbsz:2 blgp:2
	v_mfma_f32_16x16x128_f8f6f4 v[138:141], v[128:133], v[20:25], v[138:141] cbsz:2 blgp:2
	v_mfma_f32_16x16x128_f8f6f4 v[208:211], v[128:133], v[56:61], v[208:211] cbsz:2 blgp:2
	v_mfma_f32_16x16x128_f8f6f4 v[142:145], v[128:133], v[32:37], v[142:145] cbsz:2 blgp:2
	v_mfma_f32_16x16x128_f8f6f4 v[212:215], v[128:133], v[68:73], v[212:215] cbsz:2 blgp:2
	v_cndmask_b32_e64 v158, v134, v204, s[4:5]
	v_fma_mix_f32 v158, v158, v1, v148 op_sel_hi:[0,0,1]
	v_exp_f32_e32 v158, v158
	v_cndmask_b32_e64 v159, v138, v208, s[4:5]
	v_fma_mix_f32 v159, v159, v99, v152 op_sel_hi:[0,0,1]
	v_exp_f32_e32 v159, v159
	v_fma_f32 v158, v158, v186, v186
	v_rcp_f32_e32 v158, v158
	v_add_f32_e32 v159, 1.0, v159
	v_rcp_f32_e32 v159, v159
	v_cndmask_b32_e64 v160, v142, v212, s[4:5]
	v_fma_mix_f32 v161, v158, v160, v156 op_sel_hi:[0,0,1]
	v_exp_f32_e32 v161, v161
	s_add_u32 s48, s48, s40
	v_add_f32_e32 v161, 1.0, v161
	v_rcp_f32_e32 v161, v161
	s_addc_u32 s49, s49, s41
	v_fma_f32 v162, v161, -2.0, 1.0
	v_sub_f32_e32 v163, v176, v162
	v_fma_f32 v176, v159, v163, v162
	v_fma_f32 v164, |v176|, s16, v117
	v_fma_f32 v165, |v176|, s17, v118
	v_fma_f32 v166, |v176|, s18, v119
	v_lshrrev_b32_e32 v167, 26, v176
	v_min3_u32 v164, v164, v165, v166
	v_bfi_b32 v168, 31, v164, v167
	v_lshrrev_b32_e32 v169, v181, v168
	global_store_short_d16_hi v185, v176, s[48:49]
	v_mul_u32_u24_dpp v170, v168, v180 quad_perm:[1,2,3,3] row_mask:0xf bank_mask:0xf bound_ctrl:1
	v_or_b32_e32 v171, v169, v170
	ds_write_b8 v184, v171 offset:416
	s_waitcnt lgkmcnt(0)
	s_barrier
	ds_read_b64 v[122:123], v106 offset:416
	ds_read_b64 v[124:125], v106 offset:424
	ds_read_b64 v[126:127], v106 offset:432
	s_barrier
	ds_read_b64 v[128:129], v106 offset:512
	ds_read_b64 v[130:131], v106 offset:520
	ds_read_b64 v[132:133], v106 offset:528
	s_waitcnt lgkmcnt(3)
	v_mfma_f32_16x16x128_f8f6f4 v[134:137], v[122:127], v[2:7], 0 cbsz:2 blgp:2
	v_mfma_f32_16x16x128_f8f6f4 v[138:141], v[122:127], v[14:19], 0 cbsz:2 blgp:2
	v_mfma_f32_16x16x128_f8f6f4 v[142:145], v[122:127], v[26:31], v[188:191] cbsz:2 blgp:2
	v_mfma_f32_16x16x128_f8f6f4 v[204:207], v[122:127], v[38:43], 0 cbsz:2 blgp:2
	v_mfma_f32_16x16x128_f8f6f4 v[208:211], v[122:127], v[50:55], 0 cbsz:2 blgp:2
	v_mfma_f32_16x16x128_f8f6f4 v[212:215], v[122:127], v[62:67], v[188:191] cbsz:2 blgp:2
	s_waitcnt lgkmcnt(0)
	v_mfma_f32_16x16x128_f8f6f4 v[134:137], v[128:133], v[8:13], v[134:137] cbsz:2 blgp:2
	v_mfma_f32_16x16x128_f8f6f4 v[204:207], v[128:133], v[44:49], v[204:207] cbsz:2 blgp:2
	v_mfma_f32_16x16x128_f8f6f4 v[138:141], v[128:133], v[20:25], v[138:141] cbsz:2 blgp:2
	v_mfma_f32_16x16x128_f8f6f4 v[208:211], v[128:133], v[56:61], v[208:211] cbsz:2 blgp:2
	v_mfma_f32_16x16x128_f8f6f4 v[142:145], v[128:133], v[32:37], v[142:145] cbsz:2 blgp:2
	v_mfma_f32_16x16x128_f8f6f4 v[212:215], v[128:133], v[68:73], v[212:215] cbsz:2 blgp:2
	v_cndmask_b32_e64 v158, v134, v204, s[4:5]
	v_fma_mix_f32 v158, v158, v1, v148 op_sel:[0,0,1] op_sel_hi:[0,0,1]
	v_exp_f32_e32 v158, v158
	v_cndmask_b32_e64 v159, v138, v208, s[4:5]
	v_fma_mix_f32 v159, v159, v99, v152 op_sel:[0,0,1] op_sel_hi:[0,0,1]
	v_exp_f32_e32 v159, v159
	v_fma_f32 v158, v158, v186, v186
	v_rcp_f32_e32 v158, v158
	v_add_f32_e32 v159, 1.0, v159
	v_rcp_f32_e32 v159, v159
	v_cndmask_b32_e64 v160, v142, v212, s[4:5]
	v_fma_mix_f32 v161, v158, v160, v156 op_sel:[0,0,1] op_sel_hi:[0,0,1]
	v_exp_f32_e32 v161, v161
	s_add_u32 s48, s48, s40
	v_add_f32_e32 v161, 1.0, v161
	v_rcp_f32_e32 v161, v161
	s_addc_u32 s49, s49, s41
	v_fma_f32 v162, v161, -2.0, 1.0
	v_sub_f32_e32 v163, v176, v162
	v_fma_f32 v176, v159, v163, v162
	v_fma_f32 v164, |v176|, s16, v117
	v_fma_f32 v165, |v176|, s17, v118
	v_fma_f32 v166, |v176|, s18, v119
	v_lshrrev_b32_e32 v167, 26, v176
	v_min3_u32 v164, v164, v165, v166
	v_bfi_b32 v168, 31, v164, v167
	v_lshrrev_b32_e32 v169, v181, v168
	global_store_short_d16_hi v185, v176, s[48:49]
	v_mul_u32_u24_dpp v170, v168, v180 quad_perm:[1,2,3,3] row_mask:0xf bank_mask:0xf bound_ctrl:1
	v_or_b32_e32 v171, v169, v170
	ds_write_b8 v184, v171
	s_waitcnt lgkmcnt(0)
	s_barrier
	ds_read_b64 v[122:123], v106 offset:0
	ds_read_b64 v[124:125], v106 offset:8
	ds_read_b64 v[126:127], v106 offset:16
	s_barrier
	ds_read_b64 v[128:129], v106 offset:96
	ds_read_b64 v[130:131], v106 offset:104
	ds_read_b64 v[132:133], v106 offset:112
	s_waitcnt lgkmcnt(3)
	v_mfma_f32_16x16x128_f8f6f4 v[134:137], v[122:127], v[2:7], 0 cbsz:2 blgp:2
	v_mfma_f32_16x16x128_f8f6f4 v[138:141], v[122:127], v[14:19], 0 cbsz:2 blgp:2
	v_mfma_f32_16x16x128_f8f6f4 v[142:145], v[122:127], v[26:31], v[188:191] cbsz:2 blgp:2
	v_mfma_f32_16x16x128_f8f6f4 v[204:207], v[122:127], v[38:43], 0 cbsz:2 blgp:2
	v_mfma_f32_16x16x128_f8f6f4 v[208:211], v[122:127], v[50:55], 0 cbsz:2 blgp:2
	v_mfma_f32_16x16x128_f8f6f4 v[212:215], v[122:127], v[62:67], v[188:191] cbsz:2 blgp:2
	s_waitcnt lgkmcnt(0)
	v_mfma_f32_16x16x128_f8f6f4 v[134:137], v[128:133], v[8:13], v[134:137] cbsz:2 blgp:2
	v_mfma_f32_16x16x128_f8f6f4 v[204:207], v[128:133], v[44:49], v[204:207] cbsz:2 blgp:2
	v_mfma_f32_16x16x128_f8f6f4 v[138:141], v[128:133], v[20:25], v[138:141] cbsz:2 blgp:2
	v_mfma_f32_16x16x128_f8f6f4 v[208:211], v[128:133], v[56:61], v[208:211] cbsz:2 blgp:2
	v_mfma_f32_16x16x128_f8f6f4 v[142:145], v[128:133], v[32:37], v[142:145] cbsz:2 blgp:2
	v_mfma_f32_16x16x128_f8f6f4 v[212:215], v[128:133], v[68:73], v[212:215] cbsz:2 blgp:2
	v_cndmask_b32_e64 v158, v134, v204, s[4:5]
	v_fma_mix_f32 v158, v158, v1, v149 op_sel_hi:[0,0,1]
	v_exp_f32_e32 v158, v158
	v_cndmask_b32_e64 v159, v138, v208, s[4:5]
	v_fma_mix_f32 v159, v159, v99, v153 op_sel_hi:[0,0,1]
	v_exp_f32_e32 v159, v159
	v_fma_f32 v158, v158, v186, v186
	v_rcp_f32_e32 v158, v158
	v_add_f32_e32 v159, 1.0, v159
	v_rcp_f32_e32 v159, v159
	v_cndmask_b32_e64 v160, v142, v212, s[4:5]
	v_fma_mix_f32 v161, v158, v160, v157 op_sel_hi:[0,0,1]
	v_exp_f32_e32 v161, v161
	s_add_u32 s48, s48, s40
	v_add_f32_e32 v161, 1.0, v161
	v_rcp_f32_e32 v161, v161
	s_addc_u32 s49, s49, s41
	v_fma_f32 v162, v161, -2.0, 1.0
	v_sub_f32_e32 v163, v176, v162
	v_fma_f32 v176, v159, v163, v162
	v_fma_f32 v164, |v176|, s16, v117
	v_fma_f32 v165, |v176|, s17, v118
	v_fma_f32 v166, |v176|, s18, v119
	v_lshrrev_b32_e32 v167, 26, v176
	v_min3_u32 v164, v164, v165, v166
	v_bfi_b32 v168, 31, v164, v167
	v_lshrrev_b32_e32 v169, v181, v168
	global_store_short_d16_hi v185, v176, s[48:49]
	v_mul_u32_u24_dpp v170, v168, v180 quad_perm:[1,2,3,3] row_mask:0xf bank_mask:0xf bound_ctrl:1
	v_or_b32_e32 v171, v169, v170
	ds_write_b8 v184, v171 offset:416
	s_waitcnt lgkmcnt(0)
	s_barrier
	ds_read_b64 v[122:123], v106 offset:416
	ds_read_b64 v[124:125], v106 offset:424
	ds_read_b64 v[126:127], v106 offset:432
	s_barrier
	ds_read_b64 v[128:129], v106 offset:512
	ds_read_b64 v[130:131], v106 offset:520
	ds_read_b64 v[132:133], v106 offset:528
	s_add_i32 s44, s44, 16
	s_waitcnt lgkmcnt(3)
	v_mfma_f32_16x16x128_f8f6f4 v[134:137], v[122:127], v[2:7], 0 cbsz:2 blgp:2
	v_mfma_f32_16x16x128_f8f6f4 v[138:141], v[122:127], v[14:19], 0 cbsz:2 blgp:2
	v_mfma_f32_16x16x128_f8f6f4 v[142:145], v[122:127], v[26:31], v[188:191] cbsz:2 blgp:2
	v_mfma_f32_16x16x128_f8f6f4 v[204:207], v[122:127], v[38:43], 0 cbsz:2 blgp:2
	v_mfma_f32_16x16x128_f8f6f4 v[208:211], v[122:127], v[50:55], 0 cbsz:2 blgp:2
	v_mfma_f32_16x16x128_f8f6f4 v[212:215], v[122:127], v[62:67], v[188:191] cbsz:2 blgp:2
	s_waitcnt lgkmcnt(0)
	v_mfma_f32_16x16x128_f8f6f4 v[134:137], v[128:133], v[8:13], v[134:137] cbsz:2 blgp:2
	v_mfma_f32_16x16x128_f8f6f4 v[204:207], v[128:133], v[44:49], v[204:207] cbsz:2 blgp:2
	v_mfma_f32_16x16x128_f8f6f4 v[138:141], v[128:133], v[20:25], v[138:141] cbsz:2 blgp:2
	v_mfma_f32_16x16x128_f8f6f4 v[208:211], v[128:133], v[56:61], v[208:211] cbsz:2 blgp:2
	v_mfma_f32_16x16x128_f8f6f4 v[142:145], v[128:133], v[32:37], v[142:145] cbsz:2 blgp:2
	v_mfma_f32_16x16x128_f8f6f4 v[212:215], v[128:133], v[68:73], v[212:215] cbsz:2 blgp:2
	v_cndmask_b32_e64 v158, v134, v204, s[4:5]
	v_fma_mix_f32 v158, v158, v1, v149 op_sel:[0,0,1] op_sel_hi:[0,0,1]
	v_exp_f32_e32 v158, v158
	v_cndmask_b32_e64 v159, v138, v208, s[4:5]
	v_fma_mix_f32 v159, v159, v99, v153 op_sel:[0,0,1] op_sel_hi:[0,0,1]
	v_exp_f32_e32 v159, v159
	v_fma_f32 v158, v158, v186, v186
	v_rcp_f32_e32 v158, v158
	v_add_f32_e32 v159, 1.0, v159
	v_rcp_f32_e32 v159, v159
	v_cndmask_b32_e64 v160, v142, v212, s[4:5]
	v_fma_mix_f32 v161, v158, v160, v157 op_sel:[0,0,1] op_sel_hi:[0,0,1]
	v_exp_f32_e32 v161, v161
	s_add_u32 s48, s48, s40
	v_add_f32_e32 v161, 1.0, v161
	v_rcp_f32_e32 v161, v161
	s_addc_u32 s49, s49, s41
	v_fma_f32 v162, v161, -2.0, 1.0
	v_sub_f32_e32 v163, v176, v162
	v_fma_f32 v176, v159, v163, v162
	v_fma_f32 v164, |v176|, s16, v117
	v_fma_f32 v165, |v176|, s17, v118
	v_fma_f32 v166, |v176|, s18, v119
	v_lshrrev_b32_e32 v167, 26, v176
	v_min3_u32 v164, v164, v165, v166
	v_bfi_b32 v168, 31, v164, v167
	v_lshrrev_b32_e32 v169, v181, v168
	global_store_short_d16_hi v185, v176, s[48:49]
	v_mul_u32_u24_dpp v170, v168, v180 quad_perm:[1,2,3,3] row_mask:0xf bank_mask:0xf bound_ctrl:1
	v_or_b32_e32 v171, v169, v170
	ds_write_b8 v184, v171
	s_waitcnt lgkmcnt(0)
	s_barrier
	ds_read_b64 v[122:123], v106 offset:0
	ds_read_b64 v[124:125], v106 offset:8
	ds_read_b64 v[126:127], v106 offset:16
	s_cmp_lt_i32 s44, s45
	s_barrier
	s_cbranch_scc1 .Lscan_loop_a_st
	s_branch .Lscan_exit_st
.Lscan_loop_b_st:
	ds_read_b64 v[128:129], v106 offset:96
	ds_read_b64 v[130:131], v106 offset:104
	ds_read_b64 v[132:133], v106 offset:112
	s_waitcnt vmcnt(8)
	global_load_dwordx4 v[146:149], v[196:197], off
	global_load_dwordx4 v[150:153], v[196:197], off offset:512
	global_load_dwordx4 v[154:157], v[196:197], off offset:1024
	v_lshl_add_u64 v[196:197], v[196:197], 0, s[42:43]
	s_waitcnt lgkmcnt(3)
	v_mfma_f32_16x16x128_f8f6f4 v[134:137], v[122:127], v[2:7], 0 cbsz:2 blgp:2
	v_mfma_f32_16x16x128_f8f6f4 v[138:141], v[122:127], v[14:19], 0 cbsz:2 blgp:2
	v_mfma_f32_16x16x128_f8f6f4 v[142:145], v[122:127], v[26:31], v[188:191] cbsz:2 blgp:2
	v_mfma_f32_16x16x128_f8f6f4 v[204:207], v[122:127], v[38:43], 0 cbsz:2 blgp:2
	v_mfma_f32_16x16x128_f8f6f4 v[208:211], v[122:127], v[50:55], 0 cbsz:2 blgp:2
	v_mfma_f32_16x16x128_f8f6f4 v[212:215], v[122:127], v[62:67], v[188:191] cbsz:2 blgp:2
	s_waitcnt lgkmcnt(0)
	v_mfma_f32_16x16x128_f8f6f4 v[134:137], v[128:133], v[8:13], v[134:137] cbsz:2 blgp:2
	v_mfma_f32_16x16x128_f8f6f4 v[204:207], v[128:133], v[44:49], v[204:207] cbsz:2 blgp:2
	v_mfma_f32_16x16x128_f8f6f4 v[138:141], v[128:133], v[20:25], v[138:141] cbsz:2 blgp:2
	v_mfma_f32_16x16x128_f8f6f4 v[208:211], v[128:133], v[56:61], v[208:211] cbsz:2 blgp:2
	v_mfma_f32_16x16x128_f8f6f4 v[142:145], v[128:133], v[32:37], v[142:145] cbsz:2 blgp:2
	v_mfma_f32_16x16x128_f8f6f4 v[212:215], v[128:133], v[68:73], v[212:215] cbsz:2 blgp:2
	v_cndmask_b32_e64 v158, v134, v204, s[4:5]
	v_fma_mix_f32 v158, v158, v1, v82 op_sel_hi:[0,0,1]
	v_exp_f32_e32 v158, v158
	v_cndmask_b32_e64 v159, v138, v208, s[4:5]
	v_fma_mix_f32 v159, v159, v99, v74 op_sel_hi:[0,0,1]
	v_exp_f32_e32 v159, v159
	v_fma_f32 v158, v158, v186, v186
	v_rcp_f32_e32 v158, v158
	v_add_f32_e32 v159, 1.0, v159
	v_rcp_f32_e32 v159, v159
	v_cndmask_b32_e64 v160, v142, v212, s[4:5]
	v_fma_mix_f32 v161, v158, v160, v78 op_sel_hi:[0,0,1]
	v_exp_f32_e32 v161, v161
	s_add_u32 s48, s48, s40
	v_add_f32_e32 v161, 1.0, v161
	v_rcp_f32_e32 v161, v161
	s_addc_u32 s49, s49, s41
	v_fma_f32 v162, v161, -2.0, 1.0
	v_sub_f32_e32 v163, v176, v162
	v_fma_f32 v176, v159, v163, v162
	v_fma_f32 v164, |v176|, s16, v117
	v_fma_f32 v165, |v176|, s17, v118
	v_fma_f32 v166, |v176|, s18, v119
	v_lshrrev_b32_e32 v167, 26, v176
	v_min3_u32 v164, v164, v165, v166
	v_bfi_b32 v168, 31, v164, v167
	v_lshrrev_b32_e32 v169, v181, v168
	global_store_short_d16_hi v185, v176, s[48:49]
	v_mul_u32_u24_dpp v170, v168, v180 quad_perm:[1,2,3,3] row_mask:0xf bank_mask:0xf bound_ctrl:1
	v_or_b32_e32 v171, v169, v170
	ds_write_b8 v184, v171 offset:416
	s_barrier
	ds_read_b64 v[122:123], v106 offset:416
	ds_read_b64 v[124:125], v106 offset:424
	ds_read_b64 v[126:127], v106 offset:432
	s_waitcnt lgkmcnt(3)
	s_barrier
	ds_read_b64 v[128:129], v106 offset:512
	ds_read_b64 v[130:131], v106 offset:520
	ds_read_b64 v[132:133], v106 offset:528
	s_waitcnt lgkmcnt(3)
	v_mfma_f32_16x16x128_f8f6f4 v[134:137], v[122:127], v[2:7], 0 cbsz:2 blgp:2
	v_mfma_f32_16x16x128_f8f6f4 v[138:141], v[122:127], v[14:19], 0 cbsz:2 blgp:2
	v_mfma_f32_16x16x128_f8f6f4 v[142:145], v[122:127], v[26:31], v[188:191] cbsz:2 blgp:2
	v_mfma_f32_16x16x128_f8f6f4 v[204:207], v[122:127], v[38:43], 0 cbsz:2 blgp:2
	v_mfma_f32_16x16x128_f8f6f4 v[208:211], v[122:127], v[50:55], 0 cbsz:2 blgp:2
	v_mfma_f32_16x16x128_f8f6f4 v[212:215], v[122:127], v[62:67], v[188:191] cbsz:2 blgp:2
	s_waitcnt lgkmcnt(0)
	v_mfma_f32_16x16x128_f8f6f4 v[134:137], v[128:133], v[8:13], v[134:137] cbsz:2 blgp:2
	v_mfma_f32_16x16x128_f8f6f4 v[204:207], v[128:133], v[44:49], v[204:207] cbsz:2 blgp:2
	v_mfma_f32_16x16x128_f8f6f4 v[138:141], v[128:133], v[20:25], v[138:141] cbsz:2 blgp:2
	v_mfma_f32_16x16x128_f8f6f4 v[208:211], v[128:133], v[56:61], v[208:211] cbsz:2 blgp:2
	v_mfma_f32_16x16x128_f8f6f4 v[142:145], v[128:133], v[32:37], v[142:145] cbsz:2 blgp:2
	v_mfma_f32_16x16x128_f8f6f4 v[212:215], v[128:133], v[68:73], v[212:215] cbsz:2 blgp:2
	v_cndmask_b32_e64 v158, v134, v204, s[4:5]
	v_fma_mix_f32 v158, v158, v1, v82 op_sel:[0,0,1] op_sel_hi:[0,0,1]
	v_exp_f32_e32 v158, v158
	v_cndmask_b32_e64 v159, v138, v208, s[4:5]
	v_fma_mix_f32 v159, v159, v99, v74 op_sel:[0,0,1] op_sel_hi:[0,0,1]
	v_exp_f32_e32 v159, v159
	v_fma_f32 v158, v158, v186, v186
	v_rcp_f32_e32 v158, v158
	v_add_f32_e32 v159, 1.0, v159
	v_rcp_f32_e32 v159, v159
	v_cndmask_b32_e64 v160, v142, v212, s[4:5]
	v_fma_mix_f32 v161, v158, v160, v78 op_sel:[0,0,1] op_sel_hi:[0,0,1]
	v_exp_f32_e32 v161, v161
	s_add_u32 s48, s48, s40
	v_add_f32_e32 v161, 1.0, v161
	v_rcp_f32_e32 v161, v161
	s_addc_u32 s49, s49, s41
	v_fma_f32 v162, v161, -2.0, 1.0
	v_sub_f32_e32 v163, v176, v162
	v_fma_f32 v176, v159, v163, v162
	v_fma_f32 v164, |v176|, s16, v117
	v_fma_f32 v165, |v176|, s17, v118
	v_fma_f32 v166, |v176|, s18, v119
	v_lshrrev_b32_e32 v167, 26, v176
	v_min3_u32 v164, v164, v165, v166
	v_bfi_b32 v168, 31, v164, v167
	v_lshrrev_b32_e32 v169, v181, v168
	global_store_short_d16_hi v185, v176, s[48:49]
	v_mul_u32_u24_dpp v170, v168, v180 quad_perm:[1,2,3,3] row_mask:0xf bank_mask:0xf bound_ctrl:1
	v_or_b32_e32 v171, v169, v170
	ds_write_b8 v184, v171
	s_barrier
	ds_read_b64 v[122:123], v106 offset:0
	ds_read_b64 v[124:125], v106 offset:8
	ds_read_b64 v[126:127], v106 offset:16
	s_waitcnt lgkmcnt(3)
	s_barrier
	ds_read_b64 v[128:129], v106 offset:96
	ds_read_b64 v[130:131], v106 offset:104
	ds_read_b64 v[132:133], v106 offset:112
	s_waitcnt lgkmcnt(3)
	v_mfma_f32_16x16x128_f8f6f4 v[134:137], v[122:127], v[2:7], 0 cbsz:2 blgp:2
	v_mfma_f32_16x16x128_f8f6f4 v[138:141], v[122:127], v[14:19], 0 cbsz:2 blgp:2
	v_mfma_f32_16x16x128_f8f6f4 v[142:145], v[122:127], v[26:31], v[188:191] cbsz:2 blgp:2
	v_mfma_f32_16x16x128_f8f6f4 v[204:207], v[122:127], v[38:43], 0 cbsz:2 blgp:2
	v_mfma_f32_16x16x128_f8f6f4 v[208:211], v[122:127], v[50:55], 0 cbsz:2 blgp:2
	v_mfma_f32_16x16x128_f8f6f4 v[212:215], v[122:127], v[62:67], v[188:191] cbsz:2 blgp:2
	s_waitcnt lgkmcnt(0)
	v_mfma_f32_16x16x128_f8f6f4 v[134:137], v[128:133], v[8:13], v[134:137] cbsz:2 blgp:2
	v_mfma_f32_16x16x128_f8f6f4 v[204:207], v[128:133], v[44:49], v[204:207] cbsz:2 blgp:2
	v_mfma_f32_16x16x128_f8f6f4 v[138:141], v[128:133], v[20:25], v[138:141] cbsz:2 blgp:2
	v_mfma_f32_16x16x128_f8f6f4 v[208:211], v[128:133], v[56:61], v[208:211] cbsz:2 blgp:2
	v_mfma_f32_16x16x128_f8f6f4 v[142:145], v[128:133], v[32:37], v[142:145] cbsz:2 blgp:2
	v_mfma_f32_16x16x128_f8f6f4 v[212:215], v[128:133], v[68:73], v[212:215] cbsz:2 blgp:2
	v_cndmask_b32_e64 v158, v134, v204, s[4:5]
	v_fma_mix_f32 v158, v158, v1, v83 op_sel_hi:[0,0,1]
	v_exp_f32_e32 v158, v158
	v_cndmask_b32_e64 v159, v138, v208, s[4:5]
	v_fma_mix_f32 v159, v159, v99, v75 op_sel_hi:[0,0,1]
	v_exp_f32_e32 v159, v159
	v_fma_f32 v158, v158, v186, v186
	v_rcp_f32_e32 v158, v158
	v_add_f32_e32 v159, 1.0, v159
	v_rcp_f32_e32 v159, v159
	v_cndmask_b32_e64 v160, v142, v212, s[4:5]
	v_fma_mix_f32 v161, v158, v160, v79 op_sel_hi:[0,0,1]
	v_exp_f32_e32 v161, v161
	s_add_u32 s48, s48, s40
	v_add_f32_e32 v161, 1.0, v161
	v_rcp_f32_e32 v161, v161
	s_addc_u32 s49, s49, s41
	v_fma_f32 v162, v161, -2.0, 1.0
	v_sub_f32_e32 v163, v176, v162
	v_fma_f32 v176, v159, v163, v162
	v_fma_f32 v164, |v176|, s16, v117
	v_fma_f32 v165, |v176|, s17, v118
	v_fma_f32 v166, |v176|, s18, v119
	v_lshrrev_b32_e32 v167, 26, v176
	v_min3_u32 v164, v164, v165, v166
	v_bfi_b32 v168, 31, v164, v167
	v_lshrrev_b32_e32 v169, v181, v168
	global_store_short_d16_hi v185, v176, s[48:49]
	v_mul_u32_u24_dpp v170, v168, v180 quad_perm:[1,2,3,3] row_mask:0xf bank_mask:0xf bound_ctrl:1
	v_or_b32_e32 v171, v169, v170
	ds_write_b8 v184, v171 offset:416
	s_barrier
	ds_read_b64 v[122:123], v106 offset:416
	ds_read_b64 v[124:125], v106 offset:424
	ds_read_b64 v[126:127], v106 offset:432
	s_waitcnt lgkmcnt(3)
	s_barrier
	ds_read_b64 v[128:129], v106 offset:512
	ds_read_b64 v[130:131], v106 offset:520
	ds_read_b64 v[132:133], v106 offset:528
	s_waitcnt lgkmcnt(3)
	v_mfma_f32_16x16x128_f8f6f4 v[134:137], v[122:127], v[2:7], 0 cbsz:2 blgp:2
	v_mfma_f32_16x16x128_f8f6f4 v[138:141], v[122:127], v[14:19], 0 cbsz:2 blgp:2
	v_mfma_f32_16x16x128_f8f6f4 v[142:145], v[122:127], v[26:31], v[188:191] cbsz:2 blgp:2
	v_mfma_f32_16x16x128_f8f6f4 v[204:207], v[122:127], v[38:43], 0 cbsz:2 blgp:2
	v_mfma_f32_16x16x128_f8f6f4 v[208:211], v[122:127], v[50:55], 0 cbsz:2 blgp:2
	v_mfma_f32_16x16x128_f8f6f4 v[212:215], v[122:127], v[62:67], v[188:191] cbsz:2 blgp:2
	s_waitcnt lgkmcnt(0)
	v_mfma_f32_16x16x128_f8f6f4 v[134:137], v[128:133], v[8:13], v[134:137] cbsz:2 blgp:2
	v_mfma_f32_16x16x128_f8f6f4 v[204:207], v[128:133], v[44:49], v[204:207] cbsz:2 blgp:2
	v_mfma_f32_16x16x128_f8f6f4 v[138:141], v[128:133], v[20:25], v[138:141] cbsz:2 blgp:2
	v_mfma_f32_16x16x128_f8f6f4 v[208:211], v[128:133], v[56:61], v[208:211] cbsz:2 blgp:2
	v_mfma_f32_16x16x128_f8f6f4 v[142:145], v[128:133], v[32:37], v[142:145] cbsz:2 blgp:2
	v_mfma_f32_16x16x128_f8f6f4 v[212:215], v[128:133], v[68:73], v[212:215] cbsz:2 blgp:2
	v_cndmask_b32_e64 v158, v134, v204, s[4:5]
	v_fma_mix_f32 v158, v158, v1, v83 op_sel:[0,0,1] op_sel_hi:[0,0,1]
	v_exp_f32_e32 v158, v158
	v_cndmask_b32_e64 v159, v138, v208, s[4:5]
	v_fma_mix_f32 v159, v159, v99, v75 op_sel:[0,0,1] op_sel_hi:[0,0,1]
	v_exp_f32_e32 v159, v159
	v_fma_f32 v158, v158, v186, v186
	v_rcp_f32_e32 v158, v158
	v_add_f32_e32 v159, 1.0, v159
	v_rcp_f32_e32 v159, v159
	v_cndmask_b32_e64 v160, v142, v212, s[4:5]
	v_fma_mix_f32 v161, v158, v160, v79 op_sel:[0,0,1] op_sel_hi:[0,0,1]
	v_exp_f32_e32 v161, v161
	s_add_u32 s48, s48, s40
	v_add_f32_e32 v161, 1.0, v161
	v_rcp_f32_e32 v161, v161
	s_addc_u32 s49, s49, s41
	v_fma_f32 v162, v161, -2.0, 1.0
	v_sub_f32_e32 v163, v176, v162
	v_fma_f32 v176, v159, v163, v162
	v_fma_f32 v164, |v176|, s16, v117
	v_fma_f32 v165, |v176|, s17, v118
	v_fma_f32 v166, |v176|, s18, v119
	v_lshrrev_b32_e32 v167, 26, v176
	v_min3_u32 v164, v164, v165, v166
	v_bfi_b32 v168, 31, v164, v167
	v_lshrrev_b32_e32 v169, v181, v168
	global_store_short_d16_hi v185, v176, s[48:49]
	v_mul_u32_u24_dpp v170, v168, v180 quad_perm:[1,2,3,3] row_mask:0xf bank_mask:0xf bound_ctrl:1
	v_or_b32_e32 v171, v169, v170
	ds_write_b8 v184, v171
	s_barrier
	ds_read_b64 v[122:123], v106 offset:0
	ds_read_b64 v[124:125], v106 offset:8
	ds_read_b64 v[126:127], v106 offset:16
	s_waitcnt lgkmcnt(3)
	s_barrier
	ds_read_b64 v[128:129], v106 offset:96
	ds_read_b64 v[130:131], v106 offset:104
	ds_read_b64 v[132:133], v106 offset:112
	s_waitcnt lgkmcnt(3)
	v_mfma_f32_16x16x128_f8f6f4 v[134:137], v[122:127], v[2:7], 0 cbsz:2 blgp:2
	v_mfma_f32_16x16x128_f8f6f4 v[138:141], v[122:127], v[14:19], 0 cbsz:2 blgp:2
	v_mfma_f32_16x16x128_f8f6f4 v[142:145], v[122:127], v[26:31], v[188:191] cbsz:2 blgp:2
	v_mfma_f32_16x16x128_f8f6f4 v[204:207], v[122:127], v[38:43], 0 cbsz:2 blgp:2
	v_mfma_f32_16x16x128_f8f6f4 v[208:211], v[122:127], v[50:55], 0 cbsz:2 blgp:2
	v_mfma_f32_16x16x128_f8f6f4 v[212:215], v[122:127], v[62:67], v[188:191] cbsz:2 blgp:2
	s_waitcnt lgkmcnt(0)
	v_mfma_f32_16x16x128_f8f6f4 v[134:137], v[128:133], v[8:13], v[134:137] cbsz:2 blgp:2
	v_mfma_f32_16x16x128_f8f6f4 v[204:207], v[128:133], v[44:49], v[204:207] cbsz:2 blgp:2
	v_mfma_f32_16x16x128_f8f6f4 v[138:141], v[128:133], v[20:25], v[138:141] cbsz:2 blgp:2
	v_mfma_f32_16x16x128_f8f6f4 v[208:211], v[128:133], v[56:61], v[208:211] cbsz:2 blgp:2
	v_mfma_f32_16x16x128_f8f6f4 v[142:145], v[128:133], v[32:37], v[142:145] cbsz:2 blgp:2
	v_mfma_f32_16x16x128_f8f6f4 v[212:215], v[128:133], v[68:73], v[212:215] cbsz:2 blgp:2
	v_cndmask_b32_e64 v158, v134, v204, s[4:5]
	v_fma_mix_f32 v158, v158, v1, v84 op_sel_hi:[0,0,1]
	v_exp_f32_e32 v158, v158
	v_cndmask_b32_e64 v159, v138, v208, s[4:5]
	v_fma_mix_f32 v159, v159, v99, v76 op_sel_hi:[0,0,1]
	v_exp_f32_e32 v159, v159
	v_fma_f32 v158, v158, v186, v186
	v_rcp_f32_e32 v158, v158
	v_add_f32_e32 v159, 1.0, v159
	v_rcp_f32_e32 v159, v159
	v_cndmask_b32_e64 v160, v142, v212, s[4:5]
	v_fma_mix_f32 v161, v158, v160, v80 op_sel_hi:[0,0,1]
	v_exp_f32_e32 v161, v161
	s_add_u32 s48, s48, s40
	v_add_f32_e32 v161, 1.0, v161
	v_rcp_f32_e32 v161, v161
	s_addc_u32 s49, s49, s41
	v_fma_f32 v162, v161, -2.0, 1.0
	v_sub_f32_e32 v163, v176, v162
	v_fma_f32 v176, v159, v163, v162
	v_fma_f32 v164, |v176|, s16, v117
	v_fma_f32 v165, |v176|, s17, v118
	v_fma_f32 v166, |v176|, s18, v119
	v_lshrrev_b32_e32 v167, 26, v176
	v_min3_u32 v164, v164, v165, v166
	v_bfi_b32 v168, 31, v164, v167
	v_lshrrev_b32_e32 v169, v181, v168
	global_store_short_d16_hi v185, v176, s[48:49]
	v_mul_u32_u24_dpp v170, v168, v180 quad_perm:[1,2,3,3] row_mask:0xf bank_mask:0xf bound_ctrl:1
	v_or_b32_e32 v171, v169, v170
	ds_write_b8 v184, v171 offset:416
	s_barrier
	ds_read_b64 v[122:123], v106 offset:416
	ds_read_b64 v[124:125], v106 offset:424
	ds_read_b64 v[126:127], v106 offset:432
	s_waitcnt lgkmcnt(3)
	s_barrier
	ds_read_b64 v[128:129], v106 offset:512
	ds_read_b64 v[130:131], v106 offset:520
	ds_read_b64 v[132:133], v106 offset:528
	s_waitcnt lgkmcnt(3)
	v_mfma_f32_16x16x128_f8f6f4 v[134:137], v[122:127], v[2:7], 0 cbsz:2 blgp:2
	v_mfma_f32_16x16x128_f8f6f4 v[138:141], v[122:127], v[14:19], 0 cbsz:2 blgp:2
	v_mfma_f32_16x16x128_f8f6f4 v[142:145], v[122:127], v[26:31], v[188:191] cbsz:2 blgp:2
	v_mfma_f32_16x16x128_f8f6f4 v[204:207], v[122:127], v[38:43], 0 cbsz:2 blgp:2
	v_mfma_f32_16x16x128_f8f6f4 v[208:211], v[122:127], v[50:55], 0 cbsz:2 blgp:2
	v_mfma_f32_16x16x128_f8f6f4 v[212:215], v[122:127], v[62:67], v[188:191] cbsz:2 blgp:2
	s_waitcnt lgkmcnt(0)
	v_mfma_f32_16x16x128_f8f6f4 v[134:137], v[128:133], v[8:13], v[134:137] cbsz:2 blgp:2
	v_mfma_f32_16x16x128_f8f6f4 v[204:207], v[128:133], v[44:49], v[204:207] cbsz:2 blgp:2
	v_mfma_f32_16x16x128_f8f6f4 v[138:141], v[128:133], v[20:25], v[138:141] cbsz:2 blgp:2
	v_mfma_f32_16x16x128_f8f6f4 v[208:211], v[128:133], v[56:61], v[208:211] cbsz:2 blgp:2
	v_mfma_f32_16x16x128_f8f6f4 v[142:145], v[128:133], v[32:37], v[142:145] cbsz:2 blgp:2
	v_mfma_f32_16x16x128_f8f6f4 v[212:215], v[128:133], v[68:73], v[212:215] cbsz:2 blgp:2
	v_cndmask_b32_e64 v158, v134, v204, s[4:5]
	v_fma_mix_f32 v158, v158, v1, v84 op_sel:[0,0,1] op_sel_hi:[0,0,1]
	v_exp_f32_e32 v158, v158
	v_cndmask_b32_e64 v159, v138, v208, s[4:5]
	v_fma_mix_f32 v159, v159, v99, v76 op_sel:[0,0,1] op_sel_hi:[0,0,1]
	v_exp_f32_e32 v159, v159
	v_fma_f32 v158, v158, v186, v186
	v_rcp_f32_e32 v158, v158
	v_add_f32_e32 v159, 1.0, v159
	v_rcp_f32_e32 v159, v159
	v_cndmask_b32_e64 v160, v142, v212, s[4:5]
	v_fma_mix_f32 v161, v158, v160, v80 op_sel:[0,0,1] op_sel_hi:[0,0,1]
	v_exp_f32_e32 v161, v161
	s_add_u32 s48, s48, s40
	v_add_f32_e32 v161, 1.0, v161
	v_rcp_f32_e32 v161, v161
	s_addc_u32 s49, s49, s41
	v_fma_f32 v162, v161, -2.0, 1.0
	v_sub_f32_e32 v163, v176, v162
	v_fma_f32 v176, v159, v163, v162
	v_fma_f32 v164, |v176|, s16, v117
	v_fma_f32 v165, |v176|, s17, v118
	v_fma_f32 v166, |v176|, s18, v119
	v_lshrrev_b32_e32 v167, 26, v176
	v_min3_u32 v164, v164, v165, v166
	v_bfi_b32 v168, 31, v164, v167
	v_lshrrev_b32_e32 v169, v181, v168
	global_store_short_d16_hi v185, v176, s[48:49]
	v_mul_u32_u24_dpp v170, v168, v180 quad_perm:[1,2,3,3] row_mask:0xf bank_mask:0xf bound_ctrl:1
	v_or_b32_e32 v171, v169, v170
	ds_write_b8 v184, v171
	s_barrier
	ds_read_b64 v[122:123], v106 offset:0
	ds_read_b64 v[124:125], v106 offset:8
	ds_read_b64 v[126:127], v106 offset:16
	s_waitcnt lgkmcnt(3)
	s_barrier
	ds_read_b64 v[128:129], v106 offset:96
	ds_read_b64 v[130:131], v106 offset:104
	ds_read_b64 v[132:133], v106 offset:112
	s_waitcnt lgkmcnt(3)
	v_mfma_f32_16x16x128_f8f6f4 v[134:137], v[122:127], v[2:7], 0 cbsz:2 blgp:2
	v_mfma_f32_16x16x128_f8f6f4 v[138:141], v[122:127], v[14:19], 0 cbsz:2 blgp:2
	v_mfma_f32_16x16x128_f8f6f4 v[142:145], v[122:127], v[26:31], v[188:191] cbsz:2 blgp:2
	v_mfma_f32_16x16x128_f8f6f4 v[204:207], v[122:127], v[38:43], 0 cbsz:2 blgp:2
	v_mfma_f32_16x16x128_f8f6f4 v[208:211], v[122:127], v[50:55], 0 cbsz:2 blgp:2
	v_mfma_f32_16x16x128_f8f6f4 v[212:215], v[122:127], v[62:67], v[188:191] cbsz:2 blgp:2
	s_waitcnt lgkmcnt(0)
	v_mfma_f32_16x16x128_f8f6f4 v[134:137], v[128:133], v[8:13], v[134:137] cbsz:2 blgp:2
	v_mfma_f32_16x16x128_f8f6f4 v[204:207], v[128:133], v[44:49], v[204:207] cbsz:2 blgp:2
	v_mfma_f32_16x16x128_f8f6f4 v[138:141], v[128:133], v[20:25], v[138:141] cbsz:2 blgp:2
	v_mfma_f32_16x16x128_f8f6f4 v[208:211], v[128:133], v[56:61], v[208:211] cbsz:2 blgp:2
	v_mfma_f32_16x16x128_f8f6f4 v[142:145], v[128:133], v[32:37], v[142:145] cbsz:2 blgp:2
	v_mfma_f32_16x16x128_f8f6f4 v[212:215], v[128:133], v[68:73], v[212:215] cbsz:2 blgp:2
	v_cndmask_b32_e64 v158, v134, v204, s[4:5]
	v_fma_mix_f32 v158, v158, v1, v85 op_sel_hi:[0,0,1]
	v_exp_f32_e32 v158, v158
	v_cndmask_b32_e64 v159, v138, v208, s[4:5]
	v_fma_mix_f32 v159, v159, v99, v77 op_sel_hi:[0,0,1]
	v_exp_f32_e32 v159, v159
	v_fma_f32 v158, v158, v186, v186
	v_rcp_f32_e32 v158, v158
	v_add_f32_e32 v159, 1.0, v159
	v_rcp_f32_e32 v159, v159
	v_cndmask_b32_e64 v160, v142, v212, s[4:5]
	v_fma_mix_f32 v161, v158, v160, v81 op_sel_hi:[0,0,1]
	v_exp_f32_e32 v161, v161
	s_add_u32 s48, s48, s40
	v_add_f32_e32 v161, 1.0, v161
	v_rcp_f32_e32 v161, v161
	s_addc_u32 s49, s49, s41
	v_fma_f32 v162, v161, -2.0, 1.0
	v_sub_f32_e32 v163, v176, v162
	v_fma_f32 v176, v159, v163, v162
	v_fma_f32 v164, |v176|, s16, v117
	v_fma_f32 v165, |v176|, s17, v118
	v_fma_f32 v166, |v176|, s18, v119
	v_lshrrev_b32_e32 v167, 26, v176
	v_min3_u32 v164, v164, v165, v166
	v_bfi_b32 v168, 31, v164, v167
	v_lshrrev_b32_e32 v169, v181, v168
	global_store_short_d16_hi v185, v176, s[48:49]
	v_mul_u32_u24_dpp v170, v168, v180 quad_perm:[1,2,3,3] row_mask:0xf bank_mask:0xf bound_ctrl:1
	v_or_b32_e32 v171, v169, v170
	ds_write_b8 v184, v171 offset:416
	s_barrier
	ds_read_b64 v[122:123], v106 offset:416
	ds_read_b64 v[124:125], v106 offset:424
	ds_read_b64 v[126:127], v106 offset:432
	s_waitcnt lgkmcnt(3)
	s_barrier
	ds_read_b64 v[128:129], v106 offset:512
	ds_read_b64 v[130:131], v106 offset:520
	ds_read_b64 v[132:133], v106 offset:528
	s_waitcnt lgkmcnt(3)
	v_mfma_f32_16x16x128_f8f6f4 v[134:137], v[122:127], v[2:7], 0 cbsz:2 blgp:2
	v_mfma_f32_16x16x128_f8f6f4 v[138:141], v[122:127], v[14:19], 0 cbsz:2 blgp:2
	v_mfma_f32_16x16x128_f8f6f4 v[142:145], v[122:127], v[26:31], v[188:191] cbsz:2 blgp:2
	v_mfma_f32_16x16x128_f8f6f4 v[204:207], v[122:127], v[38:43], 0 cbsz:2 blgp:2
	v_mfma_f32_16x16x128_f8f6f4 v[208:211], v[122:127], v[50:55], 0 cbsz:2 blgp:2
	v_mfma_f32_16x16x128_f8f6f4 v[212:215], v[122:127], v[62:67], v[188:191] cbsz:2 blgp:2
	s_waitcnt lgkmcnt(0)
	v_mfma_f32_16x16x128_f8f6f4 v[134:137], v[128:133], v[8:13], v[134:137] cbsz:2 blgp:2
	v_mfma_f32_16x16x128_f8f6f4 v[204:207], v[128:133], v[44:49], v[204:207] cbsz:2 blgp:2
	v_mfma_f32_16x16x128_f8f6f4 v[138:141], v[128:133], v[20:25], v[138:141] cbsz:2 blgp:2
	v_mfma_f32_16x16x128_f8f6f4 v[208:211], v[128:133], v[56:61], v[208:211] cbsz:2 blgp:2
	v_mfma_f32_16x16x128_f8f6f4 v[142:145], v[128:133], v[32:37], v[142:145] cbsz:2 blgp:2
	v_mfma_f32_16x16x128_f8f6f4 v[212:215], v[128:133], v[68:73], v[212:215] cbsz:2 blgp:2
	v_cndmask_b32_e64 v158, v134, v204, s[4:5]
	v_fma_mix_f32 v158, v158, v1, v85 op_sel:[0,0,1] op_sel_hi:[0,0,1]
	v_exp_f32_e32 v158, v158
	v_cndmask_b32_e64 v159, v138, v208, s[4:5]
	v_fma_mix_f32 v159, v159, v99, v77 op_sel:[0,0,1] op_sel_hi:[0,0,1]
	v_exp_f32_e32 v159, v159
	v_fma_f32 v158, v158, v186, v186
	v_rcp_f32_e32 v158, v158
	v_add_f32_e32 v159, 1.0, v159
	v_rcp_f32_e32 v159, v159
	v_cndmask_b32_e64 v160, v142, v212, s[4:5]
	v_fma_mix_f32 v161, v158, v160, v81 op_sel:[0,0,1] op_sel_hi:[0,0,1]
	v_exp_f32_e32 v161, v161
	s_add_u32 s48, s48, s40
	v_add_f32_e32 v161, 1.0, v161
	v_rcp_f32_e32 v161, v161
	s_addc_u32 s49, s49, s41
	v_fma_f32 v162, v161, -2.0, 1.0
	v_sub_f32_e32 v163, v176, v162
	v_fma_f32 v176, v159, v163, v162
	v_fma_f32 v164, |v176|, s16, v117
	v_fma_f32 v165, |v176|, s17, v118
	v_fma_f32 v166, |v176|, s18, v119
	v_lshrrev_b32_e32 v167, 26, v176
	v_min3_u32 v164, v164, v165, v166
	v_bfi_b32 v168, 31, v164, v167
	v_lshrrev_b32_e32 v169, v181, v168
	global_store_short_d16_hi v185, v176, s[48:49]
	v_mul_u32_u24_dpp v170, v168, v180 quad_perm:[1,2,3,3] row_mask:0xf bank_mask:0xf bound_ctrl:1
	v_or_b32_e32 v171, v169, v170
	ds_write_b8 v184, v171
	s_barrier
	ds_read_b64 v[122:123], v106 offset:0
	ds_read_b64 v[124:125], v106 offset:8
	ds_read_b64 v[126:127], v106 offset:16
	s_waitcnt lgkmcnt(3)
	s_barrier
	ds_read_b64 v[128:129], v106 offset:96
	ds_read_b64 v[130:131], v106 offset:104
	ds_read_b64 v[132:133], v106 offset:112
	s_waitcnt vmcnt(8)
	global_load_dwordx4 v[82:85], v[196:197], off
	global_load_dwordx4 v[74:77], v[196:197], off offset:512
	global_load_dwordx4 v[78:81], v[196:197], off offset:1024
	v_lshl_add_u64 v[196:197], v[196:197], 0, s[42:43]
	s_waitcnt lgkmcnt(3)
	v_mfma_f32_16x16x128_f8f6f4 v[134:137], v[122:127], v[2:7], 0 cbsz:2 blgp:2
	v_mfma_f32_16x16x128_f8f6f4 v[138:141], v[122:127], v[14:19], 0 cbsz:2 blgp:2
	v_mfma_f32_16x16x128_f8f6f4 v[142:145], v[122:127], v[26:31], v[188:191] cbsz:2 blgp:2
	v_mfma_f32_16x16x128_f8f6f4 v[204:207], v[122:127], v[38:43], 0 cbsz:2 blgp:2
	v_mfma_f32_16x16x128_f8f6f4 v[208:211], v[122:127], v[50:55], 0 cbsz:2 blgp:2
	v_mfma_f32_16x16x128_f8f6f4 v[212:215], v[122:127], v[62:67], v[188:191] cbsz:2 blgp:2
	s_waitcnt lgkmcnt(0)
	v_mfma_f32_16x16x128_f8f6f4 v[134:137], v[128:133], v[8:13], v[134:137] cbsz:2 blgp:2
	v_mfma_f32_16x16x128_f8f6f4 v[204:207], v[128:133], v[44:49], v[204:207] cbsz:2 blgp:2
	v_mfma_f32_16x16x128_f8f6f4 v[138:141], v[128:133], v[20:25], v[138:141] cbsz:2 blgp:2
	v_mfma_f32_16x16x128_f8f6f4 v[208:211], v[128:133], v[56:61], v[208:211] cbsz:2 blgp:2
	v_mfma_f32_16x16x128_f8f6f4 v[142:145], v[128:133], v[32:37], v[142:145] cbsz:2 blgp:2
	v_mfma_f32_16x16x128_f8f6f4 v[212:215], v[128:133], v[68:73], v[212:215] cbsz:2 blgp:2
	v_cndmask_b32_e64 v158, v134, v204, s[4:5]
	v_fma_mix_f32 v158, v158, v1, v146 op_sel_hi:[0,0,1]
	v_exp_f32_e32 v158, v158
	v_cndmask_b32_e64 v159, v138, v208, s[4:5]
	v_fma_mix_f32 v159, v159, v99, v150 op_sel_hi:[0,0,1]
	v_exp_f32_e32 v159, v159
	v_fma_f32 v158, v158, v186, v186
	v_rcp_f32_e32 v158, v158
	v_add_f32_e32 v159, 1.0, v159
	v_rcp_f32_e32 v159, v159
	v_cndmask_b32_e64 v160, v142, v212, s[4:5]
	v_fma_mix_f32 v161, v158, v160, v154 op_sel_hi:[0,0,1]
	v_exp_f32_e32 v161, v161
	s_add_u32 s48, s48, s40
	v_add_f32_e32 v161, 1.0, v161
	v_rcp_f32_e32 v161, v161
	s_addc_u32 s49, s49, s41
	v_fma_f32 v162, v161, -2.0, 1.0
	v_sub_f32_e32 v163, v176, v162
	v_fma_f32 v176, v159, v163, v162
	v_fma_f32 v164, |v176|, s16, v117
	v_fma_f32 v165, |v176|, s17, v118
	v_fma_f32 v166, |v176|, s18, v119
	v_lshrrev_b32_e32 v167, 26, v176
	v_min3_u32 v164, v164, v165, v166
	v_bfi_b32 v168, 31, v164, v167
	v_lshrrev_b32_e32 v169, v181, v168
	global_store_short_d16_hi v185, v176, s[48:49]
	v_mul_u32_u24_dpp v170, v168, v180 quad_perm:[1,2,3,3] row_mask:0xf bank_mask:0xf bound_ctrl:1
	v_or_b32_e32 v171, v169, v170
	ds_write_b8 v184, v171 offset:416
	s_barrier
	ds_read_b64 v[122:123], v106 offset:416
	ds_read_b64 v[124:125], v106 offset:424
	ds_read_b64 v[126:127], v106 offset:432
	s_waitcnt lgkmcnt(3)
	s_barrier
	ds_read_b64 v[128:129], v106 offset:512
	ds_read_b64 v[130:131], v106 offset:520
	ds_read_b64 v[132:133], v106 offset:528
	s_waitcnt lgkmcnt(3)
	v_mfma_f32_16x16x128_f8f6f4 v[134:137], v[122:127], v[2:7], 0 cbsz:2 blgp:2
	v_mfma_f32_16x16x128_f8f6f4 v[138:141], v[122:127], v[14:19], 0 cbsz:2 blgp:2
	v_mfma_f32_16x16x128_f8f6f4 v[142:145], v[122:127], v[26:31], v[188:191] cbsz:2 blgp:2
	v_mfma_f32_16x16x128_f8f6f4 v[204:207], v[122:127], v[38:43], 0 cbsz:2 blgp:2
	v_mfma_f32_16x16x128_f8f6f4 v[208:211], v[122:127], v[50:55], 0 cbsz:2 blgp:2
	v_mfma_f32_16x16x128_f8f6f4 v[212:215], v[122:127], v[62:67], v[188:191] cbsz:2 blgp:2
	s_waitcnt lgkmcnt(0)
	v_mfma_f32_16x16x128_f8f6f4 v[134:137], v[128:133], v[8:13], v[134:137] cbsz:2 blgp:2
	v_mfma_f32_16x16x128_f8f6f4 v[204:207], v[128:133], v[44:49], v[204:207] cbsz:2 blgp:2
	v_mfma_f32_16x16x128_f8f6f4 v[138:141], v[128:133], v[20:25], v[138:141] cbsz:2 blgp:2
	v_mfma_f32_16x16x128_f8f6f4 v[208:211], v[128:133], v[56:61], v[208:211] cbsz:2 blgp:2
	v_mfma_f32_16x16x128_f8f6f4 v[142:145], v[128:133], v[32:37], v[142:145] cbsz:2 blgp:2
	v_mfma_f32_16x16x128_f8f6f4 v[212:215], v[128:133], v[68:73], v[212:215] cbsz:2 blgp:2
	v_cndmask_b32_e64 v158, v134, v204, s[4:5]
	v_fma_mix_f32 v158, v158, v1, v146 op_sel:[0,0,1] op_sel_hi:[0,0,1]
	v_exp_f32_e32 v158, v158
	v_cndmask_b32_e64 v159, v138, v208, s[4:5]
	v_fma_mix_f32 v159, v159, v99, v150 op_sel:[0,0,1] op_sel_hi:[0,0,1]
	v_exp_f32_e32 v159, v159
	v_fma_f32 v158, v158, v186, v186
	v_rcp_f32_e32 v158, v158
	v_add_f32_e32 v159, 1.0, v159
	v_rcp_f32_e32 v159, v159
	v_cndmask_b32_e64 v160, v142, v212, s[4:5]
	v_fma_mix_f32 v161, v158, v160, v154 op_sel:[0,0,1] op_sel_hi:[0,0,1]
	v_exp_f32_e32 v161, v161
	s_add_u32 s48, s48, s40
	v_add_f32_e32 v161, 1.0, v161
	v_rcp_f32_e32 v161, v161
	s_addc_u32 s49, s49, s41
	v_fma_f32 v162, v161, -2.0, 1.0
	v_sub_f32_e32 v163, v176, v162
	v_fma_f32 v176, v159, v163, v162
	v_fma_f32 v164, |v176|, s16, v117
	v_fma_f32 v165, |v176|, s17, v118
	v_fma_f32 v166, |v176|, s18, v119
	v_lshrrev_b32_e32 v167, 26, v176
	v_min3_u32 v164, v164, v165, v166
	v_bfi_b32 v168, 31, v164, v167
	v_lshrrev_b32_e32 v169, v181, v168
	global_store_short_d16_hi v185, v176, s[48:49]
	v_mul_u32_u24_dpp v170, v168, v180 quad_perm:[1,2,3,3] row_mask:0xf bank_mask:0xf bound_ctrl:1
	v_or_b32_e32 v171, v169, v170
	ds_write_b8 v184, v171
	s_barrier
	ds_read_b64 v[122:123], v106 offset:0
	ds_read_b64 v[124:125], v106 offset:8
	ds_read_b64 v[126:127], v106 offset:16
	s_waitcnt lgkmcnt(3)
	s_barrier
	ds_read_b64 v[128:129], v106 offset:96
	ds_read_b64 v[130:131], v106 offset:104
	ds_read_b64 v[132:133], v106 offset:112
	s_waitcnt lgkmcnt(3)
	v_mfma_f32_16x16x128_f8f6f4 v[134:137], v[122:127], v[2:7], 0 cbsz:2 blgp:2
	v_mfma_f32_16x16x128_f8f6f4 v[138:141], v[122:127], v[14:19], 0 cbsz:2 blgp:2
	v_mfma_f32_16x16x128_f8f6f4 v[142:145], v[122:127], v[26:31], v[188:191] cbsz:2 blgp:2
	v_mfma_f32_16x16x128_f8f6f4 v[204:207], v[122:127], v[38:43], 0 cbsz:2 blgp:2
	v_mfma_f32_16x16x128_f8f6f4 v[208:211], v[122:127], v[50:55], 0 cbsz:2 blgp:2
	v_mfma_f32_16x16x128_f8f6f4 v[212:215], v[122:127], v[62:67], v[188:191] cbsz:2 blgp:2
	s_waitcnt lgkmcnt(0)
	v_mfma_f32_16x16x128_f8f6f4 v[134:137], v[128:133], v[8:13], v[134:137] cbsz:2 blgp:2
	v_mfma_f32_16x16x128_f8f6f4 v[204:207], v[128:133], v[44:49], v[204:207] cbsz:2 blgp:2
	v_mfma_f32_16x16x128_f8f6f4 v[138:141], v[128:133], v[20:25], v[138:141] cbsz:2 blgp:2
	v_mfma_f32_16x16x128_f8f6f4 v[208:211], v[128:133], v[56:61], v[208:211] cbsz:2 blgp:2
	v_mfma_f32_16x16x128_f8f6f4 v[142:145], v[128:133], v[32:37], v[142:145] cbsz:2 blgp:2
	v_mfma_f32_16x16x128_f8f6f4 v[212:215], v[128:133], v[68:73], v[212:215] cbsz:2 blgp:2
	v_cndmask_b32_e64 v158, v134, v204, s[4:5]
	v_fma_mix_f32 v158, v158, v1, v147 op_sel_hi:[0,0,1]
	v_exp_f32_e32 v158, v158
	v_cndmask_b32_e64 v159, v138, v208, s[4:5]
	v_fma_mix_f32 v159, v159, v99, v151 op_sel_hi:[0,0,1]
	v_exp_f32_e32 v159, v159
	v_fma_f32 v158, v158, v186, v186
	v_rcp_f32_e32 v158, v158
	v_add_f32_e32 v159, 1.0, v159
	v_rcp_f32_e32 v159, v159
	v_cndmask_b32_e64 v160, v142, v212, s[4:5]
	v_fma_mix_f32 v161, v158, v160, v155 op_sel_hi:[0,0,1]
	v_exp_f32_e32 v161, v161
	s_add_u32 s48, s48, s40
	v_add_f32_e32 v161, 1.0, v161
	v_rcp_f32_e32 v161, v161
	s_addc_u32 s49, s49, s41
	v_fma_f32 v162, v161, -2.0, 1.0
	v_sub_f32_e32 v163, v176, v162
	v_fma_f32 v176, v159, v163, v162
	v_fma_f32 v164, |v176|, s16, v117
	v_fma_f32 v165, |v176|, s17, v118
	v_fma_f32 v166, |v176|, s18, v119
	v_lshrrev_b32_e32 v167, 26, v176
	v_min3_u32 v164, v164, v165, v166
	v_bfi_b32 v168, 31, v164, v167
	v_lshrrev_b32_e32 v169, v181, v168
	global_store_short_d16_hi v185, v176, s[48:49]
	v_mul_u32_u24_dpp v170, v168, v180 quad_perm:[1,2,3,3] row_mask:0xf bank_mask:0xf bound_ctrl:1
	v_or_b32_e32 v171, v169, v170
	ds_write_b8 v184, v171 offset:416
	s_barrier
	ds_read_b64 v[122:123], v106 offset:416
	ds_read_b64 v[124:125], v106 offset:424
	ds_read_b64 v[126:127], v106 offset:432
	s_waitcnt lgkmcnt(3)
	s_barrier
	ds_read_b64 v[128:129], v106 offset:512
	ds_read_b64 v[130:131], v106 offset:520
	ds_read_b64 v[132:133], v106 offset:528
	s_waitcnt lgkmcnt(3)
	v_mfma_f32_16x16x128_f8f6f4 v[134:137], v[122:127], v[2:7], 0 cbsz:2 blgp:2
	v_mfma_f32_16x16x128_f8f6f4 v[138:141], v[122:127], v[14:19], 0 cbsz:2 blgp:2
	v_mfma_f32_16x16x128_f8f6f4 v[142:145], v[122:127], v[26:31], v[188:191] cbsz:2 blgp:2
	v_mfma_f32_16x16x128_f8f6f4 v[204:207], v[122:127], v[38:43], 0 cbsz:2 blgp:2
	v_mfma_f32_16x16x128_f8f6f4 v[208:211], v[122:127], v[50:55], 0 cbsz:2 blgp:2
	v_mfma_f32_16x16x128_f8f6f4 v[212:215], v[122:127], v[62:67], v[188:191] cbsz:2 blgp:2
	s_waitcnt lgkmcnt(0)
	v_mfma_f32_16x16x128_f8f6f4 v[134:137], v[128:133], v[8:13], v[134:137] cbsz:2 blgp:2
	v_mfma_f32_16x16x128_f8f6f4 v[204:207], v[128:133], v[44:49], v[204:207] cbsz:2 blgp:2
	v_mfma_f32_16x16x128_f8f6f4 v[138:141], v[128:133], v[20:25], v[138:141] cbsz:2 blgp:2
	v_mfma_f32_16x16x128_f8f6f4 v[208:211], v[128:133], v[56:61], v[208:211] cbsz:2 blgp:2
	v_mfma_f32_16x16x128_f8f6f4 v[142:145], v[128:133], v[32:37], v[142:145] cbsz:2 blgp:2
	v_mfma_f32_16x16x128_f8f6f4 v[212:215], v[128:133], v[68:73], v[212:215] cbsz:2 blgp:2
	v_cndmask_b32_e64 v158, v134, v204, s[4:5]
	v_fma_mix_f32 v158, v158, v1, v147 op_sel:[0,0,1] op_sel_hi:[0,0,1]
	v_exp_f32_e32 v158, v158
	v_cndmask_b32_e64 v159, v138, v208, s[4:5]
	v_fma_mix_f32 v159, v159, v99, v151 op_sel:[0,0,1] op_sel_hi:[0,0,1]
	v_exp_f32_e32 v159, v159
	v_fma_f32 v158, v158, v186, v186
	v_rcp_f32_e32 v158, v158
	v_add_f32_e32 v159, 1.0, v159
	v_rcp_f32_e32 v159, v159
	v_cndmask_b32_e64 v160, v142, v212, s[4:5]
	v_fma_mix_f32 v161, v158, v160, v155 op_sel:[0,0,1] op_sel_hi:[0,0,1]
	v_exp_f32_e32 v161, v161
	s_add_u32 s48, s48, s40
	v_add_f32_e32 v161, 1.0, v161
	v_rcp_f32_e32 v161, v161
	s_addc_u32 s49, s49, s41
	v_fma_f32 v162, v161, -2.0, 1.0
	v_sub_f32_e32 v163, v176, v162
	v_fma_f32 v176, v159, v163, v162
	v_fma_f32 v164, |v176|, s16, v117
	v_fma_f32 v165, |v176|, s17, v118
	v_fma_f32 v166, |v176|, s18, v119
	v_lshrrev_b32_e32 v167, 26, v176
	v_min3_u32 v164, v164, v165, v166
	v_bfi_b32 v168, 31, v164, v167
	v_lshrrev_b32_e32 v169, v181, v168
	global_store_short_d16_hi v185, v176, s[48:49]
	v_mul_u32_u24_dpp v170, v168, v180 quad_perm:[1,2,3,3] row_mask:0xf bank_mask:0xf bound_ctrl:1
	v_or_b32_e32 v171, v169, v170
	ds_write_b8 v184, v171
	s_barrier
	ds_read_b64 v[122:123], v106 offset:0
	ds_read_b64 v[124:125], v106 offset:8
	ds_read_b64 v[126:127], v106 offset:16
	s_waitcnt lgkmcnt(3)
	s_barrier
	ds_read_b64 v[128:129], v106 offset:96
	ds_read_b64 v[130:131], v106 offset:104
	ds_read_b64 v[132:133], v106 offset:112
	s_waitcnt lgkmcnt(3)
	v_mfma_f32_16x16x128_f8f6f4 v[134:137], v[122:127], v[2:7], 0 cbsz:2 blgp:2
	v_mfma_f32_16x16x128_f8f6f4 v[138:141], v[122:127], v[14:19], 0 cbsz:2 blgp:2
	v_mfma_f32_16x16x128_f8f6f4 v[142:145], v[122:127], v[26:31], v[188:191] cbsz:2 blgp:2
	v_mfma_f32_16x16x128_f8f6f4 v[204:207], v[122:127], v[38:43], 0 cbsz:2 blgp:2
	v_mfma_f32_16x16x128_f8f6f4 v[208:211], v[122:127], v[50:55], 0 cbsz:2 blgp:2
	v_mfma_f32_16x16x128_f8f6f4 v[212:215], v[122:127], v[62:67], v[188:191] cbsz:2 blgp:2
	s_waitcnt lgkmcnt(0)
	v_mfma_f32_16x16x128_f8f6f4 v[134:137], v[128:133], v[8:13], v[134:137] cbsz:2 blgp:2
	v_mfma_f32_16x16x128_f8f6f4 v[204:207], v[128:133], v[44:49], v[204:207] cbsz:2 blgp:2
	v_mfma_f32_16x16x128_f8f6f4 v[138:141], v[128:133], v[20:25], v[138:141] cbsz:2 blgp:2
	v_mfma_f32_16x16x128_f8f6f4 v[208:211], v[128:133], v[56:61], v[208:211] cbsz:2 blgp:2
	v_mfma_f32_16x16x128_f8f6f4 v[142:145], v[128:133], v[32:37], v[142:145] cbsz:2 blgp:2
	v_mfma_f32_16x16x128_f8f6f4 v[212:215], v[128:133], v[68:73], v[212:215] cbsz:2 blgp:2
	v_cndmask_b32_e64 v158, v134, v204, s[4:5]
	v_fma_mix_f32 v158, v158, v1, v148 op_sel_hi:[0,0,1]
	v_exp_f32_e32 v158, v158
	v_cndmask_b32_e64 v159, v138, v208, s[4:5]
	v_fma_mix_f32 v159, v159, v99, v152 op_sel_hi:[0,0,1]
	v_exp_f32_e32 v159, v159
	v_fma_f32 v158, v158, v186, v186
	v_rcp_f32_e32 v158, v158
	v_add_f32_e32 v159, 1.0, v159
	v_rcp_f32_e32 v159, v159
	v_cndmask_b32_e64 v160, v142, v212, s[4:5]
	v_fma_mix_f32 v161, v158, v160, v156 op_sel_hi:[0,0,1]
	v_exp_f32_e32 v161, v161
	s_add_u32 s48, s48, s40
	v_add_f32_e32 v161, 1.0, v161
	v_rcp_f32_e32 v161, v161
	s_addc_u32 s49, s49, s41
	v_fma_f32 v162, v161, -2.0, 1.0
	v_sub_f32_e32 v163, v176, v162
	v_fma_f32 v176, v159, v163, v162
	v_fma_f32 v164, |v176|, s16, v117
	v_fma_f32 v165, |v176|, s17, v118
	v_fma_f32 v166, |v176|, s18, v119
	v_lshrrev_b32_e32 v167, 26, v176
	v_min3_u32 v164, v164, v165, v166
	v_bfi_b32 v168, 31, v164, v167
	v_lshrrev_b32_e32 v169, v181, v168
	global_store_short_d16_hi v185, v176, s[48:49]
	v_mul_u32_u24_dpp v170, v168, v180 quad_perm:[1,2,3,3] row_mask:0xf bank_mask:0xf bound_ctrl:1
	v_or_b32_e32 v171, v169, v170
	ds_write_b8 v184, v171 offset:416
	s_barrier
	ds_read_b64 v[122:123], v106 offset:416
	ds_read_b64 v[124:125], v106 offset:424
	ds_read_b64 v[126:127], v106 offset:432
	s_waitcnt lgkmcnt(3)
	s_barrier
	ds_read_b64 v[128:129], v106 offset:512
	ds_read_b64 v[130:131], v106 offset:520
	ds_read_b64 v[132:133], v106 offset:528
	s_waitcnt lgkmcnt(3)
	v_mfma_f32_16x16x128_f8f6f4 v[134:137], v[122:127], v[2:7], 0 cbsz:2 blgp:2
	v_mfma_f32_16x16x128_f8f6f4 v[138:141], v[122:127], v[14:19], 0 cbsz:2 blgp:2
	v_mfma_f32_16x16x128_f8f6f4 v[142:145], v[122:127], v[26:31], v[188:191] cbsz:2 blgp:2
	v_mfma_f32_16x16x128_f8f6f4 v[204:207], v[122:127], v[38:43], 0 cbsz:2 blgp:2
	v_mfma_f32_16x16x128_f8f6f4 v[208:211], v[122:127], v[50:55], 0 cbsz:2 blgp:2
	v_mfma_f32_16x16x128_f8f6f4 v[212:215], v[122:127], v[62:67], v[188:191] cbsz:2 blgp:2
	s_waitcnt lgkmcnt(0)
	v_mfma_f32_16x16x128_f8f6f4 v[134:137], v[128:133], v[8:13], v[134:137] cbsz:2 blgp:2
	v_mfma_f32_16x16x128_f8f6f4 v[204:207], v[128:133], v[44:49], v[204:207] cbsz:2 blgp:2
	v_mfma_f32_16x16x128_f8f6f4 v[138:141], v[128:133], v[20:25], v[138:141] cbsz:2 blgp:2
	v_mfma_f32_16x16x128_f8f6f4 v[208:211], v[128:133], v[56:61], v[208:211] cbsz:2 blgp:2
	v_mfma_f32_16x16x128_f8f6f4 v[142:145], v[128:133], v[32:37], v[142:145] cbsz:2 blgp:2
	v_mfma_f32_16x16x128_f8f6f4 v[212:215], v[128:133], v[68:73], v[212:215] cbsz:2 blgp:2
	v_cndmask_b32_e64 v158, v134, v204, s[4:5]
	v_fma_mix_f32 v158, v158, v1, v148 op_sel:[0,0,1] op_sel_hi:[0,0,1]
	v_exp_f32_e32 v158, v158
	v_cndmask_b32_e64 v159, v138, v208, s[4:5]
	v_fma_mix_f32 v159, v159, v99, v152 op_sel:[0,0,1] op_sel_hi:[0,0,1]
	v_exp_f32_e32 v159, v159
	v_fma_f32 v158, v158, v186, v186
	v_rcp_f32_e32 v158, v158
	v_add_f32_e32 v159, 1.0, v159
	v_rcp_f32_e32 v159, v159
	v_cndmask_b32_e64 v160, v142, v212, s[4:5]
	v_fma_mix_f32 v161, v158, v160, v156 op_sel:[0,0,1] op_sel_hi:[0,0,1]
	v_exp_f32_e32 v161, v161
	s_add_u32 s48, s48, s40
	v_add_f32_e32 v161, 1.0, v161
	v_rcp_f32_e32 v161, v161
	s_addc_u32 s49, s49, s41
	v_fma_f32 v162, v161, -2.0, 1.0
	v_sub_f32_e32 v163, v176, v162
	v_fma_f32 v176, v159, v163, v162
	v_fma_f32 v164, |v176|, s16, v117
	v_fma_f32 v165, |v176|, s17, v118
	v_fma_f32 v166, |v176|, s18, v119
	v_lshrrev_b32_e32 v167, 26, v176
	v_min3_u32 v164, v164, v165, v166
	v_bfi_b32 v168, 31, v164, v167
	v_lshrrev_b32_e32 v169, v181, v168
	global_store_short_d16_hi v185, v176, s[48:49]
	v_mul_u32_u24_dpp v170, v168, v180 quad_perm:[1,2,3,3] row_mask:0xf bank_mask:0xf bound_ctrl:1
	v_or_b32_e32 v171, v169, v170
	ds_write_b8 v184, v171
	s_barrier
	ds_read_b64 v[122:123], v106 offset:0
	ds_read_b64 v[124:125], v106 offset:8
	ds_read_b64 v[126:127], v106 offset:16
	s_waitcnt lgkmcnt(3)
	s_barrier
	ds_read_b64 v[128:129], v106 offset:96
	ds_read_b64 v[130:131], v106 offset:104
	ds_read_b64 v[132:133], v106 offset:112
	s_waitcnt lgkmcnt(3)
	v_mfma_f32_16x16x128_f8f6f4 v[134:137], v[122:127], v[2:7], 0 cbsz:2 blgp:2
	v_mfma_f32_16x16x128_f8f6f4 v[138:141], v[122:127], v[14:19], 0 cbsz:2 blgp:2
	v_mfma_f32_16x16x128_f8f6f4 v[142:145], v[122:127], v[26:31], v[188:191] cbsz:2 blgp:2
	v_mfma_f32_16x16x128_f8f6f4 v[204:207], v[122:127], v[38:43], 0 cbsz:2 blgp:2
	v_mfma_f32_16x16x128_f8f6f4 v[208:211], v[122:127], v[50:55], 0 cbsz:2 blgp:2
	v_mfma_f32_16x16x128_f8f6f4 v[212:215], v[122:127], v[62:67], v[188:191] cbsz:2 blgp:2
	s_waitcnt lgkmcnt(0)
	v_mfma_f32_16x16x128_f8f6f4 v[134:137], v[128:133], v[8:13], v[134:137] cbsz:2 blgp:2
	v_mfma_f32_16x16x128_f8f6f4 v[204:207], v[128:133], v[44:49], v[204:207] cbsz:2 blgp:2
	v_mfma_f32_16x16x128_f8f6f4 v[138:141], v[128:133], v[20:25], v[138:141] cbsz:2 blgp:2
	v_mfma_f32_16x16x128_f8f6f4 v[208:211], v[128:133], v[56:61], v[208:211] cbsz:2 blgp:2
	v_mfma_f32_16x16x128_f8f6f4 v[142:145], v[128:133], v[32:37], v[142:145] cbsz:2 blgp:2
	v_mfma_f32_16x16x128_f8f6f4 v[212:215], v[128:133], v[68:73], v[212:215] cbsz:2 blgp:2
	v_cndmask_b32_e64 v158, v134, v204, s[4:5]
	v_fma_mix_f32 v158, v158, v1, v149 op_sel_hi:[0,0,1]
	v_exp_f32_e32 v158, v158
	v_cndmask_b32_e64 v159, v138, v208, s[4:5]
	v_fma_mix_f32 v159, v159, v99, v153 op_sel_hi:[0,0,1]
	v_exp_f32_e32 v159, v159
	v_fma_f32 v158, v158, v186, v186
	v_rcp_f32_e32 v158, v158
	v_add_f32_e32 v159, 1.0, v159
	v_rcp_f32_e32 v159, v159
	v_cndmask_b32_e64 v160, v142, v212, s[4:5]
	v_fma_mix_f32 v161, v158, v160, v157 op_sel_hi:[0,0,1]
	v_exp_f32_e32 v161, v161
	s_add_u32 s48, s48, s40
	v_add_f32_e32 v161, 1.0, v161
	v_rcp_f32_e32 v161, v161
	s_addc_u32 s49, s49, s41
	v_fma_f32 v162, v161, -2.0, 1.0
	v_sub_f32_e32 v163, v176, v162
	v_fma_f32 v176, v159, v163, v162
	v_fma_f32 v164, |v176|, s16, v117
	v_fma_f32 v165, |v176|, s17, v118
	v_fma_f32 v166, |v176|, s18, v119
	v_lshrrev_b32_e32 v167, 26, v176
	v_min3_u32 v164, v164, v165, v166
	v_bfi_b32 v168, 31, v164, v167
	v_lshrrev_b32_e32 v169, v181, v168
	global_store_short_d16_hi v185, v176, s[48:49]
	v_mul_u32_u24_dpp v170, v168, v180 quad_perm:[1,2,3,3] row_mask:0xf bank_mask:0xf bound_ctrl:1
	v_or_b32_e32 v171, v169, v170
	ds_write_b8 v184, v171 offset:416
	s_barrier
	ds_read_b64 v[122:123], v106 offset:416
	ds_read_b64 v[124:125], v106 offset:424
	ds_read_b64 v[126:127], v106 offset:432
	s_waitcnt lgkmcnt(3)
	s_barrier
	ds_read_b64 v[128:129], v106 offset:512
	ds_read_b64 v[130:131], v106 offset:520
	ds_read_b64 v[132:133], v106 offset:528
	s_add_i32 s44, s44, 16
	s_waitcnt lgkmcnt(3)
	v_mfma_f32_16x16x128_f8f6f4 v[134:137], v[122:127], v[2:7], 0 cbsz:2 blgp:2
	v_mfma_f32_16x16x128_f8f6f4 v[138:141], v[122:127], v[14:19], 0 cbsz:2 blgp:2
	v_mfma_f32_16x16x128_f8f6f4 v[142:145], v[122:127], v[26:31], v[188:191] cbsz:2 blgp:2
	v_mfma_f32_16x16x128_f8f6f4 v[204:207], v[122:127], v[38:43], 0 cbsz:2 blgp:2
	v_mfma_f32_16x16x128_f8f6f4 v[208:211], v[122:127], v[50:55], 0 cbsz:2 blgp:2
	v_mfma_f32_16x16x128_f8f6f4 v[212:215], v[122:127], v[62:67], v[188:191] cbsz:2 blgp:2
	s_waitcnt lgkmcnt(0)
	v_mfma_f32_16x16x128_f8f6f4 v[134:137], v[128:133], v[8:13], v[134:137] cbsz:2 blgp:2
	v_mfma_f32_16x16x128_f8f6f4 v[204:207], v[128:133], v[44:49], v[204:207] cbsz:2 blgp:2
	v_mfma_f32_16x16x128_f8f6f4 v[138:141], v[128:133], v[20:25], v[138:141] cbsz:2 blgp:2
	v_mfma_f32_16x16x128_f8f6f4 v[208:211], v[128:133], v[56:61], v[208:211] cbsz:2 blgp:2
	v_mfma_f32_16x16x128_f8f6f4 v[142:145], v[128:133], v[32:37], v[142:145] cbsz:2 blgp:2
	v_mfma_f32_16x16x128_f8f6f4 v[212:215], v[128:133], v[68:73], v[212:215] cbsz:2 blgp:2
	v_cndmask_b32_e64 v158, v134, v204, s[4:5]
	v_fma_mix_f32 v158, v158, v1, v149 op_sel:[0,0,1] op_sel_hi:[0,0,1]
	v_exp_f32_e32 v158, v158
	v_cndmask_b32_e64 v159, v138, v208, s[4:5]
	v_fma_mix_f32 v159, v159, v99, v153 op_sel:[0,0,1] op_sel_hi:[0,0,1]
	v_exp_f32_e32 v159, v159
	v_fma_f32 v158, v158, v186, v186
	v_rcp_f32_e32 v158, v158
	v_add_f32_e32 v159, 1.0, v159
	v_rcp_f32_e32 v159, v159
	v_cndmask_b32_e64 v160, v142, v212, s[4:5]
	v_fma_mix_f32 v161, v158, v160, v157 op_sel:[0,0,1] op_sel_hi:[0,0,1]
	v_exp_f32_e32 v161, v161
	s_add_u32 s48, s48, s40
	v_add_f32_e32 v161, 1.0, v161
	v_rcp_f32_e32 v161, v161
	s_addc_u32 s49, s49, s41
	v_fma_f32 v162, v161, -2.0, 1.0
	v_sub_f32_e32 v163, v176, v162
	v_fma_f32 v176, v159, v163, v162
	v_fma_f32 v164, |v176|, s16, v117
	v_fma_f32 v165, |v176|, s17, v118
	v_fma_f32 v166, |v176|, s18, v119
	v_lshrrev_b32_e32 v167, 26, v176
	v_min3_u32 v164, v164, v165, v166
	v_bfi_b32 v168, 31, v164, v167
	v_lshrrev_b32_e32 v169, v181, v168
	global_store_short_d16_hi v185, v176, s[48:49]
	v_mul_u32_u24_dpp v170, v168, v180 quad_perm:[1,2,3,3] row_mask:0xf bank_mask:0xf bound_ctrl:1
	v_or_b32_e32 v171, v169, v170
	ds_write_b8 v184, v171
	s_barrier
	ds_read_b64 v[122:123], v106 offset:0
	ds_read_b64 v[124:125], v106 offset:8
	ds_read_b64 v[126:127], v106 offset:16
	s_cmp_lt_i32 s44, s45
	s_waitcnt lgkmcnt(3)
	s_barrier
	s_cbranch_scc1 .Lscan_loop_b_st

.Lscan_loop_a_f2:
	ds_read_b64 v[128:129], v105 offset:96
	ds_read_b64 v[130:131], v105 offset:104
	ds_read_b64 v[132:133], v105 offset:112
	s_waitcnt vmcnt(8)
	global_load_dwordx4 v[146:149], v[196:197], off
	global_load_dwordx4 v[150:153], v[196:197], off offset:512
	global_load_dwordx4 v[154:157], v[196:197], off offset:1024
	v_lshl_add_u64 v[196:197], v[196:197], 0, s[42:43]
	s_waitcnt lgkmcnt(3)
	v_mfma_f32_16x16x128_f8f6f4 v[134:137], v[122:127], v[2:7], 0 cbsz:2 blgp:2
	v_mfma_f32_16x16x128_f8f6f4 v[138:141], v[122:127], v[14:19], 0 cbsz:2 blgp:2
	v_mfma_f32_16x16x128_f8f6f4 v[142:145], v[122:127], v[26:31], v[188:191] cbsz:2 blgp:2
	v_mfma_f32_16x16x128_f8f6f4 v[204:207], v[122:127], v[38:43], 0 cbsz:2 blgp:2
	v_mfma_f32_16x16x128_f8f6f4 v[208:211], v[122:127], v[50:55], 0 cbsz:2 blgp:2
	v_mfma_f32_16x16x128_f8f6f4 v[212:215], v[122:127], v[62:67], v[188:191] cbsz:2 blgp:2
	s_waitcnt lgkmcnt(0)
	v_mfma_f32_16x16x128_f8f6f4 v[134:137], v[128:133], v[8:13], v[134:137] cbsz:2 blgp:2
	v_mfma_f32_16x16x128_f8f6f4 v[204:207], v[128:133], v[44:49], v[204:207] cbsz:2 blgp:2
	v_mfma_f32_16x16x128_f8f6f4 v[138:141], v[128:133], v[20:25], v[138:141] cbsz:2 blgp:2
	v_mfma_f32_16x16x128_f8f6f4 v[208:211], v[128:133], v[56:61], v[208:211] cbsz:2 blgp:2
	v_mfma_f32_16x16x128_f8f6f4 v[142:145], v[128:133], v[32:37], v[142:145] cbsz:2 blgp:2
	v_mfma_f32_16x16x128_f8f6f4 v[212:215], v[128:133], v[68:73], v[212:215] cbsz:2 blgp:2
	v_cndmask_b32_e64 v158, v134, v204, s[0:1]
	v_fma_mix_f32 v158, v158, v100, v82 op_sel_hi:[0,0,1]
	v_exp_f32_e32 v158, v158
	v_cndmask_b32_e64 v159, v138, v208, s[0:1]
	v_fma_mix_f32 v159, v159, v101, v74 op_sel_hi:[0,0,1]
	v_exp_f32_e32 v159, v159
	v_fma_f32 v158, v158, v186, v186
	v_rcp_f32_e32 v158, v158
	v_add_f32_e32 v159, 1.0, v159
	v_rcp_f32_e32 v159, v159
	v_cndmask_b32_e64 v160, v142, v212, s[0:1]
	v_fma_mix_f32 v161, v158, v160, v78 op_sel_hi:[0,0,1]
	v_exp_f32_e32 v161, v161
	s_add_u32 s48, s48, s40
	v_add_f32_e32 v161, 1.0, v161
	v_rcp_f32_e32 v161, v161
	s_addc_u32 s49, s49, s41
	v_fma_f32 v162, v161, -2.0, 1.0
	v_sub_f32_e32 v163, v176, v162
	v_fma_f32 v176, v159, v163, v162
	v_fma_f32 v164, |v176|, s17, v113
	v_fma_f32 v165, |v176|, s18, v114
	v_fma_f32 v166, |v176|, s19, v115
	v_lshrrev_b32_e32 v167, 26, v176
	v_min3_u32 v164, v164, v165, v166
	v_bfi_b32 v168, 31, v164, v167
	v_lshrrev_b32_e32 v169, v181, v168
	global_store_short_d16_hi v185, v176, s[48:49]
	v_mul_u32_u24_dpp v170, v168, v180 quad_perm:[1,2,3,3] row_mask:0xf bank_mask:0xf bound_ctrl:1
	v_or_b32_e32 v171, v169, v170
	ds_write_b8 v184, v171 offset:416
	s_waitcnt lgkmcnt(0)
	s_barrier
	ds_read_b64 v[122:123], v105 offset:416
	ds_read_b64 v[124:125], v105 offset:424
	ds_read_b64 v[126:127], v105 offset:432
	s_barrier
	ds_read_b64 v[128:129], v105 offset:512
	ds_read_b64 v[130:131], v105 offset:520
	ds_read_b64 v[132:133], v105 offset:528
	s_waitcnt lgkmcnt(3)
	v_mfma_f32_16x16x128_f8f6f4 v[134:137], v[122:127], v[2:7], 0 cbsz:2 blgp:2
	v_mfma_f32_16x16x128_f8f6f4 v[138:141], v[122:127], v[14:19], 0 cbsz:2 blgp:2
	v_mfma_f32_16x16x128_f8f6f4 v[142:145], v[122:127], v[26:31], v[188:191] cbsz:2 blgp:2
	v_mfma_f32_16x16x128_f8f6f4 v[204:207], v[122:127], v[38:43], 0 cbsz:2 blgp:2
	v_mfma_f32_16x16x128_f8f6f4 v[208:211], v[122:127], v[50:55], 0 cbsz:2 blgp:2
	v_mfma_f32_16x16x128_f8f6f4 v[212:215], v[122:127], v[62:67], v[188:191] cbsz:2 blgp:2
	s_waitcnt lgkmcnt(0)
	v_mfma_f32_16x16x128_f8f6f4 v[134:137], v[128:133], v[8:13], v[134:137] cbsz:2 blgp:2
	v_mfma_f32_16x16x128_f8f6f4 v[204:207], v[128:133], v[44:49], v[204:207] cbsz:2 blgp:2
	v_mfma_f32_16x16x128_f8f6f4 v[138:141], v[128:133], v[20:25], v[138:141] cbsz:2 blgp:2
	v_mfma_f32_16x16x128_f8f6f4 v[208:211], v[128:133], v[56:61], v[208:211] cbsz:2 blgp:2
	v_mfma_f32_16x16x128_f8f6f4 v[142:145], v[128:133], v[32:37], v[142:145] cbsz:2 blgp:2
	v_mfma_f32_16x16x128_f8f6f4 v[212:215], v[128:133], v[68:73], v[212:215] cbsz:2 blgp:2
	v_cndmask_b32_e64 v158, v134, v204, s[0:1]
	v_fma_mix_f32 v158, v158, v100, v82 op_sel:[0,0,1] op_sel_hi:[0,0,1]
	v_exp_f32_e32 v158, v158
	v_cndmask_b32_e64 v159, v138, v208, s[0:1]
	v_fma_mix_f32 v159, v159, v101, v74 op_sel:[0,0,1] op_sel_hi:[0,0,1]
	v_exp_f32_e32 v159, v159
	v_fma_f32 v158, v158, v186, v186
	v_rcp_f32_e32 v158, v158
	v_add_f32_e32 v159, 1.0, v159
	v_rcp_f32_e32 v159, v159
	v_cndmask_b32_e64 v160, v142, v212, s[0:1]
	v_fma_mix_f32 v161, v158, v160, v78 op_sel:[0,0,1] op_sel_hi:[0,0,1]
	v_exp_f32_e32 v161, v161
	s_add_u32 s48, s48, s40
	v_add_f32_e32 v161, 1.0, v161
	v_rcp_f32_e32 v161, v161
	s_addc_u32 s49, s49, s41
	v_fma_f32 v162, v161, -2.0, 1.0
	v_sub_f32_e32 v163, v176, v162
	v_fma_f32 v176, v159, v163, v162
	v_fma_f32 v164, |v176|, s17, v113
	v_fma_f32 v165, |v176|, s18, v114
	v_fma_f32 v166, |v176|, s19, v115
	v_lshrrev_b32_e32 v167, 26, v176
	v_min3_u32 v164, v164, v165, v166
	v_bfi_b32 v168, 31, v164, v167
	v_lshrrev_b32_e32 v169, v181, v168
	global_store_short_d16_hi v185, v176, s[48:49]
	v_mul_u32_u24_dpp v170, v168, v180 quad_perm:[1,2,3,3] row_mask:0xf bank_mask:0xf bound_ctrl:1
	v_or_b32_e32 v171, v169, v170
	ds_write_b8 v184, v171
	s_waitcnt lgkmcnt(0)
	s_barrier
	ds_read_b64 v[122:123], v105 offset:0
	ds_read_b64 v[124:125], v105 offset:8
	ds_read_b64 v[126:127], v105 offset:16
	s_barrier
	ds_read_b64 v[128:129], v105 offset:96
	ds_read_b64 v[130:131], v105 offset:104
	ds_read_b64 v[132:133], v105 offset:112
	s_waitcnt lgkmcnt(3)
	v_mfma_f32_16x16x128_f8f6f4 v[134:137], v[122:127], v[2:7], 0 cbsz:2 blgp:2
	v_mfma_f32_16x16x128_f8f6f4 v[138:141], v[122:127], v[14:19], 0 cbsz:2 blgp:2
	v_mfma_f32_16x16x128_f8f6f4 v[142:145], v[122:127], v[26:31], v[188:191] cbsz:2 blgp:2
	v_mfma_f32_16x16x128_f8f6f4 v[204:207], v[122:127], v[38:43], 0 cbsz:2 blgp:2
	v_mfma_f32_16x16x128_f8f6f4 v[208:211], v[122:127], v[50:55], 0 cbsz:2 blgp:2
	v_mfma_f32_16x16x128_f8f6f4 v[212:215], v[122:127], v[62:67], v[188:191] cbsz:2 blgp:2
	s_waitcnt lgkmcnt(0)
	v_mfma_f32_16x16x128_f8f6f4 v[134:137], v[128:133], v[8:13], v[134:137] cbsz:2 blgp:2
	v_mfma_f32_16x16x128_f8f6f4 v[204:207], v[128:133], v[44:49], v[204:207] cbsz:2 blgp:2
	v_mfma_f32_16x16x128_f8f6f4 v[138:141], v[128:133], v[20:25], v[138:141] cbsz:2 blgp:2
	v_mfma_f32_16x16x128_f8f6f4 v[208:211], v[128:133], v[56:61], v[208:211] cbsz:2 blgp:2
	v_mfma_f32_16x16x128_f8f6f4 v[142:145], v[128:133], v[32:37], v[142:145] cbsz:2 blgp:2
	v_mfma_f32_16x16x128_f8f6f4 v[212:215], v[128:133], v[68:73], v[212:215] cbsz:2 blgp:2
	v_cndmask_b32_e64 v158, v134, v204, s[0:1]
	v_fma_mix_f32 v158, v158, v100, v83 op_sel_hi:[0,0,1]
	v_exp_f32_e32 v158, v158
	v_cndmask_b32_e64 v159, v138, v208, s[0:1]
	v_fma_mix_f32 v159, v159, v101, v75 op_sel_hi:[0,0,1]
	v_exp_f32_e32 v159, v159
	v_fma_f32 v158, v158, v186, v186
	v_rcp_f32_e32 v158, v158
	v_add_f32_e32 v159, 1.0, v159
	v_rcp_f32_e32 v159, v159
	v_cndmask_b32_e64 v160, v142, v212, s[0:1]
	v_fma_mix_f32 v161, v158, v160, v79 op_sel_hi:[0,0,1]
	v_exp_f32_e32 v161, v161
	s_add_u32 s48, s48, s40
	v_add_f32_e32 v161, 1.0, v161
	v_rcp_f32_e32 v161, v161
	s_addc_u32 s49, s49, s41
	v_fma_f32 v162, v161, -2.0, 1.0
	v_sub_f32_e32 v163, v176, v162
	v_fma_f32 v176, v159, v163, v162
	v_fma_f32 v164, |v176|, s17, v113
	v_fma_f32 v165, |v176|, s18, v114
	v_fma_f32 v166, |v176|, s19, v115
	v_lshrrev_b32_e32 v167, 26, v176
	v_min3_u32 v164, v164, v165, v166
	v_bfi_b32 v168, 31, v164, v167
	v_lshrrev_b32_e32 v169, v181, v168
	global_store_short_d16_hi v185, v176, s[48:49]
	v_mul_u32_u24_dpp v170, v168, v180 quad_perm:[1,2,3,3] row_mask:0xf bank_mask:0xf bound_ctrl:1
	v_or_b32_e32 v171, v169, v170
	ds_write_b8 v184, v171 offset:416
	s_waitcnt lgkmcnt(0)
	s_barrier
	ds_read_b64 v[122:123], v105 offset:416
	ds_read_b64 v[124:125], v105 offset:424
	ds_read_b64 v[126:127], v105 offset:432
	s_barrier
	ds_read_b64 v[128:129], v105 offset:512
	ds_read_b64 v[130:131], v105 offset:520
	ds_read_b64 v[132:133], v105 offset:528
	s_waitcnt lgkmcnt(3)
	v_mfma_f32_16x16x128_f8f6f4 v[134:137], v[122:127], v[2:7], 0 cbsz:2 blgp:2
	v_mfma_f32_16x16x128_f8f6f4 v[138:141], v[122:127], v[14:19], 0 cbsz:2 blgp:2
	v_mfma_f32_16x16x128_f8f6f4 v[142:145], v[122:127], v[26:31], v[188:191] cbsz:2 blgp:2
	v_mfma_f32_16x16x128_f8f6f4 v[204:207], v[122:127], v[38:43], 0 cbsz:2 blgp:2
	v_mfma_f32_16x16x128_f8f6f4 v[208:211], v[122:127], v[50:55], 0 cbsz:2 blgp:2
	v_mfma_f32_16x16x128_f8f6f4 v[212:215], v[122:127], v[62:67], v[188:191] cbsz:2 blgp:2
	s_waitcnt lgkmcnt(0)
	v_mfma_f32_16x16x128_f8f6f4 v[134:137], v[128:133], v[8:13], v[134:137] cbsz:2 blgp:2
	v_mfma_f32_16x16x128_f8f6f4 v[204:207], v[128:133], v[44:49], v[204:207] cbsz:2 blgp:2
	v_mfma_f32_16x16x128_f8f6f4 v[138:141], v[128:133], v[20:25], v[138:141] cbsz:2 blgp:2
	v_mfma_f32_16x16x128_f8f6f4 v[208:211], v[128:133], v[56:61], v[208:211] cbsz:2 blgp:2
	v_mfma_f32_16x16x128_f8f6f4 v[142:145], v[128:133], v[32:37], v[142:145] cbsz:2 blgp:2
	v_mfma_f32_16x16x128_f8f6f4 v[212:215], v[128:133], v[68:73], v[212:215] cbsz:2 blgp:2
	v_cndmask_b32_e64 v158, v134, v204, s[0:1]
	v_fma_mix_f32 v158, v158, v100, v83 op_sel:[0,0,1] op_sel_hi:[0,0,1]
	v_exp_f32_e32 v158, v158
	v_cndmask_b32_e64 v159, v138, v208, s[0:1]
	v_fma_mix_f32 v159, v159, v101, v75 op_sel:[0,0,1] op_sel_hi:[0,0,1]
	v_exp_f32_e32 v159, v159
	v_fma_f32 v158, v158, v186, v186
	v_rcp_f32_e32 v158, v158
	v_add_f32_e32 v159, 1.0, v159
	v_rcp_f32_e32 v159, v159
	v_cndmask_b32_e64 v160, v142, v212, s[0:1]
	v_fma_mix_f32 v161, v158, v160, v79 op_sel:[0,0,1] op_sel_hi:[0,0,1]
	v_exp_f32_e32 v161, v161
	s_add_u32 s48, s48, s40
	v_add_f32_e32 v161, 1.0, v161
	v_rcp_f32_e32 v161, v161
	s_addc_u32 s49, s49, s41
	v_fma_f32 v162, v161, -2.0, 1.0
	v_sub_f32_e32 v163, v176, v162
	v_fma_f32 v176, v159, v163, v162
	v_fma_f32 v164, |v176|, s17, v113
	v_fma_f32 v165, |v176|, s18, v114
	v_fma_f32 v166, |v176|, s19, v115
	v_lshrrev_b32_e32 v167, 26, v176
	v_min3_u32 v164, v164, v165, v166
	v_bfi_b32 v168, 31, v164, v167
	v_lshrrev_b32_e32 v169, v181, v168
	global_store_short_d16_hi v185, v176, s[48:49]
	v_mul_u32_u24_dpp v170, v168, v180 quad_perm:[1,2,3,3] row_mask:0xf bank_mask:0xf bound_ctrl:1
	v_or_b32_e32 v171, v169, v170
	ds_write_b8 v184, v171
	s_waitcnt lgkmcnt(0)
	s_barrier
	ds_read_b64 v[122:123], v105 offset:0
	ds_read_b64 v[124:125], v105 offset:8
	ds_read_b64 v[126:127], v105 offset:16
	s_barrier
	ds_read_b64 v[128:129], v105 offset:96
	ds_read_b64 v[130:131], v105 offset:104
	ds_read_b64 v[132:133], v105 offset:112
	s_waitcnt lgkmcnt(3)
	v_mfma_f32_16x16x128_f8f6f4 v[134:137], v[122:127], v[2:7], 0 cbsz:2 blgp:2
	v_mfma_f32_16x16x128_f8f6f4 v[138:141], v[122:127], v[14:19], 0 cbsz:2 blgp:2
	v_mfma_f32_16x16x128_f8f6f4 v[142:145], v[122:127], v[26:31], v[188:191] cbsz:2 blgp:2
	v_mfma_f32_16x16x128_f8f6f4 v[204:207], v[122:127], v[38:43], 0 cbsz:2 blgp:2
	v_mfma_f32_16x16x128_f8f6f4 v[208:211], v[122:127], v[50:55], 0 cbsz:2 blgp:2
	v_mfma_f32_16x16x128_f8f6f4 v[212:215], v[122:127], v[62:67], v[188:191] cbsz:2 blgp:2
	s_waitcnt lgkmcnt(0)
	v_mfma_f32_16x16x128_f8f6f4 v[134:137], v[128:133], v[8:13], v[134:137] cbsz:2 blgp:2
	v_mfma_f32_16x16x128_f8f6f4 v[204:207], v[128:133], v[44:49], v[204:207] cbsz:2 blgp:2
	v_mfma_f32_16x16x128_f8f6f4 v[138:141], v[128:133], v[20:25], v[138:141] cbsz:2 blgp:2
	v_mfma_f32_16x16x128_f8f6f4 v[208:211], v[128:133], v[56:61], v[208:211] cbsz:2 blgp:2
	v_mfma_f32_16x16x128_f8f6f4 v[142:145], v[128:133], v[32:37], v[142:145] cbsz:2 blgp:2
	v_mfma_f32_16x16x128_f8f6f4 v[212:215], v[128:133], v[68:73], v[212:215] cbsz:2 blgp:2
	v_cndmask_b32_e64 v158, v134, v204, s[0:1]
	v_fma_mix_f32 v158, v158, v100, v84 op_sel_hi:[0,0,1]
	v_exp_f32_e32 v158, v158
	v_cndmask_b32_e64 v159, v138, v208, s[0:1]
	v_fma_mix_f32 v159, v159, v101, v76 op_sel_hi:[0,0,1]
	v_exp_f32_e32 v159, v159
	v_fma_f32 v158, v158, v186, v186
	v_rcp_f32_e32 v158, v158
	v_add_f32_e32 v159, 1.0, v159
	v_rcp_f32_e32 v159, v159
	v_cndmask_b32_e64 v160, v142, v212, s[0:1]
	v_fma_mix_f32 v161, v158, v160, v80 op_sel_hi:[0,0,1]
	v_exp_f32_e32 v161, v161
	s_add_u32 s48, s48, s40
	v_add_f32_e32 v161, 1.0, v161
	v_rcp_f32_e32 v161, v161
	s_addc_u32 s49, s49, s41
	v_fma_f32 v162, v161, -2.0, 1.0
	v_sub_f32_e32 v163, v176, v162
	v_fma_f32 v176, v159, v163, v162
	v_fma_f32 v164, |v176|, s17, v113
	v_fma_f32 v165, |v176|, s18, v114
	v_fma_f32 v166, |v176|, s19, v115
	v_lshrrev_b32_e32 v167, 26, v176
	v_min3_u32 v164, v164, v165, v166
	v_bfi_b32 v168, 31, v164, v167
	v_lshrrev_b32_e32 v169, v181, v168
	global_store_short_d16_hi v185, v176, s[48:49]
	v_mul_u32_u24_dpp v170, v168, v180 quad_perm:[1,2,3,3] row_mask:0xf bank_mask:0xf bound_ctrl:1
	v_or_b32_e32 v171, v169, v170
	ds_write_b8 v184, v171 offset:416
	s_waitcnt lgkmcnt(0)
	s_barrier
	ds_read_b64 v[122:123], v105 offset:416
	ds_read_b64 v[124:125], v105 offset:424
	ds_read_b64 v[126:127], v105 offset:432
	s_barrier
	ds_read_b64 v[128:129], v105 offset:512
	ds_read_b64 v[130:131], v105 offset:520
	ds_read_b64 v[132:133], v105 offset:528
	s_waitcnt lgkmcnt(3)
	v_mfma_f32_16x16x128_f8f6f4 v[134:137], v[122:127], v[2:7], 0 cbsz:2 blgp:2
	v_mfma_f32_16x16x128_f8f6f4 v[138:141], v[122:127], v[14:19], 0 cbsz:2 blgp:2
	v_mfma_f32_16x16x128_f8f6f4 v[142:145], v[122:127], v[26:31], v[188:191] cbsz:2 blgp:2
	v_mfma_f32_16x16x128_f8f6f4 v[204:207], v[122:127], v[38:43], 0 cbsz:2 blgp:2
	v_mfma_f32_16x16x128_f8f6f4 v[208:211], v[122:127], v[50:55], 0 cbsz:2 blgp:2
	v_mfma_f32_16x16x128_f8f6f4 v[212:215], v[122:127], v[62:67], v[188:191] cbsz:2 blgp:2
	s_waitcnt lgkmcnt(0)
	v_mfma_f32_16x16x128_f8f6f4 v[134:137], v[128:133], v[8:13], v[134:137] cbsz:2 blgp:2
	v_mfma_f32_16x16x128_f8f6f4 v[204:207], v[128:133], v[44:49], v[204:207] cbsz:2 blgp:2
	v_mfma_f32_16x16x128_f8f6f4 v[138:141], v[128:133], v[20:25], v[138:141] cbsz:2 blgp:2
	v_mfma_f32_16x16x128_f8f6f4 v[208:211], v[128:133], v[56:61], v[208:211] cbsz:2 blgp:2
	v_mfma_f32_16x16x128_f8f6f4 v[142:145], v[128:133], v[32:37], v[142:145] cbsz:2 blgp:2
	v_mfma_f32_16x16x128_f8f6f4 v[212:215], v[128:133], v[68:73], v[212:215] cbsz:2 blgp:2
	v_cndmask_b32_e64 v158, v134, v204, s[0:1]
	v_fma_mix_f32 v158, v158, v100, v84 op_sel:[0,0,1] op_sel_hi:[0,0,1]
	v_exp_f32_e32 v158, v158
	v_cndmask_b32_e64 v159, v138, v208, s[0:1]
	v_fma_mix_f32 v159, v159, v101, v76 op_sel:[0,0,1] op_sel_hi:[0,0,1]
	v_exp_f32_e32 v159, v159
	v_fma_f32 v158, v158, v186, v186
	v_rcp_f32_e32 v158, v158
	v_add_f32_e32 v159, 1.0, v159
	v_rcp_f32_e32 v159, v159
	v_cndmask_b32_e64 v160, v142, v212, s[0:1]
	v_fma_mix_f32 v161, v158, v160, v80 op_sel:[0,0,1] op_sel_hi:[0,0,1]
	v_exp_f32_e32 v161, v161
	s_add_u32 s48, s48, s40
	v_add_f32_e32 v161, 1.0, v161
	v_rcp_f32_e32 v161, v161
	s_addc_u32 s49, s49, s41
	v_fma_f32 v162, v161, -2.0, 1.0
	v_sub_f32_e32 v163, v176, v162
	v_fma_f32 v176, v159, v163, v162
	v_fma_f32 v164, |v176|, s17, v113
	v_fma_f32 v165, |v176|, s18, v114
	v_fma_f32 v166, |v176|, s19, v115
	v_lshrrev_b32_e32 v167, 26, v176
	v_min3_u32 v164, v164, v165, v166
	v_bfi_b32 v168, 31, v164, v167
	v_lshrrev_b32_e32 v169, v181, v168
	global_store_short_d16_hi v185, v176, s[48:49]
	v_mul_u32_u24_dpp v170, v168, v180 quad_perm:[1,2,3,3] row_mask:0xf bank_mask:0xf bound_ctrl:1
	v_or_b32_e32 v171, v169, v170
	ds_write_b8 v184, v171
	s_waitcnt lgkmcnt(0)
	s_barrier
	ds_read_b64 v[122:123], v105 offset:0
	ds_read_b64 v[124:125], v105 offset:8
	ds_read_b64 v[126:127], v105 offset:16
	s_barrier
	ds_read_b64 v[128:129], v105 offset:96
	ds_read_b64 v[130:131], v105 offset:104
	ds_read_b64 v[132:133], v105 offset:112
	s_waitcnt lgkmcnt(3)
	v_mfma_f32_16x16x128_f8f6f4 v[134:137], v[122:127], v[2:7], 0 cbsz:2 blgp:2
	v_mfma_f32_16x16x128_f8f6f4 v[138:141], v[122:127], v[14:19], 0 cbsz:2 blgp:2
	v_mfma_f32_16x16x128_f8f6f4 v[142:145], v[122:127], v[26:31], v[188:191] cbsz:2 blgp:2
	v_mfma_f32_16x16x128_f8f6f4 v[204:207], v[122:127], v[38:43], 0 cbsz:2 blgp:2
	v_mfma_f32_16x16x128_f8f6f4 v[208:211], v[122:127], v[50:55], 0 cbsz:2 blgp:2
	v_mfma_f32_16x16x128_f8f6f4 v[212:215], v[122:127], v[62:67], v[188:191] cbsz:2 blgp:2
	s_waitcnt lgkmcnt(0)
	v_mfma_f32_16x16x128_f8f6f4 v[134:137], v[128:133], v[8:13], v[134:137] cbsz:2 blgp:2
	v_mfma_f32_16x16x128_f8f6f4 v[204:207], v[128:133], v[44:49], v[204:207] cbsz:2 blgp:2
	v_mfma_f32_16x16x128_f8f6f4 v[138:141], v[128:133], v[20:25], v[138:141] cbsz:2 blgp:2
	v_mfma_f32_16x16x128_f8f6f4 v[208:211], v[128:133], v[56:61], v[208:211] cbsz:2 blgp:2
	v_mfma_f32_16x16x128_f8f6f4 v[142:145], v[128:133], v[32:37], v[142:145] cbsz:2 blgp:2
	v_mfma_f32_16x16x128_f8f6f4 v[212:215], v[128:133], v[68:73], v[212:215] cbsz:2 blgp:2
	v_cndmask_b32_e64 v158, v134, v204, s[0:1]
	v_fma_mix_f32 v158, v158, v100, v85 op_sel_hi:[0,0,1]
	v_exp_f32_e32 v158, v158
	v_cndmask_b32_e64 v159, v138, v208, s[0:1]
	v_fma_mix_f32 v159, v159, v101, v77 op_sel_hi:[0,0,1]
	v_exp_f32_e32 v159, v159
	v_fma_f32 v158, v158, v186, v186
	v_rcp_f32_e32 v158, v158
	v_add_f32_e32 v159, 1.0, v159
	v_rcp_f32_e32 v159, v159
	v_cndmask_b32_e64 v160, v142, v212, s[0:1]
	v_fma_mix_f32 v161, v158, v160, v81 op_sel_hi:[0,0,1]
	v_exp_f32_e32 v161, v161
	s_add_u32 s48, s48, s40
	v_add_f32_e32 v161, 1.0, v161
	v_rcp_f32_e32 v161, v161
	s_addc_u32 s49, s49, s41
	v_fma_f32 v162, v161, -2.0, 1.0
	v_sub_f32_e32 v163, v176, v162
	v_fma_f32 v176, v159, v163, v162
	v_fma_f32 v164, |v176|, s17, v113
	v_fma_f32 v165, |v176|, s18, v114
	v_fma_f32 v166, |v176|, s19, v115
	v_lshrrev_b32_e32 v167, 26, v176
	v_min3_u32 v164, v164, v165, v166
	v_bfi_b32 v168, 31, v164, v167
	v_lshrrev_b32_e32 v169, v181, v168
	global_store_short_d16_hi v185, v176, s[48:49]
	v_mul_u32_u24_dpp v170, v168, v180 quad_perm:[1,2,3,3] row_mask:0xf bank_mask:0xf bound_ctrl:1
	v_or_b32_e32 v171, v169, v170
	ds_write_b8 v184, v171 offset:416
	s_waitcnt lgkmcnt(0)
	s_barrier
	ds_read_b64 v[122:123], v105 offset:416
	ds_read_b64 v[124:125], v105 offset:424
	ds_read_b64 v[126:127], v105 offset:432
	s_barrier
	ds_read_b64 v[128:129], v105 offset:512
	ds_read_b64 v[130:131], v105 offset:520
	ds_read_b64 v[132:133], v105 offset:528
	s_waitcnt lgkmcnt(3)
	v_mfma_f32_16x16x128_f8f6f4 v[134:137], v[122:127], v[2:7], 0 cbsz:2 blgp:2
	v_mfma_f32_16x16x128_f8f6f4 v[138:141], v[122:127], v[14:19], 0 cbsz:2 blgp:2
	v_mfma_f32_16x16x128_f8f6f4 v[142:145], v[122:127], v[26:31], v[188:191] cbsz:2 blgp:2
	v_mfma_f32_16x16x128_f8f6f4 v[204:207], v[122:127], v[38:43], 0 cbsz:2 blgp:2
	v_mfma_f32_16x16x128_f8f6f4 v[208:211], v[122:127], v[50:55], 0 cbsz:2 blgp:2
	v_mfma_f32_16x16x128_f8f6f4 v[212:215], v[122:127], v[62:67], v[188:191] cbsz:2 blgp:2
	s_waitcnt lgkmcnt(0)
	v_mfma_f32_16x16x128_f8f6f4 v[134:137], v[128:133], v[8:13], v[134:137] cbsz:2 blgp:2
	v_mfma_f32_16x16x128_f8f6f4 v[204:207], v[128:133], v[44:49], v[204:207] cbsz:2 blgp:2
	v_mfma_f32_16x16x128_f8f6f4 v[138:141], v[128:133], v[20:25], v[138:141] cbsz:2 blgp:2
	v_mfma_f32_16x16x128_f8f6f4 v[208:211], v[128:133], v[56:61], v[208:211] cbsz:2 blgp:2
	v_mfma_f32_16x16x128_f8f6f4 v[142:145], v[128:133], v[32:37], v[142:145] cbsz:2 blgp:2
	v_mfma_f32_16x16x128_f8f6f4 v[212:215], v[128:133], v[68:73], v[212:215] cbsz:2 blgp:2
	v_cndmask_b32_e64 v158, v134, v204, s[0:1]
	v_fma_mix_f32 v158, v158, v100, v85 op_sel:[0,0,1] op_sel_hi:[0,0,1]
	v_exp_f32_e32 v158, v158
	v_cndmask_b32_e64 v159, v138, v208, s[0:1]
	v_fma_mix_f32 v159, v159, v101, v77 op_sel:[0,0,1] op_sel_hi:[0,0,1]
	v_exp_f32_e32 v159, v159
	v_fma_f32 v158, v158, v186, v186
	v_rcp_f32_e32 v158, v158
	v_add_f32_e32 v159, 1.0, v159
	v_rcp_f32_e32 v159, v159
	v_cndmask_b32_e64 v160, v142, v212, s[0:1]
	v_fma_mix_f32 v161, v158, v160, v81 op_sel:[0,0,1] op_sel_hi:[0,0,1]
	v_exp_f32_e32 v161, v161
	s_add_u32 s48, s48, s40
	v_add_f32_e32 v161, 1.0, v161
	v_rcp_f32_e32 v161, v161
	s_addc_u32 s49, s49, s41
	v_fma_f32 v162, v161, -2.0, 1.0
	v_sub_f32_e32 v163, v176, v162
	v_fma_f32 v176, v159, v163, v162
	v_fma_f32 v164, |v176|, s17, v113
	v_fma_f32 v165, |v176|, s18, v114
	v_fma_f32 v166, |v176|, s19, v115
	v_lshrrev_b32_e32 v167, 26, v176
	v_min3_u32 v164, v164, v165, v166
	v_bfi_b32 v168, 31, v164, v167
	v_lshrrev_b32_e32 v169, v181, v168
	global_store_short_d16_hi v185, v176, s[48:49]
	v_mul_u32_u24_dpp v170, v168, v180 quad_perm:[1,2,3,3] row_mask:0xf bank_mask:0xf bound_ctrl:1
	v_or_b32_e32 v171, v169, v170
	ds_write_b8 v184, v171
	s_waitcnt lgkmcnt(0)
	s_barrier
	ds_read_b64 v[122:123], v105 offset:0
	ds_read_b64 v[124:125], v105 offset:8
	ds_read_b64 v[126:127], v105 offset:16
	s_barrier
	ds_read_b64 v[128:129], v105 offset:96
	ds_read_b64 v[130:131], v105 offset:104
	ds_read_b64 v[132:133], v105 offset:112
	s_waitcnt vmcnt(8)
	global_load_dwordx4 v[82:85], v[196:197], off
	global_load_dwordx4 v[74:77], v[196:197], off offset:512
	global_load_dwordx4 v[78:81], v[196:197], off offset:1024
	v_lshl_add_u64 v[196:197], v[196:197], 0, s[42:43]
	s_waitcnt lgkmcnt(3)
	v_mfma_f32_16x16x128_f8f6f4 v[134:137], v[122:127], v[2:7], 0 cbsz:2 blgp:2
	v_mfma_f32_16x16x128_f8f6f4 v[138:141], v[122:127], v[14:19], 0 cbsz:2 blgp:2
	v_mfma_f32_16x16x128_f8f6f4 v[142:145], v[122:127], v[26:31], v[188:191] cbsz:2 blgp:2
	v_mfma_f32_16x16x128_f8f6f4 v[204:207], v[122:127], v[38:43], 0 cbsz:2 blgp:2
	v_mfma_f32_16x16x128_f8f6f4 v[208:211], v[122:127], v[50:55], 0 cbsz:2 blgp:2
	v_mfma_f32_16x16x128_f8f6f4 v[212:215], v[122:127], v[62:67], v[188:191] cbsz:2 blgp:2
	s_waitcnt lgkmcnt(0)
	v_mfma_f32_16x16x128_f8f6f4 v[134:137], v[128:133], v[8:13], v[134:137] cbsz:2 blgp:2
	v_mfma_f32_16x16x128_f8f6f4 v[204:207], v[128:133], v[44:49], v[204:207] cbsz:2 blgp:2
	v_mfma_f32_16x16x128_f8f6f4 v[138:141], v[128:133], v[20:25], v[138:141] cbsz:2 blgp:2
	v_mfma_f32_16x16x128_f8f6f4 v[208:211], v[128:133], v[56:61], v[208:211] cbsz:2 blgp:2
	v_mfma_f32_16x16x128_f8f6f4 v[142:145], v[128:133], v[32:37], v[142:145] cbsz:2 blgp:2
	v_mfma_f32_16x16x128_f8f6f4 v[212:215], v[128:133], v[68:73], v[212:215] cbsz:2 blgp:2
	v_cndmask_b32_e64 v158, v134, v204, s[0:1]
	v_fma_mix_f32 v158, v158, v100, v146 op_sel_hi:[0,0,1]
	v_exp_f32_e32 v158, v158
	v_cndmask_b32_e64 v159, v138, v208, s[0:1]
	v_fma_mix_f32 v159, v159, v101, v150 op_sel_hi:[0,0,1]
	v_exp_f32_e32 v159, v159
	v_fma_f32 v158, v158, v186, v186
	v_rcp_f32_e32 v158, v158
	v_add_f32_e32 v159, 1.0, v159
	v_rcp_f32_e32 v159, v159
	v_cndmask_b32_e64 v160, v142, v212, s[0:1]
	v_fma_mix_f32 v161, v158, v160, v154 op_sel_hi:[0,0,1]
	v_exp_f32_e32 v161, v161
	s_add_u32 s48, s48, s40
	v_add_f32_e32 v161, 1.0, v161
	v_rcp_f32_e32 v161, v161
	s_addc_u32 s49, s49, s41
	v_fma_f32 v162, v161, -2.0, 1.0
	v_sub_f32_e32 v163, v176, v162
	v_fma_f32 v176, v159, v163, v162
	v_fma_f32 v164, |v176|, s17, v113
	v_fma_f32 v165, |v176|, s18, v114
	v_fma_f32 v166, |v176|, s19, v115
	v_lshrrev_b32_e32 v167, 26, v176
	v_min3_u32 v164, v164, v165, v166
	v_bfi_b32 v168, 31, v164, v167
	v_lshrrev_b32_e32 v169, v181, v168
	global_store_short_d16_hi v185, v176, s[48:49]
	v_mul_u32_u24_dpp v170, v168, v180 quad_perm:[1,2,3,3] row_mask:0xf bank_mask:0xf bound_ctrl:1
	v_or_b32_e32 v171, v169, v170
	ds_write_b8 v184, v171 offset:416
	s_waitcnt lgkmcnt(0)
	s_barrier
	ds_read_b64 v[122:123], v105 offset:416
	ds_read_b64 v[124:125], v105 offset:424
	ds_read_b64 v[126:127], v105 offset:432
	s_barrier
	ds_read_b64 v[128:129], v105 offset:512
	ds_read_b64 v[130:131], v105 offset:520
	ds_read_b64 v[132:133], v105 offset:528
	s_waitcnt lgkmcnt(3)
	v_mfma_f32_16x16x128_f8f6f4 v[134:137], v[122:127], v[2:7], 0 cbsz:2 blgp:2
	v_mfma_f32_16x16x128_f8f6f4 v[138:141], v[122:127], v[14:19], 0 cbsz:2 blgp:2
	v_mfma_f32_16x16x128_f8f6f4 v[142:145], v[122:127], v[26:31], v[188:191] cbsz:2 blgp:2
	v_mfma_f32_16x16x128_f8f6f4 v[204:207], v[122:127], v[38:43], 0 cbsz:2 blgp:2
	v_mfma_f32_16x16x128_f8f6f4 v[208:211], v[122:127], v[50:55], 0 cbsz:2 blgp:2
	v_mfma_f32_16x16x128_f8f6f4 v[212:215], v[122:127], v[62:67], v[188:191] cbsz:2 blgp:2
	s_waitcnt lgkmcnt(0)
	v_mfma_f32_16x16x128_f8f6f4 v[134:137], v[128:133], v[8:13], v[134:137] cbsz:2 blgp:2
	v_mfma_f32_16x16x128_f8f6f4 v[204:207], v[128:133], v[44:49], v[204:207] cbsz:2 blgp:2
	v_mfma_f32_16x16x128_f8f6f4 v[138:141], v[128:133], v[20:25], v[138:141] cbsz:2 blgp:2
	v_mfma_f32_16x16x128_f8f6f4 v[208:211], v[128:133], v[56:61], v[208:211] cbsz:2 blgp:2
	v_mfma_f32_16x16x128_f8f6f4 v[142:145], v[128:133], v[32:37], v[142:145] cbsz:2 blgp:2
	v_mfma_f32_16x16x128_f8f6f4 v[212:215], v[128:133], v[68:73], v[212:215] cbsz:2 blgp:2
	v_cndmask_b32_e64 v158, v134, v204, s[0:1]
	v_fma_mix_f32 v158, v158, v100, v146 op_sel:[0,0,1] op_sel_hi:[0,0,1]
	v_exp_f32_e32 v158, v158
	v_cndmask_b32_e64 v159, v138, v208, s[0:1]
	v_fma_mix_f32 v159, v159, v101, v150 op_sel:[0,0,1] op_sel_hi:[0,0,1]
	v_exp_f32_e32 v159, v159
	v_fma_f32 v158, v158, v186, v186
	v_rcp_f32_e32 v158, v158
	v_add_f32_e32 v159, 1.0, v159
	v_rcp_f32_e32 v159, v159
	v_cndmask_b32_e64 v160, v142, v212, s[0:1]
	v_fma_mix_f32 v161, v158, v160, v154 op_sel:[0,0,1] op_sel_hi:[0,0,1]
	v_exp_f32_e32 v161, v161
	s_add_u32 s48, s48, s40
	v_add_f32_e32 v161, 1.0, v161
	v_rcp_f32_e32 v161, v161
	s_addc_u32 s49, s49, s41
	v_fma_f32 v162, v161, -2.0, 1.0
	v_sub_f32_e32 v163, v176, v162
	v_fma_f32 v176, v159, v163, v162
	v_fma_f32 v164, |v176|, s17, v113
	v_fma_f32 v165, |v176|, s18, v114
	v_fma_f32 v166, |v176|, s19, v115
	v_lshrrev_b32_e32 v167, 26, v176
	v_min3_u32 v164, v164, v165, v166
	v_bfi_b32 v168, 31, v164, v167
	v_lshrrev_b32_e32 v169, v181, v168
	global_store_short_d16_hi v185, v176, s[48:49]
	v_mul_u32_u24_dpp v170, v168, v180 quad_perm:[1,2,3,3] row_mask:0xf bank_mask:0xf bound_ctrl:1
	v_or_b32_e32 v171, v169, v170
	ds_write_b8 v184, v171
	s_waitcnt lgkmcnt(0)
	s_barrier
	ds_read_b64 v[122:123], v105 offset:0
	ds_read_b64 v[124:125], v105 offset:8
	ds_read_b64 v[126:127], v105 offset:16
	s_barrier
	ds_read_b64 v[128:129], v105 offset:96
	ds_read_b64 v[130:131], v105 offset:104
	ds_read_b64 v[132:133], v105 offset:112
	s_waitcnt lgkmcnt(3)
	v_mfma_f32_16x16x128_f8f6f4 v[134:137], v[122:127], v[2:7], 0 cbsz:2 blgp:2
	v_mfma_f32_16x16x128_f8f6f4 v[138:141], v[122:127], v[14:19], 0 cbsz:2 blgp:2
	v_mfma_f32_16x16x128_f8f6f4 v[142:145], v[122:127], v[26:31], v[188:191] cbsz:2 blgp:2
	v_mfma_f32_16x16x128_f8f6f4 v[204:207], v[122:127], v[38:43], 0 cbsz:2 blgp:2
	v_mfma_f32_16x16x128_f8f6f4 v[208:211], v[122:127], v[50:55], 0 cbsz:2 blgp:2
	v_mfma_f32_16x16x128_f8f6f4 v[212:215], v[122:127], v[62:67], v[188:191] cbsz:2 blgp:2
	s_waitcnt lgkmcnt(0)
	v_mfma_f32_16x16x128_f8f6f4 v[134:137], v[128:133], v[8:13], v[134:137] cbsz:2 blgp:2
	v_mfma_f32_16x16x128_f8f6f4 v[204:207], v[128:133], v[44:49], v[204:207] cbsz:2 blgp:2
	v_mfma_f32_16x16x128_f8f6f4 v[138:141], v[128:133], v[20:25], v[138:141] cbsz:2 blgp:2
	v_mfma_f32_16x16x128_f8f6f4 v[208:211], v[128:133], v[56:61], v[208:211] cbsz:2 blgp:2
	v_mfma_f32_16x16x128_f8f6f4 v[142:145], v[128:133], v[32:37], v[142:145] cbsz:2 blgp:2
	v_mfma_f32_16x16x128_f8f6f4 v[212:215], v[128:133], v[68:73], v[212:215] cbsz:2 blgp:2
	v_cndmask_b32_e64 v158, v134, v204, s[0:1]
	v_fma_mix_f32 v158, v158, v100, v147 op_sel_hi:[0,0,1]
	v_exp_f32_e32 v158, v158
	v_cndmask_b32_e64 v159, v138, v208, s[0:1]
	v_fma_mix_f32 v159, v159, v101, v151 op_sel_hi:[0,0,1]
	v_exp_f32_e32 v159, v159
	v_fma_f32 v158, v158, v186, v186
	v_rcp_f32_e32 v158, v158
	v_add_f32_e32 v159, 1.0, v159
	v_rcp_f32_e32 v159, v159
	v_cndmask_b32_e64 v160, v142, v212, s[0:1]
	v_fma_mix_f32 v161, v158, v160, v155 op_sel_hi:[0,0,1]
	v_exp_f32_e32 v161, v161
	s_add_u32 s48, s48, s40
	v_add_f32_e32 v161, 1.0, v161
	v_rcp_f32_e32 v161, v161
	s_addc_u32 s49, s49, s41
	v_fma_f32 v162, v161, -2.0, 1.0
	v_sub_f32_e32 v163, v176, v162
	v_fma_f32 v176, v159, v163, v162
	v_fma_f32 v164, |v176|, s17, v113
	v_fma_f32 v165, |v176|, s18, v114
	v_fma_f32 v166, |v176|, s19, v115
	v_lshrrev_b32_e32 v167, 26, v176
	v_min3_u32 v164, v164, v165, v166
	v_bfi_b32 v168, 31, v164, v167
	v_lshrrev_b32_e32 v169, v181, v168
	global_store_short_d16_hi v185, v176, s[48:49]
	v_mul_u32_u24_dpp v170, v168, v180 quad_perm:[1,2,3,3] row_mask:0xf bank_mask:0xf bound_ctrl:1
	v_or_b32_e32 v171, v169, v170
	ds_write_b8 v184, v171 offset:416
	s_waitcnt lgkmcnt(0)
	s_barrier
	ds_read_b64 v[122:123], v105 offset:416
	ds_read_b64 v[124:125], v105 offset:424
	ds_read_b64 v[126:127], v105 offset:432
	s_barrier
	ds_read_b64 v[128:129], v105 offset:512
	ds_read_b64 v[130:131], v105 offset:520
	ds_read_b64 v[132:133], v105 offset:528
	s_waitcnt lgkmcnt(3)
	v_mfma_f32_16x16x128_f8f6f4 v[134:137], v[122:127], v[2:7], 0 cbsz:2 blgp:2
	v_mfma_f32_16x16x128_f8f6f4 v[138:141], v[122:127], v[14:19], 0 cbsz:2 blgp:2
	v_mfma_f32_16x16x128_f8f6f4 v[142:145], v[122:127], v[26:31], v[188:191] cbsz:2 blgp:2
	v_mfma_f32_16x16x128_f8f6f4 v[204:207], v[122:127], v[38:43], 0 cbsz:2 blgp:2
	v_mfma_f32_16x16x128_f8f6f4 v[208:211], v[122:127], v[50:55], 0 cbsz:2 blgp:2
	v_mfma_f32_16x16x128_f8f6f4 v[212:215], v[122:127], v[62:67], v[188:191] cbsz:2 blgp:2
	s_waitcnt lgkmcnt(0)
	v_mfma_f32_16x16x128_f8f6f4 v[134:137], v[128:133], v[8:13], v[134:137] cbsz:2 blgp:2
	v_mfma_f32_16x16x128_f8f6f4 v[204:207], v[128:133], v[44:49], v[204:207] cbsz:2 blgp:2
	v_mfma_f32_16x16x128_f8f6f4 v[138:141], v[128:133], v[20:25], v[138:141] cbsz:2 blgp:2
	v_mfma_f32_16x16x128_f8f6f4 v[208:211], v[128:133], v[56:61], v[208:211] cbsz:2 blgp:2
	v_mfma_f32_16x16x128_f8f6f4 v[142:145], v[128:133], v[32:37], v[142:145] cbsz:2 blgp:2
	v_mfma_f32_16x16x128_f8f6f4 v[212:215], v[128:133], v[68:73], v[212:215] cbsz:2 blgp:2
	v_cndmask_b32_e64 v158, v134, v204, s[0:1]
	v_fma_mix_f32 v158, v158, v100, v147 op_sel:[0,0,1] op_sel_hi:[0,0,1]
	v_exp_f32_e32 v158, v158
	v_cndmask_b32_e64 v159, v138, v208, s[0:1]
	v_fma_mix_f32 v159, v159, v101, v151 op_sel:[0,0,1] op_sel_hi:[0,0,1]
	v_exp_f32_e32 v159, v159
	v_fma_f32 v158, v158, v186, v186
	v_rcp_f32_e32 v158, v158
	v_add_f32_e32 v159, 1.0, v159
	v_rcp_f32_e32 v159, v159
	v_cndmask_b32_e64 v160, v142, v212, s[0:1]
	v_fma_mix_f32 v161, v158, v160, v155 op_sel:[0,0,1] op_sel_hi:[0,0,1]
	v_exp_f32_e32 v161, v161
	s_add_u32 s48, s48, s40
	v_add_f32_e32 v161, 1.0, v161
	v_rcp_f32_e32 v161, v161
	s_addc_u32 s49, s49, s41
	v_fma_f32 v162, v161, -2.0, 1.0
	v_sub_f32_e32 v163, v176, v162
	v_fma_f32 v176, v159, v163, v162
	v_fma_f32 v164, |v176|, s17, v113
	v_fma_f32 v165, |v176|, s18, v114
	v_fma_f32 v166, |v176|, s19, v115
	v_lshrrev_b32_e32 v167, 26, v176
	v_min3_u32 v164, v164, v165, v166
	v_bfi_b32 v168, 31, v164, v167
	v_lshrrev_b32_e32 v169, v181, v168
	global_store_short_d16_hi v185, v176, s[48:49]
	v_mul_u32_u24_dpp v170, v168, v180 quad_perm:[1,2,3,3] row_mask:0xf bank_mask:0xf bound_ctrl:1
	v_or_b32_e32 v171, v169, v170
	ds_write_b8 v184, v171
	s_waitcnt lgkmcnt(0)
	s_barrier
	ds_read_b64 v[122:123], v105 offset:0
	ds_read_b64 v[124:125], v105 offset:8
	ds_read_b64 v[126:127], v105 offset:16
	s_barrier
	ds_read_b64 v[128:129], v105 offset:96
	ds_read_b64 v[130:131], v105 offset:104
	ds_read_b64 v[132:133], v105 offset:112
	s_waitcnt lgkmcnt(3)
	v_mfma_f32_16x16x128_f8f6f4 v[134:137], v[122:127], v[2:7], 0 cbsz:2 blgp:2
	v_mfma_f32_16x16x128_f8f6f4 v[138:141], v[122:127], v[14:19], 0 cbsz:2 blgp:2
	v_mfma_f32_16x16x128_f8f6f4 v[142:145], v[122:127], v[26:31], v[188:191] cbsz:2 blgp:2
	v_mfma_f32_16x16x128_f8f6f4 v[204:207], v[122:127], v[38:43], 0 cbsz:2 blgp:2
	v_mfma_f32_16x16x128_f8f6f4 v[208:211], v[122:127], v[50:55], 0 cbsz:2 blgp:2
	v_mfma_f32_16x16x128_f8f6f4 v[212:215], v[122:127], v[62:67], v[188:191] cbsz:2 blgp:2
	s_waitcnt lgkmcnt(0)
	v_mfma_f32_16x16x128_f8f6f4 v[134:137], v[128:133], v[8:13], v[134:137] cbsz:2 blgp:2
	v_mfma_f32_16x16x128_f8f6f4 v[204:207], v[128:133], v[44:49], v[204:207] cbsz:2 blgp:2
	v_mfma_f32_16x16x128_f8f6f4 v[138:141], v[128:133], v[20:25], v[138:141] cbsz:2 blgp:2
	v_mfma_f32_16x16x128_f8f6f4 v[208:211], v[128:133], v[56:61], v[208:211] cbsz:2 blgp:2
	v_mfma_f32_16x16x128_f8f6f4 v[142:145], v[128:133], v[32:37], v[142:145] cbsz:2 blgp:2
	v_mfma_f32_16x16x128_f8f6f4 v[212:215], v[128:133], v[68:73], v[212:215] cbsz:2 blgp:2
	v_cndmask_b32_e64 v158, v134, v204, s[0:1]
	v_fma_mix_f32 v158, v158, v100, v148 op_sel_hi:[0,0,1]
	v_exp_f32_e32 v158, v158
	v_cndmask_b32_e64 v159, v138, v208, s[0:1]
	v_fma_mix_f32 v159, v159, v101, v152 op_sel_hi:[0,0,1]
	v_exp_f32_e32 v159, v159
	v_fma_f32 v158, v158, v186, v186
	v_rcp_f32_e32 v158, v158
	v_add_f32_e32 v159, 1.0, v159
	v_rcp_f32_e32 v159, v159
	v_cndmask_b32_e64 v160, v142, v212, s[0:1]
	v_fma_mix_f32 v161, v158, v160, v156 op_sel_hi:[0,0,1]
	v_exp_f32_e32 v161, v161
	s_add_u32 s48, s48, s40
	v_add_f32_e32 v161, 1.0, v161
	v_rcp_f32_e32 v161, v161
	s_addc_u32 s49, s49, s41
	v_fma_f32 v162, v161, -2.0, 1.0
	v_sub_f32_e32 v163, v176, v162
	v_fma_f32 v176, v159, v163, v162
	v_fma_f32 v164, |v176|, s17, v113
	v_fma_f32 v165, |v176|, s18, v114
	v_fma_f32 v166, |v176|, s19, v115
	v_lshrrev_b32_e32 v167, 26, v176
	v_min3_u32 v164, v164, v165, v166
	v_bfi_b32 v168, 31, v164, v167
	v_lshrrev_b32_e32 v169, v181, v168
	global_store_short_d16_hi v185, v176, s[48:49]
	v_mul_u32_u24_dpp v170, v168, v180 quad_perm:[1,2,3,3] row_mask:0xf bank_mask:0xf bound_ctrl:1
	v_or_b32_e32 v171, v169, v170
	ds_write_b8 v184, v171 offset:416
	s_waitcnt lgkmcnt(0)
	s_barrier
	ds_read_b64 v[122:123], v105 offset:416
	ds_read_b64 v[124:125], v105 offset:424
	ds_read_b64 v[126:127], v105 offset:432
	s_barrier
	ds_read_b64 v[128:129], v105 offset:512
	ds_read_b64 v[130:131], v105 offset:520
	ds_read_b64 v[132:133], v105 offset:528
	s_waitcnt lgkmcnt(3)
	v_mfma_f32_16x16x128_f8f6f4 v[134:137], v[122:127], v[2:7], 0 cbsz:2 blgp:2
	v_mfma_f32_16x16x128_f8f6f4 v[138:141], v[122:127], v[14:19], 0 cbsz:2 blgp:2
	v_mfma_f32_16x16x128_f8f6f4 v[142:145], v[122:127], v[26:31], v[188:191] cbsz:2 blgp:2
	v_mfma_f32_16x16x128_f8f6f4 v[204:207], v[122:127], v[38:43], 0 cbsz:2 blgp:2
	v_mfma_f32_16x16x128_f8f6f4 v[208:211], v[122:127], v[50:55], 0 cbsz:2 blgp:2
	v_mfma_f32_16x16x128_f8f6f4 v[212:215], v[122:127], v[62:67], v[188:191] cbsz:2 blgp:2
	s_waitcnt lgkmcnt(0)
	v_mfma_f32_16x16x128_f8f6f4 v[134:137], v[128:133], v[8:13], v[134:137] cbsz:2 blgp:2
	v_mfma_f32_16x16x128_f8f6f4 v[204:207], v[128:133], v[44:49], v[204:207] cbsz:2 blgp:2
	v_mfma_f32_16x16x128_f8f6f4 v[138:141], v[128:133], v[20:25], v[138:141] cbsz:2 blgp:2
	v_mfma_f32_16x16x128_f8f6f4 v[208:211], v[128:133], v[56:61], v[208:211] cbsz:2 blgp:2
	v_mfma_f32_16x16x128_f8f6f4 v[142:145], v[128:133], v[32:37], v[142:145] cbsz:2 blgp:2
	v_mfma_f32_16x16x128_f8f6f4 v[212:215], v[128:133], v[68:73], v[212:215] cbsz:2 blgp:2
	v_cndmask_b32_e64 v158, v134, v204, s[0:1]
	v_fma_mix_f32 v158, v158, v100, v148 op_sel:[0,0,1] op_sel_hi:[0,0,1]
	v_exp_f32_e32 v158, v158
	v_cndmask_b32_e64 v159, v138, v208, s[0:1]
	v_fma_mix_f32 v159, v159, v101, v152 op_sel:[0,0,1] op_sel_hi:[0,0,1]
	v_exp_f32_e32 v159, v159
	v_fma_f32 v158, v158, v186, v186
	v_rcp_f32_e32 v158, v158
	v_add_f32_e32 v159, 1.0, v159
	v_rcp_f32_e32 v159, v159
	v_cndmask_b32_e64 v160, v142, v212, s[0:1]
	v_fma_mix_f32 v161, v158, v160, v156 op_sel:[0,0,1] op_sel_hi:[0,0,1]
	v_exp_f32_e32 v161, v161
	s_add_u32 s48, s48, s40
	v_add_f32_e32 v161, 1.0, v161
	v_rcp_f32_e32 v161, v161
	s_addc_u32 s49, s49, s41
	v_fma_f32 v162, v161, -2.0, 1.0
	v_sub_f32_e32 v163, v176, v162
	v_fma_f32 v176, v159, v163, v162
	v_fma_f32 v164, |v176|, s17, v113
	v_fma_f32 v165, |v176|, s18, v114
	v_fma_f32 v166, |v176|, s19, v115
	v_lshrrev_b32_e32 v167, 26, v176
	v_min3_u32 v164, v164, v165, v166
	v_bfi_b32 v168, 31, v164, v167
	v_lshrrev_b32_e32 v169, v181, v168
	global_store_short_d16_hi v185, v176, s[48:49]
	v_mul_u32_u24_dpp v170, v168, v180 quad_perm:[1,2,3,3] row_mask:0xf bank_mask:0xf bound_ctrl:1
	v_or_b32_e32 v171, v169, v170
	ds_write_b8 v184, v171
	s_waitcnt lgkmcnt(0)
	s_barrier
	ds_read_b64 v[122:123], v105 offset:0
	ds_read_b64 v[124:125], v105 offset:8
	ds_read_b64 v[126:127], v105 offset:16
	s_barrier
	ds_read_b64 v[128:129], v105 offset:96
	ds_read_b64 v[130:131], v105 offset:104
	ds_read_b64 v[132:133], v105 offset:112
	s_waitcnt lgkmcnt(3)
	v_mfma_f32_16x16x128_f8f6f4 v[134:137], v[122:127], v[2:7], 0 cbsz:2 blgp:2
	v_mfma_f32_16x16x128_f8f6f4 v[138:141], v[122:127], v[14:19], 0 cbsz:2 blgp:2
	v_mfma_f32_16x16x128_f8f6f4 v[142:145], v[122:127], v[26:31], v[188:191] cbsz:2 blgp:2
	v_mfma_f32_16x16x128_f8f6f4 v[204:207], v[122:127], v[38:43], 0 cbsz:2 blgp:2
	v_mfma_f32_16x16x128_f8f6f4 v[208:211], v[122:127], v[50:55], 0 cbsz:2 blgp:2
	v_mfma_f32_16x16x128_f8f6f4 v[212:215], v[122:127], v[62:67], v[188:191] cbsz:2 blgp:2
	s_waitcnt lgkmcnt(0)
	v_mfma_f32_16x16x128_f8f6f4 v[134:137], v[128:133], v[8:13], v[134:137] cbsz:2 blgp:2
	v_mfma_f32_16x16x128_f8f6f4 v[204:207], v[128:133], v[44:49], v[204:207] cbsz:2 blgp:2
	v_mfma_f32_16x16x128_f8f6f4 v[138:141], v[128:133], v[20:25], v[138:141] cbsz:2 blgp:2
	v_mfma_f32_16x16x128_f8f6f4 v[208:211], v[128:133], v[56:61], v[208:211] cbsz:2 blgp:2
	v_mfma_f32_16x16x128_f8f6f4 v[142:145], v[128:133], v[32:37], v[142:145] cbsz:2 blgp:2
	v_mfma_f32_16x16x128_f8f6f4 v[212:215], v[128:133], v[68:73], v[212:215] cbsz:2 blgp:2
	v_cndmask_b32_e64 v158, v134, v204, s[0:1]
	v_fma_mix_f32 v158, v158, v100, v149 op_sel_hi:[0,0,1]
	v_exp_f32_e32 v158, v158
	v_cndmask_b32_e64 v159, v138, v208, s[0:1]
	v_fma_mix_f32 v159, v159, v101, v153 op_sel_hi:[0,0,1]
	v_exp_f32_e32 v159, v159
	v_fma_f32 v158, v158, v186, v186
	v_rcp_f32_e32 v158, v158
	v_add_f32_e32 v159, 1.0, v159
	v_rcp_f32_e32 v159, v159
	v_cndmask_b32_e64 v160, v142, v212, s[0:1]
	v_fma_mix_f32 v161, v158, v160, v157 op_sel_hi:[0,0,1]
	v_exp_f32_e32 v161, v161
	s_add_u32 s48, s48, s40
	v_add_f32_e32 v161, 1.0, v161
	v_rcp_f32_e32 v161, v161
	s_addc_u32 s49, s49, s41
	v_fma_f32 v162, v161, -2.0, 1.0
	v_sub_f32_e32 v163, v176, v162
	v_fma_f32 v176, v159, v163, v162
	v_fma_f32 v164, |v176|, s17, v113
	v_fma_f32 v165, |v176|, s18, v114
	v_fma_f32 v166, |v176|, s19, v115
	v_lshrrev_b32_e32 v167, 26, v176
	v_min3_u32 v164, v164, v165, v166
	v_bfi_b32 v168, 31, v164, v167
	v_lshrrev_b32_e32 v169, v181, v168
	global_store_short_d16_hi v185, v176, s[48:49]
	v_mul_u32_u24_dpp v170, v168, v180 quad_perm:[1,2,3,3] row_mask:0xf bank_mask:0xf bound_ctrl:1
	v_or_b32_e32 v171, v169, v170
	ds_write_b8 v184, v171 offset:416
	s_waitcnt lgkmcnt(0)
	s_barrier
	ds_read_b64 v[122:123], v105 offset:416
	ds_read_b64 v[124:125], v105 offset:424
	ds_read_b64 v[126:127], v105 offset:432
	s_barrier
	ds_read_b64 v[128:129], v105 offset:512
	ds_read_b64 v[130:131], v105 offset:520
	ds_read_b64 v[132:133], v105 offset:528
	s_add_i32 s44, s44, 16
	s_waitcnt lgkmcnt(3)
	v_mfma_f32_16x16x128_f8f6f4 v[134:137], v[122:127], v[2:7], 0 cbsz:2 blgp:2
	v_mfma_f32_16x16x128_f8f6f4 v[138:141], v[122:127], v[14:19], 0 cbsz:2 blgp:2
	v_mfma_f32_16x16x128_f8f6f4 v[142:145], v[122:127], v[26:31], v[188:191] cbsz:2 blgp:2
	v_mfma_f32_16x16x128_f8f6f4 v[204:207], v[122:127], v[38:43], 0 cbsz:2 blgp:2
	v_mfma_f32_16x16x128_f8f6f4 v[208:211], v[122:127], v[50:55], 0 cbsz:2 blgp:2
	v_mfma_f32_16x16x128_f8f6f4 v[212:215], v[122:127], v[62:67], v[188:191] cbsz:2 blgp:2
	s_waitcnt lgkmcnt(0)
	v_mfma_f32_16x16x128_f8f6f4 v[134:137], v[128:133], v[8:13], v[134:137] cbsz:2 blgp:2
	v_mfma_f32_16x16x128_f8f6f4 v[204:207], v[128:133], v[44:49], v[204:207] cbsz:2 blgp:2
	v_mfma_f32_16x16x128_f8f6f4 v[138:141], v[128:133], v[20:25], v[138:141] cbsz:2 blgp:2
	v_mfma_f32_16x16x128_f8f6f4 v[208:211], v[128:133], v[56:61], v[208:211] cbsz:2 blgp:2
	v_mfma_f32_16x16x128_f8f6f4 v[142:145], v[128:133], v[32:37], v[142:145] cbsz:2 blgp:2
	v_mfma_f32_16x16x128_f8f6f4 v[212:215], v[128:133], v[68:73], v[212:215] cbsz:2 blgp:2
	v_cndmask_b32_e64 v158, v134, v204, s[0:1]
	v_fma_mix_f32 v158, v158, v100, v149 op_sel:[0,0,1] op_sel_hi:[0,0,1]
	v_exp_f32_e32 v158, v158
	v_cndmask_b32_e64 v159, v138, v208, s[0:1]
	v_fma_mix_f32 v159, v159, v101, v153 op_sel:[0,0,1] op_sel_hi:[0,0,1]
	v_exp_f32_e32 v159, v159
	v_fma_f32 v158, v158, v186, v186
	v_rcp_f32_e32 v158, v158
	v_add_f32_e32 v159, 1.0, v159
	v_rcp_f32_e32 v159, v159
	v_cndmask_b32_e64 v160, v142, v212, s[0:1]
	v_fma_mix_f32 v161, v158, v160, v157 op_sel:[0,0,1] op_sel_hi:[0,0,1]
	v_exp_f32_e32 v161, v161
	s_add_u32 s48, s48, s40
	v_add_f32_e32 v161, 1.0, v161
	v_rcp_f32_e32 v161, v161
	s_addc_u32 s49, s49, s41
	v_fma_f32 v162, v161, -2.0, 1.0
	v_sub_f32_e32 v163, v176, v162
	v_fma_f32 v176, v159, v163, v162
	v_fma_f32 v164, |v176|, s17, v113
	v_fma_f32 v165, |v176|, s18, v114
	v_fma_f32 v166, |v176|, s19, v115
	v_lshrrev_b32_e32 v167, 26, v176
	v_min3_u32 v164, v164, v165, v166
	v_bfi_b32 v168, 31, v164, v167
	v_lshrrev_b32_e32 v169, v181, v168
	global_store_short_d16_hi v185, v176, s[48:49]
	v_mul_u32_u24_dpp v170, v168, v180 quad_perm:[1,2,3,3] row_mask:0xf bank_mask:0xf bound_ctrl:1
	v_or_b32_e32 v171, v169, v170
	ds_write_b8 v184, v171
	s_waitcnt lgkmcnt(0)
	s_barrier
	ds_read_b64 v[122:123], v105 offset:0
	ds_read_b64 v[124:125], v105 offset:8
	ds_read_b64 v[126:127], v105 offset:16
	s_cmp_lt_i32 s44, s45
	s_barrier
	s_cbranch_scc1 .Lscan_loop_a_f2
	s_branch .Lscan_exit_f2
.Lscan_loop_b_f2:
	ds_read_b64 v[128:129], v105 offset:96
	ds_read_b64 v[130:131], v105 offset:104
	ds_read_b64 v[132:133], v105 offset:112
	s_waitcnt vmcnt(8)
	global_load_dwordx4 v[146:149], v[196:197], off
	global_load_dwordx4 v[150:153], v[196:197], off offset:512
	global_load_dwordx4 v[154:157], v[196:197], off offset:1024
	v_lshl_add_u64 v[196:197], v[196:197], 0, s[42:43]
	s_waitcnt lgkmcnt(3)
	v_mfma_f32_16x16x128_f8f6f4 v[134:137], v[122:127], v[2:7], 0 cbsz:2 blgp:2
	v_mfma_f32_16x16x128_f8f6f4 v[138:141], v[122:127], v[14:19], 0 cbsz:2 blgp:2
	v_mfma_f32_16x16x128_f8f6f4 v[142:145], v[122:127], v[26:31], v[188:191] cbsz:2 blgp:2
	v_mfma_f32_16x16x128_f8f6f4 v[204:207], v[122:127], v[38:43], 0 cbsz:2 blgp:2
	v_mfma_f32_16x16x128_f8f6f4 v[208:211], v[122:127], v[50:55], 0 cbsz:2 blgp:2
	v_mfma_f32_16x16x128_f8f6f4 v[212:215], v[122:127], v[62:67], v[188:191] cbsz:2 blgp:2
	s_waitcnt lgkmcnt(0)
	v_mfma_f32_16x16x128_f8f6f4 v[134:137], v[128:133], v[8:13], v[134:137] cbsz:2 blgp:2
	v_mfma_f32_16x16x128_f8f6f4 v[204:207], v[128:133], v[44:49], v[204:207] cbsz:2 blgp:2
	v_mfma_f32_16x16x128_f8f6f4 v[138:141], v[128:133], v[20:25], v[138:141] cbsz:2 blgp:2
	v_mfma_f32_16x16x128_f8f6f4 v[208:211], v[128:133], v[56:61], v[208:211] cbsz:2 blgp:2
	v_mfma_f32_16x16x128_f8f6f4 v[142:145], v[128:133], v[32:37], v[142:145] cbsz:2 blgp:2
	v_mfma_f32_16x16x128_f8f6f4 v[212:215], v[128:133], v[68:73], v[212:215] cbsz:2 blgp:2
	v_cndmask_b32_e64 v158, v134, v204, s[0:1]
	v_fma_mix_f32 v158, v158, v100, v82 op_sel_hi:[0,0,1]
	v_exp_f32_e32 v158, v158
	v_cndmask_b32_e64 v159, v138, v208, s[0:1]
	v_fma_mix_f32 v159, v159, v101, v74 op_sel_hi:[0,0,1]
	v_exp_f32_e32 v159, v159
	v_fma_f32 v158, v158, v186, v186
	v_rcp_f32_e32 v158, v158
	v_add_f32_e32 v159, 1.0, v159
	v_rcp_f32_e32 v159, v159
	v_cndmask_b32_e64 v160, v142, v212, s[0:1]
	v_fma_mix_f32 v161, v158, v160, v78 op_sel_hi:[0,0,1]
	v_exp_f32_e32 v161, v161
	s_add_u32 s48, s48, s40
	v_add_f32_e32 v161, 1.0, v161
	v_rcp_f32_e32 v161, v161
	s_addc_u32 s49, s49, s41
	v_fma_f32 v162, v161, -2.0, 1.0
	v_sub_f32_e32 v163, v176, v162
	v_fma_f32 v176, v159, v163, v162
	v_fma_f32 v164, |v176|, s17, v113
	v_fma_f32 v165, |v176|, s18, v114
	v_fma_f32 v166, |v176|, s19, v115
	v_lshrrev_b32_e32 v167, 26, v176
	v_min3_u32 v164, v164, v165, v166
	v_bfi_b32 v168, 31, v164, v167
	v_lshrrev_b32_e32 v169, v181, v168
	global_store_short_d16_hi v185, v176, s[48:49]
	v_mul_u32_u24_dpp v170, v168, v180 quad_perm:[1,2,3,3] row_mask:0xf bank_mask:0xf bound_ctrl:1
	v_or_b32_e32 v171, v169, v170
	ds_write_b8 v184, v171 offset:416
	s_barrier
	ds_read_b64 v[122:123], v105 offset:416
	ds_read_b64 v[124:125], v105 offset:424
	ds_read_b64 v[126:127], v105 offset:432
	s_waitcnt lgkmcnt(3)
	s_barrier
	ds_read_b64 v[128:129], v105 offset:512
	ds_read_b64 v[130:131], v105 offset:520
	ds_read_b64 v[132:133], v105 offset:528
	s_waitcnt lgkmcnt(3)
	v_mfma_f32_16x16x128_f8f6f4 v[134:137], v[122:127], v[2:7], 0 cbsz:2 blgp:2
	v_mfma_f32_16x16x128_f8f6f4 v[138:141], v[122:127], v[14:19], 0 cbsz:2 blgp:2
	v_mfma_f32_16x16x128_f8f6f4 v[142:145], v[122:127], v[26:31], v[188:191] cbsz:2 blgp:2
	v_mfma_f32_16x16x128_f8f6f4 v[204:207], v[122:127], v[38:43], 0 cbsz:2 blgp:2
	v_mfma_f32_16x16x128_f8f6f4 v[208:211], v[122:127], v[50:55], 0 cbsz:2 blgp:2
	v_mfma_f32_16x16x128_f8f6f4 v[212:215], v[122:127], v[62:67], v[188:191] cbsz:2 blgp:2
	s_waitcnt lgkmcnt(0)
	v_mfma_f32_16x16x128_f8f6f4 v[134:137], v[128:133], v[8:13], v[134:137] cbsz:2 blgp:2
	v_mfma_f32_16x16x128_f8f6f4 v[204:207], v[128:133], v[44:49], v[204:207] cbsz:2 blgp:2
	v_mfma_f32_16x16x128_f8f6f4 v[138:141], v[128:133], v[20:25], v[138:141] cbsz:2 blgp:2
	v_mfma_f32_16x16x128_f8f6f4 v[208:211], v[128:133], v[56:61], v[208:211] cbsz:2 blgp:2
	v_mfma_f32_16x16x128_f8f6f4 v[142:145], v[128:133], v[32:37], v[142:145] cbsz:2 blgp:2
	v_mfma_f32_16x16x128_f8f6f4 v[212:215], v[128:133], v[68:73], v[212:215] cbsz:2 blgp:2
	v_cndmask_b32_e64 v158, v134, v204, s[0:1]
	v_fma_mix_f32 v158, v158, v100, v82 op_sel:[0,0,1] op_sel_hi:[0,0,1]
	v_exp_f32_e32 v158, v158
	v_cndmask_b32_e64 v159, v138, v208, s[0:1]
	v_fma_mix_f32 v159, v159, v101, v74 op_sel:[0,0,1] op_sel_hi:[0,0,1]
	v_exp_f32_e32 v159, v159
	v_fma_f32 v158, v158, v186, v186
	v_rcp_f32_e32 v158, v158
	v_add_f32_e32 v159, 1.0, v159
	v_rcp_f32_e32 v159, v159
	v_cndmask_b32_e64 v160, v142, v212, s[0:1]
	v_fma_mix_f32 v161, v158, v160, v78 op_sel:[0,0,1] op_sel_hi:[0,0,1]
	v_exp_f32_e32 v161, v161
	s_add_u32 s48, s48, s40
	v_add_f32_e32 v161, 1.0, v161
	v_rcp_f32_e32 v161, v161
	s_addc_u32 s49, s49, s41
	v_fma_f32 v162, v161, -2.0, 1.0
	v_sub_f32_e32 v163, v176, v162
	v_fma_f32 v176, v159, v163, v162
	v_fma_f32 v164, |v176|, s17, v113
	v_fma_f32 v165, |v176|, s18, v114
	v_fma_f32 v166, |v176|, s19, v115
	v_lshrrev_b32_e32 v167, 26, v176
	v_min3_u32 v164, v164, v165, v166
	v_bfi_b32 v168, 31, v164, v167
	v_lshrrev_b32_e32 v169, v181, v168
	global_store_short_d16_hi v185, v176, s[48:49]
	v_mul_u32_u24_dpp v170, v168, v180 quad_perm:[1,2,3,3] row_mask:0xf bank_mask:0xf bound_ctrl:1
	v_or_b32_e32 v171, v169, v170
	ds_write_b8 v184, v171
	s_barrier
	ds_read_b64 v[122:123], v105 offset:0
	ds_read_b64 v[124:125], v105 offset:8
	ds_read_b64 v[126:127], v105 offset:16
	s_waitcnt lgkmcnt(3)
	s_barrier
	ds_read_b64 v[128:129], v105 offset:96
	ds_read_b64 v[130:131], v105 offset:104
	ds_read_b64 v[132:133], v105 offset:112
	s_waitcnt lgkmcnt(3)
	v_mfma_f32_16x16x128_f8f6f4 v[134:137], v[122:127], v[2:7], 0 cbsz:2 blgp:2
	v_mfma_f32_16x16x128_f8f6f4 v[138:141], v[122:127], v[14:19], 0 cbsz:2 blgp:2
	v_mfma_f32_16x16x128_f8f6f4 v[142:145], v[122:127], v[26:31], v[188:191] cbsz:2 blgp:2
	v_mfma_f32_16x16x128_f8f6f4 v[204:207], v[122:127], v[38:43], 0 cbsz:2 blgp:2
	v_mfma_f32_16x16x128_f8f6f4 v[208:211], v[122:127], v[50:55], 0 cbsz:2 blgp:2
	v_mfma_f32_16x16x128_f8f6f4 v[212:215], v[122:127], v[62:67], v[188:191] cbsz:2 blgp:2
	s_waitcnt lgkmcnt(0)
	v_mfma_f32_16x16x128_f8f6f4 v[134:137], v[128:133], v[8:13], v[134:137] cbsz:2 blgp:2
	v_mfma_f32_16x16x128_f8f6f4 v[204:207], v[128:133], v[44:49], v[204:207] cbsz:2 blgp:2
	v_mfma_f32_16x16x128_f8f6f4 v[138:141], v[128:133], v[20:25], v[138:141] cbsz:2 blgp:2
	v_mfma_f32_16x16x128_f8f6f4 v[208:211], v[128:133], v[56:61], v[208:211] cbsz:2 blgp:2
	v_mfma_f32_16x16x128_f8f6f4 v[142:145], v[128:133], v[32:37], v[142:145] cbsz:2 blgp:2
	v_mfma_f32_16x16x128_f8f6f4 v[212:215], v[128:133], v[68:73], v[212:215] cbsz:2 blgp:2
	v_cndmask_b32_e64 v158, v134, v204, s[0:1]
	v_fma_mix_f32 v158, v158, v100, v83 op_sel_hi:[0,0,1]
	v_exp_f32_e32 v158, v158
	v_cndmask_b32_e64 v159, v138, v208, s[0:1]
	v_fma_mix_f32 v159, v159, v101, v75 op_sel_hi:[0,0,1]
	v_exp_f32_e32 v159, v159
	v_fma_f32 v158, v158, v186, v186
	v_rcp_f32_e32 v158, v158
	v_add_f32_e32 v159, 1.0, v159
	v_rcp_f32_e32 v159, v159
	v_cndmask_b32_e64 v160, v142, v212, s[0:1]
	v_fma_mix_f32 v161, v158, v160, v79 op_sel_hi:[0,0,1]
	v_exp_f32_e32 v161, v161
	s_add_u32 s48, s48, s40
	v_add_f32_e32 v161, 1.0, v161
	v_rcp_f32_e32 v161, v161
	s_addc_u32 s49, s49, s41
	v_fma_f32 v162, v161, -2.0, 1.0
	v_sub_f32_e32 v163, v176, v162
	v_fma_f32 v176, v159, v163, v162
	v_fma_f32 v164, |v176|, s17, v113
	v_fma_f32 v165, |v176|, s18, v114
	v_fma_f32 v166, |v176|, s19, v115
	v_lshrrev_b32_e32 v167, 26, v176
	v_min3_u32 v164, v164, v165, v166
	v_bfi_b32 v168, 31, v164, v167
	v_lshrrev_b32_e32 v169, v181, v168
	global_store_short_d16_hi v185, v176, s[48:49]
	v_mul_u32_u24_dpp v170, v168, v180 quad_perm:[1,2,3,3] row_mask:0xf bank_mask:0xf bound_ctrl:1
	v_or_b32_e32 v171, v169, v170
	ds_write_b8 v184, v171 offset:416
	s_barrier
	ds_read_b64 v[122:123], v105 offset:416
	ds_read_b64 v[124:125], v105 offset:424
	ds_read_b64 v[126:127], v105 offset:432
	s_waitcnt lgkmcnt(3)
	s_barrier
	ds_read_b64 v[128:129], v105 offset:512
	ds_read_b64 v[130:131], v105 offset:520
	ds_read_b64 v[132:133], v105 offset:528
	s_waitcnt lgkmcnt(3)
	v_mfma_f32_16x16x128_f8f6f4 v[134:137], v[122:127], v[2:7], 0 cbsz:2 blgp:2
	v_mfma_f32_16x16x128_f8f6f4 v[138:141], v[122:127], v[14:19], 0 cbsz:2 blgp:2
	v_mfma_f32_16x16x128_f8f6f4 v[142:145], v[122:127], v[26:31], v[188:191] cbsz:2 blgp:2
	v_mfma_f32_16x16x128_f8f6f4 v[204:207], v[122:127], v[38:43], 0 cbsz:2 blgp:2
	v_mfma_f32_16x16x128_f8f6f4 v[208:211], v[122:127], v[50:55], 0 cbsz:2 blgp:2
	v_mfma_f32_16x16x128_f8f6f4 v[212:215], v[122:127], v[62:67], v[188:191] cbsz:2 blgp:2
	s_waitcnt lgkmcnt(0)
	v_mfma_f32_16x16x128_f8f6f4 v[134:137], v[128:133], v[8:13], v[134:137] cbsz:2 blgp:2
	v_mfma_f32_16x16x128_f8f6f4 v[204:207], v[128:133], v[44:49], v[204:207] cbsz:2 blgp:2
	v_mfma_f32_16x16x128_f8f6f4 v[138:141], v[128:133], v[20:25], v[138:141] cbsz:2 blgp:2
	v_mfma_f32_16x16x128_f8f6f4 v[208:211], v[128:133], v[56:61], v[208:211] cbsz:2 blgp:2
	v_mfma_f32_16x16x128_f8f6f4 v[142:145], v[128:133], v[32:37], v[142:145] cbsz:2 blgp:2
	v_mfma_f32_16x16x128_f8f6f4 v[212:215], v[128:133], v[68:73], v[212:215] cbsz:2 blgp:2
	v_cndmask_b32_e64 v158, v134, v204, s[0:1]
	v_fma_mix_f32 v158, v158, v100, v83 op_sel:[0,0,1] op_sel_hi:[0,0,1]
	v_exp_f32_e32 v158, v158
	v_cndmask_b32_e64 v159, v138, v208, s[0:1]
	v_fma_mix_f32 v159, v159, v101, v75 op_sel:[0,0,1] op_sel_hi:[0,0,1]
	v_exp_f32_e32 v159, v159
	v_fma_f32 v158, v158, v186, v186
	v_rcp_f32_e32 v158, v158
	v_add_f32_e32 v159, 1.0, v159
	v_rcp_f32_e32 v159, v159
	v_cndmask_b32_e64 v160, v142, v212, s[0:1]
	v_fma_mix_f32 v161, v158, v160, v79 op_sel:[0,0,1] op_sel_hi:[0,0,1]
	v_exp_f32_e32 v161, v161
	s_add_u32 s48, s48, s40
	v_add_f32_e32 v161, 1.0, v161
	v_rcp_f32_e32 v161, v161
	s_addc_u32 s49, s49, s41
	v_fma_f32 v162, v161, -2.0, 1.0
	v_sub_f32_e32 v163, v176, v162
	v_fma_f32 v176, v159, v163, v162
	v_fma_f32 v164, |v176|, s17, v113
	v_fma_f32 v165, |v176|, s18, v114
	v_fma_f32 v166, |v176|, s19, v115
	v_lshrrev_b32_e32 v167, 26, v176
	v_min3_u32 v164, v164, v165, v166
	v_bfi_b32 v168, 31, v164, v167
	v_lshrrev_b32_e32 v169, v181, v168
	global_store_short_d16_hi v185, v176, s[48:49]
	v_mul_u32_u24_dpp v170, v168, v180 quad_perm:[1,2,3,3] row_mask:0xf bank_mask:0xf bound_ctrl:1
	v_or_b32_e32 v171, v169, v170
	ds_write_b8 v184, v171
	s_barrier
	ds_read_b64 v[122:123], v105 offset:0
	ds_read_b64 v[124:125], v105 offset:8
	ds_read_b64 v[126:127], v105 offset:16
	s_waitcnt lgkmcnt(3)
	s_barrier
	ds_read_b64 v[128:129], v105 offset:96
	ds_read_b64 v[130:131], v105 offset:104
	ds_read_b64 v[132:133], v105 offset:112
	s_waitcnt lgkmcnt(3)
	v_mfma_f32_16x16x128_f8f6f4 v[134:137], v[122:127], v[2:7], 0 cbsz:2 blgp:2
	v_mfma_f32_16x16x128_f8f6f4 v[138:141], v[122:127], v[14:19], 0 cbsz:2 blgp:2
	v_mfma_f32_16x16x128_f8f6f4 v[142:145], v[122:127], v[26:31], v[188:191] cbsz:2 blgp:2
	v_mfma_f32_16x16x128_f8f6f4 v[204:207], v[122:127], v[38:43], 0 cbsz:2 blgp:2
	v_mfma_f32_16x16x128_f8f6f4 v[208:211], v[122:127], v[50:55], 0 cbsz:2 blgp:2
	v_mfma_f32_16x16x128_f8f6f4 v[212:215], v[122:127], v[62:67], v[188:191] cbsz:2 blgp:2
	s_waitcnt lgkmcnt(0)
	v_mfma_f32_16x16x128_f8f6f4 v[134:137], v[128:133], v[8:13], v[134:137] cbsz:2 blgp:2
	v_mfma_f32_16x16x128_f8f6f4 v[204:207], v[128:133], v[44:49], v[204:207] cbsz:2 blgp:2
	v_mfma_f32_16x16x128_f8f6f4 v[138:141], v[128:133], v[20:25], v[138:141] cbsz:2 blgp:2
	v_mfma_f32_16x16x128_f8f6f4 v[208:211], v[128:133], v[56:61], v[208:211] cbsz:2 blgp:2
	v_mfma_f32_16x16x128_f8f6f4 v[142:145], v[128:133], v[32:37], v[142:145] cbsz:2 blgp:2
	v_mfma_f32_16x16x128_f8f6f4 v[212:215], v[128:133], v[68:73], v[212:215] cbsz:2 blgp:2
	v_cndmask_b32_e64 v158, v134, v204, s[0:1]
	v_fma_mix_f32 v158, v158, v100, v84 op_sel_hi:[0,0,1]
	v_exp_f32_e32 v158, v158
	v_cndmask_b32_e64 v159, v138, v208, s[0:1]
	v_fma_mix_f32 v159, v159, v101, v76 op_sel_hi:[0,0,1]
	v_exp_f32_e32 v159, v159
	v_fma_f32 v158, v158, v186, v186
	v_rcp_f32_e32 v158, v158
	v_add_f32_e32 v159, 1.0, v159
	v_rcp_f32_e32 v159, v159
	v_cndmask_b32_e64 v160, v142, v212, s[0:1]
	v_fma_mix_f32 v161, v158, v160, v80 op_sel_hi:[0,0,1]
	v_exp_f32_e32 v161, v161
	s_add_u32 s48, s48, s40
	v_add_f32_e32 v161, 1.0, v161
	v_rcp_f32_e32 v161, v161
	s_addc_u32 s49, s49, s41
	v_fma_f32 v162, v161, -2.0, 1.0
	v_sub_f32_e32 v163, v176, v162
	v_fma_f32 v176, v159, v163, v162
	v_fma_f32 v164, |v176|, s17, v113
	v_fma_f32 v165, |v176|, s18, v114
	v_fma_f32 v166, |v176|, s19, v115
	v_lshrrev_b32_e32 v167, 26, v176
	v_min3_u32 v164, v164, v165, v166
	v_bfi_b32 v168, 31, v164, v167
	v_lshrrev_b32_e32 v169, v181, v168
	global_store_short_d16_hi v185, v176, s[48:49]
	v_mul_u32_u24_dpp v170, v168, v180 quad_perm:[1,2,3,3] row_mask:0xf bank_mask:0xf bound_ctrl:1
	v_or_b32_e32 v171, v169, v170
	ds_write_b8 v184, v171 offset:416
	s_barrier
	ds_read_b64 v[122:123], v105 offset:416
	ds_read_b64 v[124:125], v105 offset:424
	ds_read_b64 v[126:127], v105 offset:432
	s_waitcnt lgkmcnt(3)
	s_barrier
	ds_read_b64 v[128:129], v105 offset:512
	ds_read_b64 v[130:131], v105 offset:520
	ds_read_b64 v[132:133], v105 offset:528
	s_waitcnt lgkmcnt(3)
	v_mfma_f32_16x16x128_f8f6f4 v[134:137], v[122:127], v[2:7], 0 cbsz:2 blgp:2
	v_mfma_f32_16x16x128_f8f6f4 v[138:141], v[122:127], v[14:19], 0 cbsz:2 blgp:2
	v_mfma_f32_16x16x128_f8f6f4 v[142:145], v[122:127], v[26:31], v[188:191] cbsz:2 blgp:2
	v_mfma_f32_16x16x128_f8f6f4 v[204:207], v[122:127], v[38:43], 0 cbsz:2 blgp:2
	v_mfma_f32_16x16x128_f8f6f4 v[208:211], v[122:127], v[50:55], 0 cbsz:2 blgp:2
	v_mfma_f32_16x16x128_f8f6f4 v[212:215], v[122:127], v[62:67], v[188:191] cbsz:2 blgp:2
	s_waitcnt lgkmcnt(0)
	v_mfma_f32_16x16x128_f8f6f4 v[134:137], v[128:133], v[8:13], v[134:137] cbsz:2 blgp:2
	v_mfma_f32_16x16x128_f8f6f4 v[204:207], v[128:133], v[44:49], v[204:207] cbsz:2 blgp:2
	v_mfma_f32_16x16x128_f8f6f4 v[138:141], v[128:133], v[20:25], v[138:141] cbsz:2 blgp:2
	v_mfma_f32_16x16x128_f8f6f4 v[208:211], v[128:133], v[56:61], v[208:211] cbsz:2 blgp:2
	v_mfma_f32_16x16x128_f8f6f4 v[142:145], v[128:133], v[32:37], v[142:145] cbsz:2 blgp:2
	v_mfma_f32_16x16x128_f8f6f4 v[212:215], v[128:133], v[68:73], v[212:215] cbsz:2 blgp:2
	v_cndmask_b32_e64 v158, v134, v204, s[0:1]
	v_fma_mix_f32 v158, v158, v100, v84 op_sel:[0,0,1] op_sel_hi:[0,0,1]
	v_exp_f32_e32 v158, v158
	v_cndmask_b32_e64 v159, v138, v208, s[0:1]
	v_fma_mix_f32 v159, v159, v101, v76 op_sel:[0,0,1] op_sel_hi:[0,0,1]
	v_exp_f32_e32 v159, v159
	v_fma_f32 v158, v158, v186, v186
	v_rcp_f32_e32 v158, v158
	v_add_f32_e32 v159, 1.0, v159
	v_rcp_f32_e32 v159, v159
	v_cndmask_b32_e64 v160, v142, v212, s[0:1]
	v_fma_mix_f32 v161, v158, v160, v80 op_sel:[0,0,1] op_sel_hi:[0,0,1]
	v_exp_f32_e32 v161, v161
	s_add_u32 s48, s48, s40
	v_add_f32_e32 v161, 1.0, v161
	v_rcp_f32_e32 v161, v161
	s_addc_u32 s49, s49, s41
	v_fma_f32 v162, v161, -2.0, 1.0
	v_sub_f32_e32 v163, v176, v162
	v_fma_f32 v176, v159, v163, v162
	v_fma_f32 v164, |v176|, s17, v113
	v_fma_f32 v165, |v176|, s18, v114
	v_fma_f32 v166, |v176|, s19, v115
	v_lshrrev_b32_e32 v167, 26, v176
	v_min3_u32 v164, v164, v165, v166
	v_bfi_b32 v168, 31, v164, v167
	v_lshrrev_b32_e32 v169, v181, v168
	global_store_short_d16_hi v185, v176, s[48:49]
	v_mul_u32_u24_dpp v170, v168, v180 quad_perm:[1,2,3,3] row_mask:0xf bank_mask:0xf bound_ctrl:1
	v_or_b32_e32 v171, v169, v170
	ds_write_b8 v184, v171
	s_barrier
	ds_read_b64 v[122:123], v105 offset:0
	ds_read_b64 v[124:125], v105 offset:8
	ds_read_b64 v[126:127], v105 offset:16
	s_waitcnt lgkmcnt(3)
	s_barrier
	ds_read_b64 v[128:129], v105 offset:96
	ds_read_b64 v[130:131], v105 offset:104
	ds_read_b64 v[132:133], v105 offset:112
	s_waitcnt lgkmcnt(3)
	v_mfma_f32_16x16x128_f8f6f4 v[134:137], v[122:127], v[2:7], 0 cbsz:2 blgp:2
	v_mfma_f32_16x16x128_f8f6f4 v[138:141], v[122:127], v[14:19], 0 cbsz:2 blgp:2
	v_mfma_f32_16x16x128_f8f6f4 v[142:145], v[122:127], v[26:31], v[188:191] cbsz:2 blgp:2
	v_mfma_f32_16x16x128_f8f6f4 v[204:207], v[122:127], v[38:43], 0 cbsz:2 blgp:2
	v_mfma_f32_16x16x128_f8f6f4 v[208:211], v[122:127], v[50:55], 0 cbsz:2 blgp:2
	v_mfma_f32_16x16x128_f8f6f4 v[212:215], v[122:127], v[62:67], v[188:191] cbsz:2 blgp:2
	s_waitcnt lgkmcnt(0)
	v_mfma_f32_16x16x128_f8f6f4 v[134:137], v[128:133], v[8:13], v[134:137] cbsz:2 blgp:2
	v_mfma_f32_16x16x128_f8f6f4 v[204:207], v[128:133], v[44:49], v[204:207] cbsz:2 blgp:2
	v_mfma_f32_16x16x128_f8f6f4 v[138:141], v[128:133], v[20:25], v[138:141] cbsz:2 blgp:2
	v_mfma_f32_16x16x128_f8f6f4 v[208:211], v[128:133], v[56:61], v[208:211] cbsz:2 blgp:2
	v_mfma_f32_16x16x128_f8f6f4 v[142:145], v[128:133], v[32:37], v[142:145] cbsz:2 blgp:2
	v_mfma_f32_16x16x128_f8f6f4 v[212:215], v[128:133], v[68:73], v[212:215] cbsz:2 blgp:2
	v_cndmask_b32_e64 v158, v134, v204, s[0:1]
	v_fma_mix_f32 v158, v158, v100, v85 op_sel_hi:[0,0,1]
	v_exp_f32_e32 v158, v158
	v_cndmask_b32_e64 v159, v138, v208, s[0:1]
	v_fma_mix_f32 v159, v159, v101, v77 op_sel_hi:[0,0,1]
	v_exp_f32_e32 v159, v159
	v_fma_f32 v158, v158, v186, v186
	v_rcp_f32_e32 v158, v158
	v_add_f32_e32 v159, 1.0, v159
	v_rcp_f32_e32 v159, v159
	v_cndmask_b32_e64 v160, v142, v212, s[0:1]
	v_fma_mix_f32 v161, v158, v160, v81 op_sel_hi:[0,0,1]
	v_exp_f32_e32 v161, v161
	s_add_u32 s48, s48, s40
	v_add_f32_e32 v161, 1.0, v161
	v_rcp_f32_e32 v161, v161
	s_addc_u32 s49, s49, s41
	v_fma_f32 v162, v161, -2.0, 1.0
	v_sub_f32_e32 v163, v176, v162
	v_fma_f32 v176, v159, v163, v162
	v_fma_f32 v164, |v176|, s17, v113
	v_fma_f32 v165, |v176|, s18, v114
	v_fma_f32 v166, |v176|, s19, v115
	v_lshrrev_b32_e32 v167, 26, v176
	v_min3_u32 v164, v164, v165, v166
	v_bfi_b32 v168, 31, v164, v167
	v_lshrrev_b32_e32 v169, v181, v168
	global_store_short_d16_hi v185, v176, s[48:49]
	v_mul_u32_u24_dpp v170, v168, v180 quad_perm:[1,2,3,3] row_mask:0xf bank_mask:0xf bound_ctrl:1
	v_or_b32_e32 v171, v169, v170
	ds_write_b8 v184, v171 offset:416
	s_barrier
	ds_read_b64 v[122:123], v105 offset:416
	ds_read_b64 v[124:125], v105 offset:424
	ds_read_b64 v[126:127], v105 offset:432
	s_waitcnt lgkmcnt(3)
	s_barrier
	ds_read_b64 v[128:129], v105 offset:512
	ds_read_b64 v[130:131], v105 offset:520
	ds_read_b64 v[132:133], v105 offset:528
	s_waitcnt lgkmcnt(3)
	v_mfma_f32_16x16x128_f8f6f4 v[134:137], v[122:127], v[2:7], 0 cbsz:2 blgp:2
	v_mfma_f32_16x16x128_f8f6f4 v[138:141], v[122:127], v[14:19], 0 cbsz:2 blgp:2
	v_mfma_f32_16x16x128_f8f6f4 v[142:145], v[122:127], v[26:31], v[188:191] cbsz:2 blgp:2
	v_mfma_f32_16x16x128_f8f6f4 v[204:207], v[122:127], v[38:43], 0 cbsz:2 blgp:2
	v_mfma_f32_16x16x128_f8f6f4 v[208:211], v[122:127], v[50:55], 0 cbsz:2 blgp:2
	v_mfma_f32_16x16x128_f8f6f4 v[212:215], v[122:127], v[62:67], v[188:191] cbsz:2 blgp:2
	s_waitcnt lgkmcnt(0)
	v_mfma_f32_16x16x128_f8f6f4 v[134:137], v[128:133], v[8:13], v[134:137] cbsz:2 blgp:2
	v_mfma_f32_16x16x128_f8f6f4 v[204:207], v[128:133], v[44:49], v[204:207] cbsz:2 blgp:2
	v_mfma_f32_16x16x128_f8f6f4 v[138:141], v[128:133], v[20:25], v[138:141] cbsz:2 blgp:2
	v_mfma_f32_16x16x128_f8f6f4 v[208:211], v[128:133], v[56:61], v[208:211] cbsz:2 blgp:2
	v_mfma_f32_16x16x128_f8f6f4 v[142:145], v[128:133], v[32:37], v[142:145] cbsz:2 blgp:2
	v_mfma_f32_16x16x128_f8f6f4 v[212:215], v[128:133], v[68:73], v[212:215] cbsz:2 blgp:2
	v_cndmask_b32_e64 v158, v134, v204, s[0:1]
	v_fma_mix_f32 v158, v158, v100, v85 op_sel:[0,0,1] op_sel_hi:[0,0,1]
	v_exp_f32_e32 v158, v158
	v_cndmask_b32_e64 v159, v138, v208, s[0:1]
	v_fma_mix_f32 v159, v159, v101, v77 op_sel:[0,0,1] op_sel_hi:[0,0,1]
	v_exp_f32_e32 v159, v159
	v_fma_f32 v158, v158, v186, v186
	v_rcp_f32_e32 v158, v158
	v_add_f32_e32 v159, 1.0, v159
	v_rcp_f32_e32 v159, v159
	v_cndmask_b32_e64 v160, v142, v212, s[0:1]
	v_fma_mix_f32 v161, v158, v160, v81 op_sel:[0,0,1] op_sel_hi:[0,0,1]
	v_exp_f32_e32 v161, v161
	s_add_u32 s48, s48, s40
	v_add_f32_e32 v161, 1.0, v161
	v_rcp_f32_e32 v161, v161
	s_addc_u32 s49, s49, s41
	v_fma_f32 v162, v161, -2.0, 1.0
	v_sub_f32_e32 v163, v176, v162
	v_fma_f32 v176, v159, v163, v162
	v_fma_f32 v164, |v176|, s17, v113
	v_fma_f32 v165, |v176|, s18, v114
	v_fma_f32 v166, |v176|, s19, v115
	v_lshrrev_b32_e32 v167, 26, v176
	v_min3_u32 v164, v164, v165, v166
	v_bfi_b32 v168, 31, v164, v167
	v_lshrrev_b32_e32 v169, v181, v168
	global_store_short_d16_hi v185, v176, s[48:49]
	v_mul_u32_u24_dpp v170, v168, v180 quad_perm:[1,2,3,3] row_mask:0xf bank_mask:0xf bound_ctrl:1
	v_or_b32_e32 v171, v169, v170
	ds_write_b8 v184, v171
	s_barrier
	ds_read_b64 v[122:123], v105 offset:0
	ds_read_b64 v[124:125], v105 offset:8
	ds_read_b64 v[126:127], v105 offset:16
	s_waitcnt lgkmcnt(3)
	s_barrier
	ds_read_b64 v[128:129], v105 offset:96
	ds_read_b64 v[130:131], v105 offset:104
	ds_read_b64 v[132:133], v105 offset:112
	s_waitcnt vmcnt(8)
	global_load_dwordx4 v[82:85], v[196:197], off
	global_load_dwordx4 v[74:77], v[196:197], off offset:512
	global_load_dwordx4 v[78:81], v[196:197], off offset:1024
	v_lshl_add_u64 v[196:197], v[196:197], 0, s[42:43]
	s_waitcnt lgkmcnt(3)
	v_mfma_f32_16x16x128_f8f6f4 v[134:137], v[122:127], v[2:7], 0 cbsz:2 blgp:2
	v_mfma_f32_16x16x128_f8f6f4 v[138:141], v[122:127], v[14:19], 0 cbsz:2 blgp:2
	v_mfma_f32_16x16x128_f8f6f4 v[142:145], v[122:127], v[26:31], v[188:191] cbsz:2 blgp:2
	v_mfma_f32_16x16x128_f8f6f4 v[204:207], v[122:127], v[38:43], 0 cbsz:2 blgp:2
	v_mfma_f32_16x16x128_f8f6f4 v[208:211], v[122:127], v[50:55], 0 cbsz:2 blgp:2
	v_mfma_f32_16x16x128_f8f6f4 v[212:215], v[122:127], v[62:67], v[188:191] cbsz:2 blgp:2
	s_waitcnt lgkmcnt(0)
	v_mfma_f32_16x16x128_f8f6f4 v[134:137], v[128:133], v[8:13], v[134:137] cbsz:2 blgp:2
	v_mfma_f32_16x16x128_f8f6f4 v[204:207], v[128:133], v[44:49], v[204:207] cbsz:2 blgp:2
	v_mfma_f32_16x16x128_f8f6f4 v[138:141], v[128:133], v[20:25], v[138:141] cbsz:2 blgp:2
	v_mfma_f32_16x16x128_f8f6f4 v[208:211], v[128:133], v[56:61], v[208:211] cbsz:2 blgp:2
	v_mfma_f32_16x16x128_f8f6f4 v[142:145], v[128:133], v[32:37], v[142:145] cbsz:2 blgp:2
	v_mfma_f32_16x16x128_f8f6f4 v[212:215], v[128:133], v[68:73], v[212:215] cbsz:2 blgp:2
	v_cndmask_b32_e64 v158, v134, v204, s[0:1]
	v_fma_mix_f32 v158, v158, v100, v146 op_sel_hi:[0,0,1]
	v_exp_f32_e32 v158, v158
	v_cndmask_b32_e64 v159, v138, v208, s[0:1]
	v_fma_mix_f32 v159, v159, v101, v150 op_sel_hi:[0,0,1]
	v_exp_f32_e32 v159, v159
	v_fma_f32 v158, v158, v186, v186
	v_rcp_f32_e32 v158, v158
	v_add_f32_e32 v159, 1.0, v159
	v_rcp_f32_e32 v159, v159
	v_cndmask_b32_e64 v160, v142, v212, s[0:1]
	v_fma_mix_f32 v161, v158, v160, v154 op_sel_hi:[0,0,1]
	v_exp_f32_e32 v161, v161
	s_add_u32 s48, s48, s40
	v_add_f32_e32 v161, 1.0, v161
	v_rcp_f32_e32 v161, v161
	s_addc_u32 s49, s49, s41
	v_fma_f32 v162, v161, -2.0, 1.0
	v_sub_f32_e32 v163, v176, v162
	v_fma_f32 v176, v159, v163, v162
	v_fma_f32 v164, |v176|, s17, v113
	v_fma_f32 v165, |v176|, s18, v114
	v_fma_f32 v166, |v176|, s19, v115
	v_lshrrev_b32_e32 v167, 26, v176
	v_min3_u32 v164, v164, v165, v166
	v_bfi_b32 v168, 31, v164, v167
	v_lshrrev_b32_e32 v169, v181, v168
	global_store_short_d16_hi v185, v176, s[48:49]
	v_mul_u32_u24_dpp v170, v168, v180 quad_perm:[1,2,3,3] row_mask:0xf bank_mask:0xf bound_ctrl:1
	v_or_b32_e32 v171, v169, v170
	ds_write_b8 v184, v171 offset:416
	s_barrier
	ds_read_b64 v[122:123], v105 offset:416
	ds_read_b64 v[124:125], v105 offset:424
	ds_read_b64 v[126:127], v105 offset:432
	s_waitcnt lgkmcnt(3)
	s_barrier
	ds_read_b64 v[128:129], v105 offset:512
	ds_read_b64 v[130:131], v105 offset:520
	ds_read_b64 v[132:133], v105 offset:528
	s_waitcnt lgkmcnt(3)
	v_mfma_f32_16x16x128_f8f6f4 v[134:137], v[122:127], v[2:7], 0 cbsz:2 blgp:2
	v_mfma_f32_16x16x128_f8f6f4 v[138:141], v[122:127], v[14:19], 0 cbsz:2 blgp:2
	v_mfma_f32_16x16x128_f8f6f4 v[142:145], v[122:127], v[26:31], v[188:191] cbsz:2 blgp:2
	v_mfma_f32_16x16x128_f8f6f4 v[204:207], v[122:127], v[38:43], 0 cbsz:2 blgp:2
	v_mfma_f32_16x16x128_f8f6f4 v[208:211], v[122:127], v[50:55], 0 cbsz:2 blgp:2
	v_mfma_f32_16x16x128_f8f6f4 v[212:215], v[122:127], v[62:67], v[188:191] cbsz:2 blgp:2
	s_waitcnt lgkmcnt(0)
	v_mfma_f32_16x16x128_f8f6f4 v[134:137], v[128:133], v[8:13], v[134:137] cbsz:2 blgp:2
	v_mfma_f32_16x16x128_f8f6f4 v[204:207], v[128:133], v[44:49], v[204:207] cbsz:2 blgp:2
	v_mfma_f32_16x16x128_f8f6f4 v[138:141], v[128:133], v[20:25], v[138:141] cbsz:2 blgp:2
	v_mfma_f32_16x16x128_f8f6f4 v[208:211], v[128:133], v[56:61], v[208:211] cbsz:2 blgp:2
	v_mfma_f32_16x16x128_f8f6f4 v[142:145], v[128:133], v[32:37], v[142:145] cbsz:2 blgp:2
	v_mfma_f32_16x16x128_f8f6f4 v[212:215], v[128:133], v[68:73], v[212:215] cbsz:2 blgp:2
	v_cndmask_b32_e64 v158, v134, v204, s[0:1]
	v_fma_mix_f32 v158, v158, v100, v146 op_sel:[0,0,1] op_sel_hi:[0,0,1]
	v_exp_f32_e32 v158, v158
	v_cndmask_b32_e64 v159, v138, v208, s[0:1]
	v_fma_mix_f32 v159, v159, v101, v150 op_sel:[0,0,1] op_sel_hi:[0,0,1]
	v_exp_f32_e32 v159, v159
	v_fma_f32 v158, v158, v186, v186
	v_rcp_f32_e32 v158, v158
	v_add_f32_e32 v159, 1.0, v159
	v_rcp_f32_e32 v159, v159
	v_cndmask_b32_e64 v160, v142, v212, s[0:1]
	v_fma_mix_f32 v161, v158, v160, v154 op_sel:[0,0,1] op_sel_hi:[0,0,1]
	v_exp_f32_e32 v161, v161
	s_add_u32 s48, s48, s40
	v_add_f32_e32 v161, 1.0, v161
	v_rcp_f32_e32 v161, v161
	s_addc_u32 s49, s49, s41
	v_fma_f32 v162, v161, -2.0, 1.0
	v_sub_f32_e32 v163, v176, v162
	v_fma_f32 v176, v159, v163, v162
	v_fma_f32 v164, |v176|, s17, v113
	v_fma_f32 v165, |v176|, s18, v114
	v_fma_f32 v166, |v176|, s19, v115
	v_lshrrev_b32_e32 v167, 26, v176
	v_min3_u32 v164, v164, v165, v166
	v_bfi_b32 v168, 31, v164, v167
	v_lshrrev_b32_e32 v169, v181, v168
	global_store_short_d16_hi v185, v176, s[48:49]
	v_mul_u32_u24_dpp v170, v168, v180 quad_perm:[1,2,3,3] row_mask:0xf bank_mask:0xf bound_ctrl:1
	v_or_b32_e32 v171, v169, v170
	ds_write_b8 v184, v171
	s_barrier
	ds_read_b64 v[122:123], v105 offset:0
	ds_read_b64 v[124:125], v105 offset:8
	ds_read_b64 v[126:127], v105 offset:16
	s_waitcnt lgkmcnt(3)
	s_barrier
	ds_read_b64 v[128:129], v105 offset:96
	ds_read_b64 v[130:131], v105 offset:104
	ds_read_b64 v[132:133], v105 offset:112
	s_waitcnt lgkmcnt(3)
	v_mfma_f32_16x16x128_f8f6f4 v[134:137], v[122:127], v[2:7], 0 cbsz:2 blgp:2
	v_mfma_f32_16x16x128_f8f6f4 v[138:141], v[122:127], v[14:19], 0 cbsz:2 blgp:2
	v_mfma_f32_16x16x128_f8f6f4 v[142:145], v[122:127], v[26:31], v[188:191] cbsz:2 blgp:2
	v_mfma_f32_16x16x128_f8f6f4 v[204:207], v[122:127], v[38:43], 0 cbsz:2 blgp:2
	v_mfma_f32_16x16x128_f8f6f4 v[208:211], v[122:127], v[50:55], 0 cbsz:2 blgp:2
	v_mfma_f32_16x16x128_f8f6f4 v[212:215], v[122:127], v[62:67], v[188:191] cbsz:2 blgp:2
	s_waitcnt lgkmcnt(0)
	v_mfma_f32_16x16x128_f8f6f4 v[134:137], v[128:133], v[8:13], v[134:137] cbsz:2 blgp:2
	v_mfma_f32_16x16x128_f8f6f4 v[204:207], v[128:133], v[44:49], v[204:207] cbsz:2 blgp:2
	v_mfma_f32_16x16x128_f8f6f4 v[138:141], v[128:133], v[20:25], v[138:141] cbsz:2 blgp:2
	v_mfma_f32_16x16x128_f8f6f4 v[208:211], v[128:133], v[56:61], v[208:211] cbsz:2 blgp:2
	v_mfma_f32_16x16x128_f8f6f4 v[142:145], v[128:133], v[32:37], v[142:145] cbsz:2 blgp:2
	v_mfma_f32_16x16x128_f8f6f4 v[212:215], v[128:133], v[68:73], v[212:215] cbsz:2 blgp:2
	v_cndmask_b32_e64 v158, v134, v204, s[0:1]
	v_fma_mix_f32 v158, v158, v100, v147 op_sel_hi:[0,0,1]
	v_exp_f32_e32 v158, v158
	v_cndmask_b32_e64 v159, v138, v208, s[0:1]
	v_fma_mix_f32 v159, v159, v101, v151 op_sel_hi:[0,0,1]
	v_exp_f32_e32 v159, v159
	v_fma_f32 v158, v158, v186, v186
	v_rcp_f32_e32 v158, v158
	v_add_f32_e32 v159, 1.0, v159
	v_rcp_f32_e32 v159, v159
	v_cndmask_b32_e64 v160, v142, v212, s[0:1]
	v_fma_mix_f32 v161, v158, v160, v155 op_sel_hi:[0,0,1]
	v_exp_f32_e32 v161, v161
	s_add_u32 s48, s48, s40
	v_add_f32_e32 v161, 1.0, v161
	v_rcp_f32_e32 v161, v161
	s_addc_u32 s49, s49, s41
	v_fma_f32 v162, v161, -2.0, 1.0
	v_sub_f32_e32 v163, v176, v162
	v_fma_f32 v176, v159, v163, v162
	v_fma_f32 v164, |v176|, s17, v113
	v_fma_f32 v165, |v176|, s18, v114
	v_fma_f32 v166, |v176|, s19, v115
	v_lshrrev_b32_e32 v167, 26, v176
	v_min3_u32 v164, v164, v165, v166
	v_bfi_b32 v168, 31, v164, v167
	v_lshrrev_b32_e32 v169, v181, v168
	global_store_short_d16_hi v185, v176, s[48:49]
	v_mul_u32_u24_dpp v170, v168, v180 quad_perm:[1,2,3,3] row_mask:0xf bank_mask:0xf bound_ctrl:1
	v_or_b32_e32 v171, v169, v170
	ds_write_b8 v184, v171 offset:416
	s_barrier
	ds_read_b64 v[122:123], v105 offset:416
	ds_read_b64 v[124:125], v105 offset:424
	ds_read_b64 v[126:127], v105 offset:432
	s_waitcnt lgkmcnt(3)
	s_barrier
	ds_read_b64 v[128:129], v105 offset:512
	ds_read_b64 v[130:131], v105 offset:520
	ds_read_b64 v[132:133], v105 offset:528
	s_waitcnt lgkmcnt(3)
	v_mfma_f32_16x16x128_f8f6f4 v[134:137], v[122:127], v[2:7], 0 cbsz:2 blgp:2
	v_mfma_f32_16x16x128_f8f6f4 v[138:141], v[122:127], v[14:19], 0 cbsz:2 blgp:2
	v_mfma_f32_16x16x128_f8f6f4 v[142:145], v[122:127], v[26:31], v[188:191] cbsz:2 blgp:2
	v_mfma_f32_16x16x128_f8f6f4 v[204:207], v[122:127], v[38:43], 0 cbsz:2 blgp:2
	v_mfma_f32_16x16x128_f8f6f4 v[208:211], v[122:127], v[50:55], 0 cbsz:2 blgp:2
	v_mfma_f32_16x16x128_f8f6f4 v[212:215], v[122:127], v[62:67], v[188:191] cbsz:2 blgp:2
	s_waitcnt lgkmcnt(0)
	v_mfma_f32_16x16x128_f8f6f4 v[134:137], v[128:133], v[8:13], v[134:137] cbsz:2 blgp:2
	v_mfma_f32_16x16x128_f8f6f4 v[204:207], v[128:133], v[44:49], v[204:207] cbsz:2 blgp:2
	v_mfma_f32_16x16x128_f8f6f4 v[138:141], v[128:133], v[20:25], v[138:141] cbsz:2 blgp:2
	v_mfma_f32_16x16x128_f8f6f4 v[208:211], v[128:133], v[56:61], v[208:211] cbsz:2 blgp:2
	v_mfma_f32_16x16x128_f8f6f4 v[142:145], v[128:133], v[32:37], v[142:145] cbsz:2 blgp:2
	v_mfma_f32_16x16x128_f8f6f4 v[212:215], v[128:133], v[68:73], v[212:215] cbsz:2 blgp:2
	v_cndmask_b32_e64 v158, v134, v204, s[0:1]
	v_fma_mix_f32 v158, v158, v100, v147 op_sel:[0,0,1] op_sel_hi:[0,0,1]
	v_exp_f32_e32 v158, v158
	v_cndmask_b32_e64 v159, v138, v208, s[0:1]
	v_fma_mix_f32 v159, v159, v101, v151 op_sel:[0,0,1] op_sel_hi:[0,0,1]
	v_exp_f32_e32 v159, v159
	v_fma_f32 v158, v158, v186, v186
	v_rcp_f32_e32 v158, v158
	v_add_f32_e32 v159, 1.0, v159
	v_rcp_f32_e32 v159, v159
	v_cndmask_b32_e64 v160, v142, v212, s[0:1]
	v_fma_mix_f32 v161, v158, v160, v155 op_sel:[0,0,1] op_sel_hi:[0,0,1]
	v_exp_f32_e32 v161, v161
	s_add_u32 s48, s48, s40
	v_add_f32_e32 v161, 1.0, v161
	v_rcp_f32_e32 v161, v161
	s_addc_u32 s49, s49, s41
	v_fma_f32 v162, v161, -2.0, 1.0
	v_sub_f32_e32 v163, v176, v162
	v_fma_f32 v176, v159, v163, v162
	v_fma_f32 v164, |v176|, s17, v113
	v_fma_f32 v165, |v176|, s18, v114
	v_fma_f32 v166, |v176|, s19, v115
	v_lshrrev_b32_e32 v167, 26, v176
	v_min3_u32 v164, v164, v165, v166
	v_bfi_b32 v168, 31, v164, v167
	v_lshrrev_b32_e32 v169, v181, v168
	global_store_short_d16_hi v185, v176, s[48:49]
	v_mul_u32_u24_dpp v170, v168, v180 quad_perm:[1,2,3,3] row_mask:0xf bank_mask:0xf bound_ctrl:1
	v_or_b32_e32 v171, v169, v170
	ds_write_b8 v184, v171
	s_barrier
	ds_read_b64 v[122:123], v105 offset:0
	ds_read_b64 v[124:125], v105 offset:8
	ds_read_b64 v[126:127], v105 offset:16
	s_waitcnt lgkmcnt(3)
	s_barrier
	ds_read_b64 v[128:129], v105 offset:96
	ds_read_b64 v[130:131], v105 offset:104
	ds_read_b64 v[132:133], v105 offset:112
	s_waitcnt lgkmcnt(3)
	v_mfma_f32_16x16x128_f8f6f4 v[134:137], v[122:127], v[2:7], 0 cbsz:2 blgp:2
	v_mfma_f32_16x16x128_f8f6f4 v[138:141], v[122:127], v[14:19], 0 cbsz:2 blgp:2
	v_mfma_f32_16x16x128_f8f6f4 v[142:145], v[122:127], v[26:31], v[188:191] cbsz:2 blgp:2
	v_mfma_f32_16x16x128_f8f6f4 v[204:207], v[122:127], v[38:43], 0 cbsz:2 blgp:2
	v_mfma_f32_16x16x128_f8f6f4 v[208:211], v[122:127], v[50:55], 0 cbsz:2 blgp:2
	v_mfma_f32_16x16x128_f8f6f4 v[212:215], v[122:127], v[62:67], v[188:191] cbsz:2 blgp:2
	s_waitcnt lgkmcnt(0)
	v_mfma_f32_16x16x128_f8f6f4 v[134:137], v[128:133], v[8:13], v[134:137] cbsz:2 blgp:2
	v_mfma_f32_16x16x128_f8f6f4 v[204:207], v[128:133], v[44:49], v[204:207] cbsz:2 blgp:2
	v_mfma_f32_16x16x128_f8f6f4 v[138:141], v[128:133], v[20:25], v[138:141] cbsz:2 blgp:2
	v_mfma_f32_16x16x128_f8f6f4 v[208:211], v[128:133], v[56:61], v[208:211] cbsz:2 blgp:2
	v_mfma_f32_16x16x128_f8f6f4 v[142:145], v[128:133], v[32:37], v[142:145] cbsz:2 blgp:2
	v_mfma_f32_16x16x128_f8f6f4 v[212:215], v[128:133], v[68:73], v[212:215] cbsz:2 blgp:2
	v_cndmask_b32_e64 v158, v134, v204, s[0:1]
	v_fma_mix_f32 v158, v158, v100, v148 op_sel_hi:[0,0,1]
	v_exp_f32_e32 v158, v158
	v_cndmask_b32_e64 v159, v138, v208, s[0:1]
	v_fma_mix_f32 v159, v159, v101, v152 op_sel_hi:[0,0,1]
	v_exp_f32_e32 v159, v159
	v_fma_f32 v158, v158, v186, v186
	v_rcp_f32_e32 v158, v158
	v_add_f32_e32 v159, 1.0, v159
	v_rcp_f32_e32 v159, v159
	v_cndmask_b32_e64 v160, v142, v212, s[0:1]
	v_fma_mix_f32 v161, v158, v160, v156 op_sel_hi:[0,0,1]
	v_exp_f32_e32 v161, v161
	s_add_u32 s48, s48, s40
	v_add_f32_e32 v161, 1.0, v161
	v_rcp_f32_e32 v161, v161
	s_addc_u32 s49, s49, s41
	v_fma_f32 v162, v161, -2.0, 1.0
	v_sub_f32_e32 v163, v176, v162
	v_fma_f32 v176, v159, v163, v162
	v_fma_f32 v164, |v176|, s17, v113
	v_fma_f32 v165, |v176|, s18, v114
	v_fma_f32 v166, |v176|, s19, v115
	v_lshrrev_b32_e32 v167, 26, v176
	v_min3_u32 v164, v164, v165, v166
	v_bfi_b32 v168, 31, v164, v167
	v_lshrrev_b32_e32 v169, v181, v168
	global_store_short_d16_hi v185, v176, s[48:49]
	v_mul_u32_u24_dpp v170, v168, v180 quad_perm:[1,2,3,3] row_mask:0xf bank_mask:0xf bound_ctrl:1
	v_or_b32_e32 v171, v169, v170
	ds_write_b8 v184, v171 offset:416
	s_barrier
	ds_read_b64 v[122:123], v105 offset:416
	ds_read_b64 v[124:125], v105 offset:424
	ds_read_b64 v[126:127], v105 offset:432
	s_waitcnt lgkmcnt(3)
	s_barrier
	ds_read_b64 v[128:129], v105 offset:512
	ds_read_b64 v[130:131], v105 offset:520
	ds_read_b64 v[132:133], v105 offset:528
	s_waitcnt lgkmcnt(3)
	v_mfma_f32_16x16x128_f8f6f4 v[134:137], v[122:127], v[2:7], 0 cbsz:2 blgp:2
	v_mfma_f32_16x16x128_f8f6f4 v[138:141], v[122:127], v[14:19], 0 cbsz:2 blgp:2
	v_mfma_f32_16x16x128_f8f6f4 v[142:145], v[122:127], v[26:31], v[188:191] cbsz:2 blgp:2
	v_mfma_f32_16x16x128_f8f6f4 v[204:207], v[122:127], v[38:43], 0 cbsz:2 blgp:2
	v_mfma_f32_16x16x128_f8f6f4 v[208:211], v[122:127], v[50:55], 0 cbsz:2 blgp:2
	v_mfma_f32_16x16x128_f8f6f4 v[212:215], v[122:127], v[62:67], v[188:191] cbsz:2 blgp:2
	s_waitcnt lgkmcnt(0)
	v_mfma_f32_16x16x128_f8f6f4 v[134:137], v[128:133], v[8:13], v[134:137] cbsz:2 blgp:2
	v_mfma_f32_16x16x128_f8f6f4 v[204:207], v[128:133], v[44:49], v[204:207] cbsz:2 blgp:2
	v_mfma_f32_16x16x128_f8f6f4 v[138:141], v[128:133], v[20:25], v[138:141] cbsz:2 blgp:2
	v_mfma_f32_16x16x128_f8f6f4 v[208:211], v[128:133], v[56:61], v[208:211] cbsz:2 blgp:2
	v_mfma_f32_16x16x128_f8f6f4 v[142:145], v[128:133], v[32:37], v[142:145] cbsz:2 blgp:2
	v_mfma_f32_16x16x128_f8f6f4 v[212:215], v[128:133], v[68:73], v[212:215] cbsz:2 blgp:2
	v_cndmask_b32_e64 v158, v134, v204, s[0:1]
	v_fma_mix_f32 v158, v158, v100, v148 op_sel:[0,0,1] op_sel_hi:[0,0,1]
	v_exp_f32_e32 v158, v158
	v_cndmask_b32_e64 v159, v138, v208, s[0:1]
	v_fma_mix_f32 v159, v159, v101, v152 op_sel:[0,0,1] op_sel_hi:[0,0,1]
	v_exp_f32_e32 v159, v159
	v_fma_f32 v158, v158, v186, v186
	v_rcp_f32_e32 v158, v158
	v_add_f32_e32 v159, 1.0, v159
	v_rcp_f32_e32 v159, v159
	v_cndmask_b32_e64 v160, v142, v212, s[0:1]
	v_fma_mix_f32 v161, v158, v160, v156 op_sel:[0,0,1] op_sel_hi:[0,0,1]
	v_exp_f32_e32 v161, v161
	s_add_u32 s48, s48, s40
	v_add_f32_e32 v161, 1.0, v161
	v_rcp_f32_e32 v161, v161
	s_addc_u32 s49, s49, s41
	v_fma_f32 v162, v161, -2.0, 1.0
	v_sub_f32_e32 v163, v176, v162
	v_fma_f32 v176, v159, v163, v162
	v_fma_f32 v164, |v176|, s17, v113
	v_fma_f32 v165, |v176|, s18, v114
	v_fma_f32 v166, |v176|, s19, v115
	v_lshrrev_b32_e32 v167, 26, v176
	v_min3_u32 v164, v164, v165, v166
	v_bfi_b32 v168, 31, v164, v167
	v_lshrrev_b32_e32 v169, v181, v168
	global_store_short_d16_hi v185, v176, s[48:49]
	v_mul_u32_u24_dpp v170, v168, v180 quad_perm:[1,2,3,3] row_mask:0xf bank_mask:0xf bound_ctrl:1
	v_or_b32_e32 v171, v169, v170
	ds_write_b8 v184, v171
	s_barrier
	ds_read_b64 v[122:123], v105 offset:0
	ds_read_b64 v[124:125], v105 offset:8
	ds_read_b64 v[126:127], v105 offset:16
	s_waitcnt lgkmcnt(3)
	s_barrier
	ds_read_b64 v[128:129], v105 offset:96
	ds_read_b64 v[130:131], v105 offset:104
	ds_read_b64 v[132:133], v105 offset:112
	s_waitcnt lgkmcnt(3)
	v_mfma_f32_16x16x128_f8f6f4 v[134:137], v[122:127], v[2:7], 0 cbsz:2 blgp:2
	v_mfma_f32_16x16x128_f8f6f4 v[138:141], v[122:127], v[14:19], 0 cbsz:2 blgp:2
	v_mfma_f32_16x16x128_f8f6f4 v[142:145], v[122:127], v[26:31], v[188:191] cbsz:2 blgp:2
	v_mfma_f32_16x16x128_f8f6f4 v[204:207], v[122:127], v[38:43], 0 cbsz:2 blgp:2
	v_mfma_f32_16x16x128_f8f6f4 v[208:211], v[122:127], v[50:55], 0 cbsz:2 blgp:2
	v_mfma_f32_16x16x128_f8f6f4 v[212:215], v[122:127], v[62:67], v[188:191] cbsz:2 blgp:2
	s_waitcnt lgkmcnt(0)
	v_mfma_f32_16x16x128_f8f6f4 v[134:137], v[128:133], v[8:13], v[134:137] cbsz:2 blgp:2
	v_mfma_f32_16x16x128_f8f6f4 v[204:207], v[128:133], v[44:49], v[204:207] cbsz:2 blgp:2
	v_mfma_f32_16x16x128_f8f6f4 v[138:141], v[128:133], v[20:25], v[138:141] cbsz:2 blgp:2
	v_mfma_f32_16x16x128_f8f6f4 v[208:211], v[128:133], v[56:61], v[208:211] cbsz:2 blgp:2
	v_mfma_f32_16x16x128_f8f6f4 v[142:145], v[128:133], v[32:37], v[142:145] cbsz:2 blgp:2
	v_mfma_f32_16x16x128_f8f6f4 v[212:215], v[128:133], v[68:73], v[212:215] cbsz:2 blgp:2
	v_cndmask_b32_e64 v158, v134, v204, s[0:1]
	v_fma_mix_f32 v158, v158, v100, v149 op_sel_hi:[0,0,1]
	v_exp_f32_e32 v158, v158
	v_cndmask_b32_e64 v159, v138, v208, s[0:1]
	v_fma_mix_f32 v159, v159, v101, v153 op_sel_hi:[0,0,1]
	v_exp_f32_e32 v159, v159
	v_fma_f32 v158, v158, v186, v186
	v_rcp_f32_e32 v158, v158
	v_add_f32_e32 v159, 1.0, v159
	v_rcp_f32_e32 v159, v159
	v_cndmask_b32_e64 v160, v142, v212, s[0:1]
	v_fma_mix_f32 v161, v158, v160, v157 op_sel_hi:[0,0,1]
	v_exp_f32_e32 v161, v161
	s_add_u32 s48, s48, s40
	v_add_f32_e32 v161, 1.0, v161
	v_rcp_f32_e32 v161, v161
	s_addc_u32 s49, s49, s41
	v_fma_f32 v162, v161, -2.0, 1.0
	v_sub_f32_e32 v163, v176, v162
	v_fma_f32 v176, v159, v163, v162
	v_fma_f32 v164, |v176|, s17, v113
	v_fma_f32 v165, |v176|, s18, v114
	v_fma_f32 v166, |v176|, s19, v115
	v_lshrrev_b32_e32 v167, 26, v176
	v_min3_u32 v164, v164, v165, v166
	v_bfi_b32 v168, 31, v164, v167
	v_lshrrev_b32_e32 v169, v181, v168
	global_store_short_d16_hi v185, v176, s[48:49]
	v_mul_u32_u24_dpp v170, v168, v180 quad_perm:[1,2,3,3] row_mask:0xf bank_mask:0xf bound_ctrl:1
	v_or_b32_e32 v171, v169, v170
	ds_write_b8 v184, v171 offset:416
	s_barrier
	ds_read_b64 v[122:123], v105 offset:416
	ds_read_b64 v[124:125], v105 offset:424
	ds_read_b64 v[126:127], v105 offset:432
	s_waitcnt lgkmcnt(3)
	s_barrier
	ds_read_b64 v[128:129], v105 offset:512
	ds_read_b64 v[130:131], v105 offset:520
	ds_read_b64 v[132:133], v105 offset:528
	s_add_i32 s44, s44, 16
	s_waitcnt lgkmcnt(3)
	v_mfma_f32_16x16x128_f8f6f4 v[134:137], v[122:127], v[2:7], 0 cbsz:2 blgp:2
	v_mfma_f32_16x16x128_f8f6f4 v[138:141], v[122:127], v[14:19], 0 cbsz:2 blgp:2
	v_mfma_f32_16x16x128_f8f6f4 v[142:145], v[122:127], v[26:31], v[188:191] cbsz:2 blgp:2
	v_mfma_f32_16x16x128_f8f6f4 v[204:207], v[122:127], v[38:43], 0 cbsz:2 blgp:2
	v_mfma_f32_16x16x128_f8f6f4 v[208:211], v[122:127], v[50:55], 0 cbsz:2 blgp:2
	v_mfma_f32_16x16x128_f8f6f4 v[212:215], v[122:127], v[62:67], v[188:191] cbsz:2 blgp:2
	s_waitcnt lgkmcnt(0)
	v_mfma_f32_16x16x128_f8f6f4 v[134:137], v[128:133], v[8:13], v[134:137] cbsz:2 blgp:2
	v_mfma_f32_16x16x128_f8f6f4 v[204:207], v[128:133], v[44:49], v[204:207] cbsz:2 blgp:2
	v_mfma_f32_16x16x128_f8f6f4 v[138:141], v[128:133], v[20:25], v[138:141] cbsz:2 blgp:2
	v_mfma_f32_16x16x128_f8f6f4 v[208:211], v[128:133], v[56:61], v[208:211] cbsz:2 blgp:2
	v_mfma_f32_16x16x128_f8f6f4 v[142:145], v[128:133], v[32:37], v[142:145] cbsz:2 blgp:2
	v_mfma_f32_16x16x128_f8f6f4 v[212:215], v[128:133], v[68:73], v[212:215] cbsz:2 blgp:2
	v_cndmask_b32_e64 v158, v134, v204, s[0:1]
	v_fma_mix_f32 v158, v158, v100, v149 op_sel:[0,0,1] op_sel_hi:[0,0,1]
	v_exp_f32_e32 v158, v158
	v_cndmask_b32_e64 v159, v138, v208, s[0:1]
	v_fma_mix_f32 v159, v159, v101, v153 op_sel:[0,0,1] op_sel_hi:[0,0,1]
	v_exp_f32_e32 v159, v159
	v_fma_f32 v158, v158, v186, v186
	v_rcp_f32_e32 v158, v158
	v_add_f32_e32 v159, 1.0, v159
	v_rcp_f32_e32 v159, v159
	v_cndmask_b32_e64 v160, v142, v212, s[0:1]
	v_fma_mix_f32 v161, v158, v160, v157 op_sel:[0,0,1] op_sel_hi:[0,0,1]
	v_exp_f32_e32 v161, v161
	s_add_u32 s48, s48, s40
	v_add_f32_e32 v161, 1.0, v161
	v_rcp_f32_e32 v161, v161
	s_addc_u32 s49, s49, s41
	v_fma_f32 v162, v161, -2.0, 1.0
	v_sub_f32_e32 v163, v176, v162
	v_fma_f32 v176, v159, v163, v162
	v_fma_f32 v164, |v176|, s17, v113
	v_fma_f32 v165, |v176|, s18, v114
	v_fma_f32 v166, |v176|, s19, v115
	v_lshrrev_b32_e32 v167, 26, v176
	v_min3_u32 v164, v164, v165, v166
	v_bfi_b32 v168, 31, v164, v167
	v_lshrrev_b32_e32 v169, v181, v168
	global_store_short_d16_hi v185, v176, s[48:49]
	v_mul_u32_u24_dpp v170, v168, v180 quad_perm:[1,2,3,3] row_mask:0xf bank_mask:0xf bound_ctrl:1
	v_or_b32_e32 v171, v169, v170
	ds_write_b8 v184, v171
	s_barrier
	ds_read_b64 v[122:123], v105 offset:0
	ds_read_b64 v[124:125], v105 offset:8
	ds_read_b64 v[126:127], v105 offset:16
	s_cmp_lt_i32 s44, s45
	s_waitcnt lgkmcnt(3)
	s_barrier
	s_cbranch_scc1 .Lscan_loop_b_f2
